# full-128B-line LDS-DMA pieces (8 rows x 128B) for all six GEMM K-loops, new XOR swizzle; plus m0 cleanup
# speedup vs baseline: 1.0112x; 1.0112x over previous
.LBB0_230:
	s_mul_i32 s3, s44, 11
	s_add_i32 s2, s3, 1
	s_cmp_gt_i32 s89, s2
	s_waitcnt lgkmcnt(0)
	s_cselect_b64 s[4:5], -1, 0
	v_writelane_b32 v254, s3, 36
	s_add_i32 s3, s3, 12
	s_cmp_lt_i32 s88, s3
	s_cselect_b64 s[6:7], -1, 0
	s_and_b64 s[4:5], s[4:5], s[6:7]
	s_andn2_b64 vcc, exec, s[4:5]
	s_cbranch_vccnz .LBB0_229
	v_writelane_b32 v254, s3, 37
	s_cmp_le_i32 s88, s2
	s_mov_b64 s[2:3], -1
	v_writelane_b32 v254, s44, 38
	s_cbranch_scc0 .LBB0_334
	v_readlane_b32 s6, v252, 0
	v_readlane_b32 s7, v252, 1
	s_waitcnt vmcnt(0) expcnt(0) lgkmcnt(0)
	s_load_dwordx2 s[4:5], s[6:7], 0x98
	v_mbcnt_lo_u32_b32 v0, -1, 0
	v_mbcnt_hi_u32_b32 v0, -1, v0
	v_readlane_b32 s2, v252, 8
	v_add_u32_e32 v156, s93, v0
	v_readlane_b32 s3, v252, 9
	v_mov_b32_e32 v0, v156
	s_andn2_b64 vcc, exec, s[2:3]
	v_readfirstlane_b32 s16, v0
	s_cbranch_vccnz .LBB0_256
	v_bfe_i32 v3, v0, 27, 1
	v_lshlrev_b32_e32 v1, 4, v0
	v_lshrrev_b32_e32 v3, 22, v3
	v_add_u32_e32 v3, v1, v3
	v_and_b32_e32 v3, 0xfffffc00, v3
	v_sub_u32_e32 v3, v1, v3
	v_ashrrev_i32_e32 v2, 31, v0
	v_lshrrev_b32_e32 v4, 4, v3
	v_lshrrev_b32_e32 v2, 26, v2
	v_bitop3_b32 v3, v4, v3, 32 bitop3:0x6c
	v_add_u32_e32 v2, v0, v2
	v_ashrrev_i32_e32 v5, 31, v3
	s_mul_i32 s3, s44, 0x500000
	v_ashrrev_i32_e32 v2, 6, v2
	v_lshrrev_b32_e32 v5, 26, v5
	s_mul_hi_u32 s2, s44, 0x500000
	s_waitcnt lgkmcnt(0)
	s_add_u32 s3, s4, s3
	v_lshlrev_b32_e32 v4, 3, v2
	v_add_u32_e32 v5, v3, v5
	s_addc_u32 s2, s5, s2
	v_and_b32_e32 v4, -16, v4
	v_ashrrev_i32_e32 v6, 6, v5
	v_and_b32_e32 v5, 0xc0, v5
	s_add_u32 s38, s3, 0x100000
	v_add_u32_e32 v4, v6, v4
	v_sub_u32_e32 v3, v3, v5
	s_addc_u32 s39, s2, 0
	s_load_dwordx2 s[2:3], s[6:7], 0x10
	s_load_dwordx2 s[12:13], s[6:7], 0x20
	v_lshlrev_b32_e32 v2, 5, v2
	v_ashrrev_i16_sdwa v3, v239, sext(v3) dst_sel:DWORD dst_unused:UNUSED_PAD src0_sel:DWORD src1_sel:BYTE_0
	v_lshlrev_b32_e32 v5, 1, v4
	v_lshrrev_b32_e32 v7, 2, v4
	v_and_b32_e32 v6, 3, v6
	s_mov_b32 s6, 0x1fffe0
	v_and_b32_e32 v2, 32, v2
	v_bfe_i32 v3, v3, 0, 16
	v_and_b32_e32 v5, 24, v5
	v_and_b32_e32 v7, 4, v7
	v_and_or_b32 v6, v4, s6, v6
	v_or3_b32 v5, v6, v7, v5
	v_add_lshl_u32 v2, v2, v3, 1
	v_add_u32_e32 v1, 0x2000, v1
	v_lshl_add_u32 v157, v4, 11, v2
	v_mbcnt_lo_u32_b32 v134, -1, 0
	v_mbcnt_hi_u32_b32 v134, -1, v134
	v_add_u32_e32 v134, s93, v134
	v_lshrrev_b32_e32 v135, 3, v134
	v_lshrrev_b32_e32 v136, 4, v134
	v_xor_b32_e32 v136, v136, v134
	v_lshlrev_b32_e32 v136, 4, v136
	v_and_b32_e32 v136, 0x70, v136
	v_lshl_add_u32 v157, v135, 11, v136
	v_lshl_add_u32 v158, v5, 11, v2
	v_mbcnt_lo_u32_b32 v134, -1, 0
	v_mbcnt_hi_u32_b32 v134, -1, v134
	v_add_u32_e32 v134, s93, v134
	v_lshrrev_b32_e32 v135, 3, v134
	v_and_b32_e32 v136, 12, v135
	v_lshlrev_b32_e32 v136, 1, v136
	v_and_b32_e32 v158, 0xffffffe3, v135
	v_or_b32_e32 v136, v136, v158
	v_lshrrev_b32_e32 v135, 2, v135
	v_and_b32_e32 v135, 4, v135
	v_or_b32_e32 v135, v135, v136
	v_lshrrev_b32_e32 v136, 4, v134
	v_xor_b32_e32 v136, v136, v134
	v_lshlrev_b32_e32 v136, 4, v136
	v_and_b32_e32 v136, 0x70, v136
	v_lshl_add_u32 v158, v135, 11, v136
	v_ashrrev_i32_e32 v2, 31, v1
	v_lshrrev_b32_e32 v2, 22, v2
	v_add_u32_e32 v2, v1, v2
	v_ashrrev_i32_e32 v2, 10, v2
	v_mul_i32_i24_e32 v3, 0x400, v2
	v_sub_u32_e32 v1, v1, v3
	v_lshrrev_b32_e32 v3, 4, v1
	v_bitop3_b32 v1, v3, v1, 32 bitop3:0x6c
	v_ashrrev_i32_e32 v4, 31, v1
	v_lshrrev_b32_e32 v4, 26, v4
	v_lshlrev_b32_e32 v3, 3, v2
	v_add_u32_e32 v4, v1, v4
	s_add_u32 s40, s4, 0x33b00000
	v_and_b32_e32 v3, -16, v3
	v_ashrrev_i32_e32 v5, 6, v4
	s_addc_u32 s41, s5, 0
	s_ashr_i32 s17, s16, 6
	v_add_u32_e32 v3, v5, v3
	v_and_b32_e32 v4, 0xc0, v4
	v_and_b32_e32 v5, 3, v5
	v_sub_u32_e32 v1, v1, v4
	v_and_or_b32 v5, v3, s6, v5
	s_ashr_i32 s18, s16, 8
	s_lshl_b32 s6, s17, 10
	v_readlane_b32 s8, v253, 14
	v_lshlrev_b32_e32 v2, 5, v2
	v_ashrrev_i16_sdwa v1, v239, sext(v1) dst_sel:DWORD dst_unused:UNUSED_PAD src0_sel:DWORD src1_sel:BYTE_0
	v_lshlrev_b32_e32 v4, 1, v3
	v_lshrrev_b32_e32 v6, 2, v3
	v_readlane_b32 s9, v253, 15
	s_add_u32 s28, s38, s8
	v_and_b32_e32 v2, 32, v2
	v_bfe_i32 v1, v1, 0, 16
	v_and_b32_e32 v4, 24, v4
	v_and_b32_e32 v6, 4, v6
	s_addc_u32 s29, s39, s9
	s_add_i32 s42, s6, 0
	v_or3_b32 v4, v5, v6, v4
	v_add_lshl_u32 v1, v2, v1, 1
	s_add_i32 s43, s42, 0x10000
	s_mov_b32 m0, s43
	s_nop 0
	global_load_lds_dwordx4 v158, s[28:29]
	v_lshl_add_u32 v160, v4, 11, v1
	v_mbcnt_lo_u32_b32 v134, -1, 0
	v_mbcnt_hi_u32_b32 v134, -1, v134
	v_add_u32_e32 v134, s93, v134
	v_lshrrev_b32_e32 v135, 3, v134
	v_add_u32_e32 v135, 64, v135
	v_and_b32_e32 v136, 12, v135
	v_lshlrev_b32_e32 v136, 1, v136
	v_and_b32_e32 v160, 0xffffffe3, v135
	v_or_b32_e32 v136, v136, v160
	v_lshrrev_b32_e32 v135, 2, v135
	v_and_b32_e32 v135, 4, v135
	v_or_b32_e32 v135, v135, v136
	v_lshrrev_b32_e32 v136, 4, v134
	v_xor_b32_e32 v136, v136, v134
	v_lshlrev_b32_e32 v136, 4, v136
	v_and_b32_e32 v136, 0x70, v136
	v_lshl_add_u32 v160, v135, 11, v136
	s_add_i32 s44, s42, 0x12000
	s_mov_b32 m0, s44
	s_nop 0
	global_load_lds_dwordx4 v160, s[28:29]
	s_add_u32 s6, s28, 0x40000
	s_addc_u32 s7, s29, 0
	s_add_i32 s45, s42, 0x14000
	s_mov_b32 m0, s45
	s_nop 0
	global_load_lds_dwordx4 v158, s[6:7]
	s_add_i32 s46, s42, 0x16000
	s_mov_b32 m0, s46
	s_nop 0
	global_load_lds_dwordx4 v160, s[6:7]
	v_readlane_b32 s6, v253, 25
	v_readlane_b32 s7, v253, 26
	s_add_u32 s26, s40, s6
	s_addc_u32 s27, s41, s7
	s_mov_b32 m0, s42
	s_nop 0
	global_load_lds_dwordx4 v157, s[26:27]
	v_lshl_add_u32 v159, v3, 11, v1
	v_mbcnt_lo_u32_b32 v134, -1, 0
	v_mbcnt_hi_u32_b32 v134, -1, v134
	v_add_u32_e32 v134, s93, v134
	v_lshrrev_b32_e32 v135, 3, v134
	v_add_u32_e32 v135, 64, v135
	v_lshrrev_b32_e32 v136, 4, v134
	v_xor_b32_e32 v136, v136, v134
	v_lshlrev_b32_e32 v136, 4, v136
	v_and_b32_e32 v136, 0x70, v136
	v_lshl_add_u32 v159, v135, 11, v136
	s_add_i32 s47, s42, 0x2000
	s_mov_b32 m0, s47
	s_nop 0
	global_load_lds_dwordx4 v159, s[26:27]
	s_add_u32 s6, s26, 0x40000
	s_addc_u32 s7, s27, 0
	s_add_i32 s48, s42, 0x4000
	s_mov_b32 m0, s48
	s_nop 0
	global_load_lds_dwordx4 v157, s[6:7]
	s_add_i32 s49, s42, 0x6000
	s_mov_b32 m0, s49
	s_nop 0
	global_load_lds_dwordx4 v159, s[6:7]
	s_cmp_eq_u32 s18, 1
	s_cselect_b64 s[6:7], -1, 0
	s_cmp_lg_u32 s18, 1
	s_cbranch_scc1 .LBB0_235
	s_barrier
.LBB0_235:
	s_add_u32 s50, s4, 0x37b00000
	s_addc_u32 s51, s5, 0
	s_add_u32 s8, s4, 0x42300000
	s_addc_u32 s9, s5, 0
	s_add_u32 s10, s4, 0x42b00000
	v_readlane_b32 s19, v254, 38
	s_addc_u32 s11, s5, 0
	s_lshl_b32 s86, s19, 7
	s_lshl_b64 s[14:15], s[86:87], 2
	s_waitcnt lgkmcnt(0)
	s_add_u32 s12, s12, s14
	s_addc_u32 s13, s13, s15
	s_lshl_b32 s86, s19, 2
	s_lshl_b64 s[14:15], s[86:87], 2
	v_bfe_u32 v162, v0, 4, 2
	s_add_u32 s14, s2, s14
	v_and_b32_e32 v161, 15, v0
	v_lshlrev_b32_e32 v1, 4, v162
	v_lshlrev_b32_e32 v0, 2, v0
	s_addc_u32 s15, s3, s15
	s_and_b32 s52, s17, 3
	v_lshl_or_b32 v1, v161, 6, v1
	s_lshl_b32 s2, s18, 13
	v_and_b32_e32 v0, 32, v0
	s_lshl_b32 s53, s18, 6
	v_bitop3_b32 v2, v1, s2, v0 bitop3:0xde
	v_mbcnt_lo_u32_b32 v134, -1, 0
	v_mbcnt_hi_u32_b32 v134, -1, v134
	v_add_u32_e32 v134, s93, v134
	v_bfe_u32 v135, v134, 4, 2
	v_bfe_u32 v136, v134, 1, 3
	v_xor_b32_e32 v135, v135, v136
	v_lshlrev_b32_e32 v135, 4, v135
	v_and_b32_e32 v136, 15, v134
	v_lshl_or_b32 v135, v136, 7, v135
	v_lshrrev_b32_e32 v136, 8, v134
	v_lshl_or_b32 v2, v136, 13, v135
	s_lshl_b32 s54, s52, 5
	s_lshl_b32 s2, s52, 12
	v_bitop3_b32 v0, v1, s2, v0 bitop3:0xde
	v_mbcnt_lo_u32_b32 v134, -1, 0
	v_mbcnt_hi_u32_b32 v134, -1, v134
	v_add_u32_e32 v134, s93, v134
	v_bfe_u32 v135, v134, 4, 2
	v_bfe_u32 v136, v134, 1, 3
	v_xor_b32_e32 v135, v135, v136
	v_lshlrev_b32_e32 v135, 4, v135
	v_and_b32_e32 v136, 15, v134
	v_lshl_or_b32 v135, v136, 7, v135
	v_bfe_u32 v136, v134, 6, 2
	v_lshl_or_b32 v0, v136, 12, v135
	s_add_u32 s2, s28, 0x80
	s_waitcnt vmcnt(2)
	s_barrier
	s_addc_u32 s3, s29, 0
	s_add_i32 s55, s42, 0x18000
	s_mov_b32 m0, s55
	s_nop 0
	global_load_lds_dwordx4 v158, s[2:3]
	s_add_i32 s56, s42, 0x1a000
	s_mov_b32 m0, s56
	s_nop 0
	global_load_lds_dwordx4 v160, s[2:3]
	s_add_u32 s2, s26, 0x80
	s_addc_u32 s3, s27, 0
	s_add_i32 s57, s42, 0x8000
	s_mov_b32 m0, s57
	s_nop 0
	global_load_lds_dwordx4 v157, s[2:3]
	s_add_i32 s58, s42, 0xa000
	s_mov_b32 m0, s58
	s_nop 0
	global_load_lds_dwordx4 v159, s[2:3]
	s_add_u32 s2, s28, 0x40080
	s_addc_u32 s3, s29, 0
	s_add_i32 s59, s42, 0x1c000
	s_mov_b32 m0, s59
	s_nop 0
	global_load_lds_dwordx4 v158, s[2:3]
	s_add_i32 s60, s42, 0x1e000
	s_mov_b32 m0, s60
	s_nop 0
	global_load_lds_dwordx4 v160, s[2:3]
	s_waitcnt vmcnt(6)
	s_add_i32 s61, s42, 0xc000
	s_cmpk_lt_u32 s16, 0x100
	v_add_u32_e32 v0, 0, v0
	v_readlane_b32 s2, v253, 12
	s_mov_b32 s62, 0
	s_cselect_b64 s[16:17], -1, 0
	v_add_u32_e32 v163, 0x10000, v0
	v_add_u32_e32 v164, 0x14000, v0
	v_add_u32_e32 v165, 0, v2
	v_add_u32_e32 v166, 0x18000, v0
	v_add_u32_e32 v167, 0x1c000, v0
	s_mov_b32 s24, s2
	v_readlane_b32 s25, v253, 13
	s_barrier
	s_branch .LBB0_238

.LBB0_243:
	v_xor_b32_e32 v145, 64, v163
	ds_read_b128 v[130:133], v163
	ds_read_b128 v[134:137], v145
	ds_read_b128 v[138:141], v163 offset:2048
	ds_read_b128 v[142:145], v145 offset:2048
	v_xor_b32_e32 v175, 64, v164
	ds_read_b128 v[146:149], v164
	ds_read_b128 v[150:153], v175
	ds_read_b128 v[168:171], v164 offset:2048
	ds_read_b128 v[172:175], v175 offset:2048
	s_add_u32 s2, s26, 0x100
	s_addc_u32 s3, s27, 0
	s_cmp_eq_u32 s65, 12
	s_cselect_b32 s34, s22, s2
	s_cselect_b32 s35, s23, s3
	s_cselect_b32 s30, s20, s19
	s_cselect_b32 s31, s21, s64
	s_add_u32 s28, s34, 0x80
	s_addc_u32 s29, s35, 0
	v_xor_b32_e32 v213, 64, v165
	ds_read_b128 v[176:179], v165
	ds_read_b128 v[180:183], v213
	ds_read_b128 v[184:187], v165 offset:2048
	ds_read_b128 v[188:191], v213 offset:2048
	ds_read_b128 v[198:201], v165 offset:4096
	ds_read_b128 v[202:205], v213 offset:4096
	ds_read_b128 v[206:209], v165 offset:6144
	ds_read_b128 v[210:213], v213 offset:6144
	s_add_u32 s26, s26, 0x40080
	s_addc_u32 s27, s27, 0
	s_mov_b32 m0, s61
	s_nop 0
	global_load_lds_dwordx4 v157, s[26:27]
	s_add_i32 s66, s42, 0xe000
	s_mov_b32 m0, s66
	s_nop 0
	global_load_lds_dwordx4 v159, s[26:27]
	s_waitcnt vmcnt(8)
	s_waitcnt lgkmcnt(0)
	s_barrier
	s_setprio 1
	s_waitcnt lgkmcnt(7)
	v_mfma_f32_16x16x32_bf16 v[126:129], v[130:133], v[176:179], v[126:129]
	v_mfma_f32_16x16x32_bf16 v[122:125], v[138:141], v[176:179], v[122:125]
	s_waitcnt lgkmcnt(5)
	v_mfma_f32_16x16x32_bf16 v[118:121], v[130:133], v[184:187], v[118:121]
	v_mfma_f32_16x16x32_bf16 v[110:113], v[138:141], v[184:187], v[110:113]
	s_waitcnt lgkmcnt(3)
	v_mfma_f32_16x16x32_bf16 v[102:105], v[130:133], v[198:201], v[102:105]
	v_mfma_f32_16x16x32_bf16 v[92:95], v[138:141], v[198:201], v[92:95]
	s_waitcnt lgkmcnt(1)
	v_mfma_f32_16x16x32_bf16 v[84:87], v[130:133], v[206:209], v[84:87]
	v_mfma_f32_16x16x32_bf16 v[76:79], v[138:141], v[206:209], v[76:79]
	v_mfma_f32_16x16x32_bf16 v[126:129], v[134:137], v[180:183], v[126:129]
	v_mfma_f32_16x16x32_bf16 v[122:125], v[142:145], v[180:183], v[122:125]
	v_mfma_f32_16x16x32_bf16 v[118:121], v[134:137], v[188:191], v[118:121]
	v_mfma_f32_16x16x32_bf16 v[110:113], v[142:145], v[188:191], v[110:113]
	v_mfma_f32_16x16x32_bf16 v[102:105], v[134:137], v[202:205], v[102:105]
	v_mfma_f32_16x16x32_bf16 v[92:95], v[142:145], v[202:205], v[92:95]
	s_waitcnt lgkmcnt(0)
	v_mfma_f32_16x16x32_bf16 v[84:87], v[134:137], v[210:213], v[84:87]
	v_mfma_f32_16x16x32_bf16 v[76:79], v[142:145], v[210:213], v[76:79]
	s_setprio 0
	s_setprio 1
	v_mfma_f32_16x16x32_bf16 v[114:117], v[146:149], v[176:179], v[114:117]
	v_mfma_f32_16x16x32_bf16 v[106:109], v[168:171], v[176:179], v[106:109]
	v_mfma_f32_16x16x32_bf16 v[98:101], v[146:149], v[184:187], v[98:101]
	v_mfma_f32_16x16x32_bf16 v[88:91], v[168:171], v[184:187], v[88:91]
	v_mfma_f32_16x16x32_bf16 v[80:83], v[146:149], v[198:201], v[80:83]
	v_mfma_f32_16x16x32_bf16 v[72:75], v[168:171], v[198:201], v[72:75]
	v_mfma_f32_16x16x32_bf16 v[68:71], v[146:149], v[206:209], v[68:71]
	v_mfma_f32_16x16x32_bf16 v[64:67], v[168:171], v[206:209], v[64:67]
	v_mfma_f32_16x16x32_bf16 v[114:117], v[150:153], v[180:183], v[114:117]
	v_mfma_f32_16x16x32_bf16 v[106:109], v[172:175], v[180:183], v[106:109]
	v_mfma_f32_16x16x32_bf16 v[98:101], v[150:153], v[188:191], v[98:101]
	v_mfma_f32_16x16x32_bf16 v[88:91], v[172:175], v[188:191], v[88:91]
	v_mfma_f32_16x16x32_bf16 v[80:83], v[150:153], v[202:205], v[80:83]
	v_mfma_f32_16x16x32_bf16 v[72:75], v[172:175], v[202:205], v[72:75]
	v_mfma_f32_16x16x32_bf16 v[68:71], v[150:153], v[210:213], v[68:71]
	v_mfma_f32_16x16x32_bf16 v[64:67], v[172:175], v[210:213], v[64:67]
	s_setprio 0
	s_barrier
	v_xor_b32_e32 v213, 64, v165
	ds_read_b128 v[176:179], v165 offset:16384
	ds_read_b128 v[180:183], v213 offset:16384
	ds_read_b128 v[184:187], v165 offset:18432
	ds_read_b128 v[188:191], v213 offset:18432
	ds_read_b128 v[198:201], v165 offset:20480
	ds_read_b128 v[202:205], v213 offset:20480
	ds_read_b128 v[206:209], v165 offset:22528
	ds_read_b128 v[210:213], v213 offset:22528
	s_mov_b32 m0, s43
	s_nop 0
	global_load_lds_dwordx4 v158, s[30:31]
	s_nop 0
	s_mov_b32 m0, s44
	s_nop 0
	global_load_lds_dwordx4 v160, s[30:31]
	s_add_u32 s26, s30, 0x40000
	s_addc_u32 s27, s31, 0
	s_mov_b32 m0, s45
	s_nop 0
	global_load_lds_dwordx4 v158, s[26:27]
	s_nop 0
	s_mov_b32 m0, s46
	s_nop 0
	global_load_lds_dwordx4 v160, s[26:27]
	s_mov_b32 m0, s42
	s_nop 0
	global_load_lds_dwordx4 v157, s[34:35]
	s_nop 0
	s_mov_b32 m0, s47
	s_nop 0
	global_load_lds_dwordx4 v159, s[34:35]
	s_waitcnt vmcnt(8)
	s_waitcnt lgkmcnt(0)
	s_barrier
	s_setprio 1
	s_waitcnt lgkmcnt(7)
	v_mfma_f32_16x16x32_bf16 v[60:63], v[130:133], v[176:179], v[60:63]
	v_mfma_f32_16x16x32_bf16 v[56:59], v[138:141], v[176:179], v[56:59]
	s_waitcnt lgkmcnt(5)
	v_mfma_f32_16x16x32_bf16 v[52:55], v[130:133], v[184:187], v[52:55]
	v_mfma_f32_16x16x32_bf16 v[44:47], v[138:141], v[184:187], v[44:47]
	s_waitcnt lgkmcnt(3)
	v_mfma_f32_16x16x32_bf16 v[36:39], v[130:133], v[198:201], v[36:39]
	v_mfma_f32_16x16x32_bf16 v[28:31], v[138:141], v[198:201], v[28:31]
	s_waitcnt lgkmcnt(1)
	v_mfma_f32_16x16x32_bf16 v[20:23], v[130:133], v[206:209], v[20:23]
	v_mfma_f32_16x16x32_bf16 v[12:15], v[138:141], v[206:209], v[12:15]
	v_mfma_f32_16x16x32_bf16 v[60:63], v[134:137], v[180:183], v[60:63]
	v_mfma_f32_16x16x32_bf16 v[56:59], v[142:145], v[180:183], v[56:59]
	v_mfma_f32_16x16x32_bf16 v[52:55], v[134:137], v[188:191], v[52:55]
	v_mfma_f32_16x16x32_bf16 v[44:47], v[142:145], v[188:191], v[44:47]
	v_mfma_f32_16x16x32_bf16 v[36:39], v[134:137], v[202:205], v[36:39]
	v_mfma_f32_16x16x32_bf16 v[28:31], v[142:145], v[202:205], v[28:31]
	s_waitcnt lgkmcnt(0)
	v_mfma_f32_16x16x32_bf16 v[20:23], v[134:137], v[210:213], v[20:23]
	v_mfma_f32_16x16x32_bf16 v[12:15], v[142:145], v[210:213], v[12:15]
	s_setprio 0
	s_setprio 1
	v_mfma_f32_16x16x32_bf16 v[48:51], v[146:149], v[176:179], v[48:51]
	v_mfma_f32_16x16x32_bf16 v[40:43], v[168:171], v[176:179], v[40:43]
	v_mfma_f32_16x16x32_bf16 v[32:35], v[146:149], v[184:187], v[32:35]
	v_mfma_f32_16x16x32_bf16 v[24:27], v[168:171], v[184:187], v[24:27]
	v_mfma_f32_16x16x32_bf16 v[16:19], v[146:149], v[198:201], v[16:19]
	v_mfma_f32_16x16x32_bf16 v[8:11], v[168:171], v[198:201], v[8:11]
	v_mfma_f32_16x16x32_bf16 v[4:7], v[146:149], v[206:209], v[4:7]
	v_mfma_f32_16x16x32_bf16 v[0:3], v[168:171], v[206:209], v[0:3]
	v_mfma_f32_16x16x32_bf16 v[48:51], v[150:153], v[180:183], v[48:51]
	v_mfma_f32_16x16x32_bf16 v[40:43], v[172:175], v[180:183], v[40:43]
	v_mfma_f32_16x16x32_bf16 v[32:35], v[150:153], v[188:191], v[32:35]
	v_mfma_f32_16x16x32_bf16 v[24:27], v[172:175], v[188:191], v[24:27]
	v_mfma_f32_16x16x32_bf16 v[16:19], v[150:153], v[202:205], v[16:19]
	v_mfma_f32_16x16x32_bf16 v[8:11], v[172:175], v[202:205], v[8:11]
	v_mfma_f32_16x16x32_bf16 v[4:7], v[150:153], v[210:213], v[4:7]
	v_mfma_f32_16x16x32_bf16 v[0:3], v[172:175], v[210:213], v[0:3]
	s_setprio 0
	s_barrier
	v_xor_b32_e32 v145, 64, v166
	ds_read_b128 v[130:133], v166
	ds_read_b128 v[134:137], v145
	ds_read_b128 v[138:141], v166 offset:2048
	ds_read_b128 v[142:145], v145 offset:2048
	v_xor_b32_e32 v175, 64, v167
	ds_read_b128 v[146:149], v167
	ds_read_b128 v[150:153], v175
	ds_read_b128 v[168:171], v167 offset:2048
	ds_read_b128 v[172:175], v175 offset:2048
	v_xor_b32_e32 v213, 64, v165
	ds_read_b128 v[176:179], v165 offset:32768
	ds_read_b128 v[180:183], v213 offset:32768
	ds_read_b128 v[184:187], v165 offset:34816
	ds_read_b128 v[188:191], v213 offset:34816
	ds_read_b128 v[198:201], v165 offset:36864
	ds_read_b128 v[202:205], v213 offset:36864
	ds_read_b128 v[206:209], v165 offset:38912
	ds_read_b128 v[210:213], v213 offset:38912
	s_add_u32 s26, s34, 0x40000
	s_addc_u32 s27, s35, 0
	s_mov_b32 m0, s48
	s_nop 0
	global_load_lds_dwordx4 v157, s[26:27]
	s_nop 0
	s_mov_b32 m0, s49
	s_nop 0
	global_load_lds_dwordx4 v159, s[26:27]
	s_waitcnt vmcnt(8)
	s_waitcnt lgkmcnt(0)
	s_barrier
	s_setprio 1
	s_waitcnt lgkmcnt(7)
	v_mfma_f32_16x16x32_bf16 v[126:129], v[130:133], v[176:179], v[126:129]
	v_mfma_f32_16x16x32_bf16 v[122:125], v[138:141], v[176:179], v[122:125]
	s_waitcnt lgkmcnt(5)
	v_mfma_f32_16x16x32_bf16 v[118:121], v[130:133], v[184:187], v[118:121]
	v_mfma_f32_16x16x32_bf16 v[110:113], v[138:141], v[184:187], v[110:113]
	s_waitcnt lgkmcnt(3)
	v_mfma_f32_16x16x32_bf16 v[102:105], v[130:133], v[198:201], v[102:105]
	v_mfma_f32_16x16x32_bf16 v[92:95], v[138:141], v[198:201], v[92:95]
	s_waitcnt lgkmcnt(1)
	v_mfma_f32_16x16x32_bf16 v[84:87], v[130:133], v[206:209], v[84:87]
	v_mfma_f32_16x16x32_bf16 v[76:79], v[138:141], v[206:209], v[76:79]
	v_mfma_f32_16x16x32_bf16 v[126:129], v[134:137], v[180:183], v[126:129]
	v_mfma_f32_16x16x32_bf16 v[122:125], v[142:145], v[180:183], v[122:125]
	v_mfma_f32_16x16x32_bf16 v[118:121], v[134:137], v[188:191], v[118:121]
	v_mfma_f32_16x16x32_bf16 v[110:113], v[142:145], v[188:191], v[110:113]
	v_mfma_f32_16x16x32_bf16 v[102:105], v[134:137], v[202:205], v[102:105]
	v_mfma_f32_16x16x32_bf16 v[92:95], v[142:145], v[202:205], v[92:95]
	s_waitcnt lgkmcnt(0)
	v_mfma_f32_16x16x32_bf16 v[84:87], v[134:137], v[210:213], v[84:87]
	v_mfma_f32_16x16x32_bf16 v[76:79], v[142:145], v[210:213], v[76:79]
	s_setprio 0
	s_setprio 1
	v_mfma_f32_16x16x32_bf16 v[114:117], v[146:149], v[176:179], v[114:117]
	v_mfma_f32_16x16x32_bf16 v[106:109], v[168:171], v[176:179], v[106:109]
	v_mfma_f32_16x16x32_bf16 v[98:101], v[146:149], v[184:187], v[98:101]
	v_mfma_f32_16x16x32_bf16 v[88:91], v[168:171], v[184:187], v[88:91]
	v_mfma_f32_16x16x32_bf16 v[80:83], v[146:149], v[198:201], v[80:83]
	v_mfma_f32_16x16x32_bf16 v[72:75], v[168:171], v[198:201], v[72:75]
	v_mfma_f32_16x16x32_bf16 v[68:71], v[146:149], v[206:209], v[68:71]
	v_mfma_f32_16x16x32_bf16 v[64:67], v[168:171], v[206:209], v[64:67]
	v_mfma_f32_16x16x32_bf16 v[114:117], v[150:153], v[180:183], v[114:117]
	v_mfma_f32_16x16x32_bf16 v[106:109], v[172:175], v[180:183], v[106:109]
	v_mfma_f32_16x16x32_bf16 v[98:101], v[150:153], v[188:191], v[98:101]
	v_mfma_f32_16x16x32_bf16 v[88:91], v[172:175], v[188:191], v[88:91]
	v_mfma_f32_16x16x32_bf16 v[80:83], v[150:153], v[202:205], v[80:83]
	v_mfma_f32_16x16x32_bf16 v[72:75], v[172:175], v[202:205], v[72:75]
	v_mfma_f32_16x16x32_bf16 v[68:71], v[150:153], v[210:213], v[68:71]
	v_mfma_f32_16x16x32_bf16 v[64:67], v[172:175], v[210:213], v[64:67]
	s_setprio 0
	s_barrier
	v_xor_b32_e32 v213, 64, v165
	ds_read_b128 v[176:179], v165 offset:49152
	ds_read_b128 v[180:183], v213 offset:49152
	ds_read_b128 v[184:187], v165 offset:51200
	ds_read_b128 v[188:191], v213 offset:51200
	ds_read_b128 v[198:201], v165 offset:53248
	ds_read_b128 v[202:205], v213 offset:53248
	ds_read_b128 v[206:209], v165 offset:55296
	ds_read_b128 v[210:213], v213 offset:55296
	s_add_u32 s26, s30, 0x80
	s_addc_u32 s27, s31, 0
	s_mov_b32 m0, s55
	s_nop 0
	global_load_lds_dwordx4 v158, s[26:27]
	s_nop 0
	s_mov_b32 m0, s56
	s_nop 0
	global_load_lds_dwordx4 v160, s[26:27]
	s_add_u32 s26, s30, 0x40080
	s_addc_u32 s27, s31, 0
	s_mov_b32 m0, s59
	s_nop 0
	global_load_lds_dwordx4 v158, s[26:27]
	s_nop 0
	s_mov_b32 m0, s60
	s_nop 0
	global_load_lds_dwordx4 v160, s[26:27]
	s_mov_b32 m0, s57
	s_nop 0
	global_load_lds_dwordx4 v157, s[28:29]
	s_nop 0
	s_mov_b32 m0, s58
	s_nop 0
	global_load_lds_dwordx4 v159, s[28:29]
	s_waitcnt vmcnt(8)
	s_waitcnt lgkmcnt(0)
	s_barrier
	s_setprio 1
	s_waitcnt lgkmcnt(7)
	v_mfma_f32_16x16x32_bf16 v[60:63], v[130:133], v[176:179], v[60:63]
	v_mfma_f32_16x16x32_bf16 v[56:59], v[138:141], v[176:179], v[56:59]
	s_waitcnt lgkmcnt(5)
	v_mfma_f32_16x16x32_bf16 v[52:55], v[130:133], v[184:187], v[52:55]
	v_mfma_f32_16x16x32_bf16 v[44:47], v[138:141], v[184:187], v[44:47]
	s_waitcnt lgkmcnt(3)
	v_mfma_f32_16x16x32_bf16 v[36:39], v[130:133], v[198:201], v[36:39]
	v_mfma_f32_16x16x32_bf16 v[28:31], v[138:141], v[198:201], v[28:31]
	s_waitcnt lgkmcnt(1)
	v_mfma_f32_16x16x32_bf16 v[20:23], v[130:133], v[206:209], v[20:23]
	v_mfma_f32_16x16x32_bf16 v[12:15], v[138:141], v[206:209], v[12:15]
	v_mfma_f32_16x16x32_bf16 v[60:63], v[134:137], v[180:183], v[60:63]
	v_mfma_f32_16x16x32_bf16 v[56:59], v[142:145], v[180:183], v[56:59]
	v_mfma_f32_16x16x32_bf16 v[52:55], v[134:137], v[188:191], v[52:55]
	v_mfma_f32_16x16x32_bf16 v[44:47], v[142:145], v[188:191], v[44:47]
	v_mfma_f32_16x16x32_bf16 v[36:39], v[134:137], v[202:205], v[36:39]
	v_mfma_f32_16x16x32_bf16 v[28:31], v[142:145], v[202:205], v[28:31]
	s_waitcnt lgkmcnt(0)
	v_mfma_f32_16x16x32_bf16 v[20:23], v[134:137], v[210:213], v[20:23]
	v_mfma_f32_16x16x32_bf16 v[12:15], v[142:145], v[210:213], v[12:15]
	s_setprio 0
	s_setprio 1
	v_mfma_f32_16x16x32_bf16 v[48:51], v[146:149], v[176:179], v[48:51]
	v_mfma_f32_16x16x32_bf16 v[40:43], v[168:171], v[176:179], v[40:43]
	v_mfma_f32_16x16x32_bf16 v[32:35], v[146:149], v[184:187], v[32:35]
	v_mfma_f32_16x16x32_bf16 v[24:27], v[168:171], v[184:187], v[24:27]
	v_mfma_f32_16x16x32_bf16 v[16:19], v[146:149], v[198:201], v[16:19]
	v_mfma_f32_16x16x32_bf16 v[8:11], v[168:171], v[198:201], v[8:11]
	v_mfma_f32_16x16x32_bf16 v[4:7], v[146:149], v[206:209], v[4:7]
	v_mfma_f32_16x16x32_bf16 v[0:3], v[168:171], v[206:209], v[0:3]
	v_mfma_f32_16x16x32_bf16 v[48:51], v[150:153], v[180:183], v[48:51]
	v_mfma_f32_16x16x32_bf16 v[40:43], v[172:175], v[180:183], v[40:43]
	v_mfma_f32_16x16x32_bf16 v[32:35], v[150:153], v[188:191], v[32:35]
	v_mfma_f32_16x16x32_bf16 v[24:27], v[172:175], v[188:191], v[24:27]
	v_mfma_f32_16x16x32_bf16 v[16:19], v[150:153], v[202:205], v[16:19]
	v_mfma_f32_16x16x32_bf16 v[8:11], v[172:175], v[202:205], v[8:11]
	v_mfma_f32_16x16x32_bf16 v[4:7], v[150:153], v[210:213], v[4:7]
	v_mfma_f32_16x16x32_bf16 v[0:3], v[172:175], v[210:213], v[0:3]
	s_setprio 0
	s_barrier
	s_add_i32 s65, s65, 2
	s_add_u32 s19, s19, 0x100
	s_addc_u32 s64, s64, 0
	s_cmp_gt_u32 s65, 13
	s_mov_b64 s[26:27], s[2:3]
	s_cbranch_scc0 .LBB0_243
	s_and_b64 vcc, exec, s[16:17]
	s_cbranch_vccz .LBB0_246
	s_barrier

.LBB0_256:
	s_waitcnt vmcnt(0)
	s_waitcnt vmcnt(0)
	v_readlane_b32 s2, v252, 14
	s_movk_i32 s6, 0x400
	v_readlane_b32 s3, v252, 15
	s_waitcnt lgkmcnt(0)
	s_barrier
	s_andn2_b64 vcc, exec, s[2:3]
	v_readfirstlane_b32 s16, v156
	s_cbranch_vccnz .LBB0_280
	v_bfe_i32 v2, v156, 27, 1
	v_lshlrev_b32_e32 v1, 4, v156
	v_lshrrev_b32_e32 v2, 22, v2
	v_add_u32_e32 v2, v1, v2
	v_and_b32_e32 v2, 0xfffffc00, v2
	v_sub_u32_e32 v2, v1, v2
	v_ashrrev_i32_e32 v0, 31, v156
	v_lshrrev_b32_e32 v3, 4, v2
	v_lshrrev_b32_e32 v0, 26, v0
	v_bitop3_b32 v2, v3, v2, 32 bitop3:0x6c
	v_add_u32_e32 v0, v156, v0
	v_ashrrev_i32_e32 v4, 31, v2
	v_ashrrev_i32_e32 v0, 6, v0
	v_lshrrev_b32_e32 v4, 26, v4
	v_lshlrev_b32_e32 v3, 3, v0
	v_add_u32_e32 v4, v2, v4
	v_and_b32_e32 v3, -16, v3
	v_ashrrev_i32_e32 v5, 6, v4
	v_and_b32_e32 v4, 0xc0, v4
	s_mul_i32 s3, s44, 0x300000
	v_add_u32_e32 v3, v5, v3
	v_sub_u32_e32 v2, v2, v4
	s_mul_hi_u32 s2, s44, 0x300000
	s_add_u32 s3, s4, s3
	v_lshlrev_b32_e32 v0, 5, v0
	v_ashrrev_i16_sdwa v2, v239, sext(v2) dst_sel:DWORD dst_unused:UNUSED_PAD src0_sel:DWORD src1_sel:BYTE_0
	v_lshlrev_b32_e32 v4, 1, v3
	v_lshrrev_b32_e32 v6, 2, v3
	v_and_b32_e32 v5, 3, v5
	s_movk_i32 s7, 0xffe0
	s_addc_u32 s2, s5, s2
	v_and_b32_e32 v0, 32, v0
	v_bfe_i32 v2, v2, 0, 16
	v_and_b32_e32 v4, 24, v4
	v_and_b32_e32 v6, 4, v6
	v_and_or_b32 v5, v3, s7, v5
	s_add_u32 s28, s3, 0x6b100000
	v_or3_b32 v4, v5, v6, v4
	v_add_lshl_u32 v0, v0, v2, 1
	s_addc_u32 s29, s2, 0
	v_mad_u64_u32 v[130:131], s[2:3], v3, s6, v[0:1]
	v_mbcnt_lo_u32_b32 v142, -1, 0
	v_mbcnt_hi_u32_b32 v142, -1, v142
	v_add_u32_e32 v142, s93, v142
	v_lshrrev_b32_e32 v143, 3, v142
	v_lshrrev_b32_e32 v144, 4, v142
	v_xor_b32_e32 v144, v144, v142
	v_lshlrev_b32_e32 v144, 4, v144
	v_and_b32_e32 v144, 0x70, v144
	v_lshl_add_u32 v130, v143, 10, v144
	v_mad_u64_u32 v[132:133], s[2:3], v4, s6, v[0:1]
	v_mbcnt_lo_u32_b32 v142, -1, 0
	v_mbcnt_hi_u32_b32 v142, -1, v142
	v_add_u32_e32 v142, s93, v142
	v_lshrrev_b32_e32 v143, 3, v142
	v_and_b32_e32 v144, 12, v143
	v_lshlrev_b32_e32 v144, 1, v144
	v_and_b32_e32 v132, 0xffffffe3, v143
	v_or_b32_e32 v144, v144, v132
	v_lshrrev_b32_e32 v143, 2, v143
	v_and_b32_e32 v143, 4, v143
	v_or_b32_e32 v143, v143, v144
	v_lshrrev_b32_e32 v144, 4, v142
	v_xor_b32_e32 v144, v144, v142
	v_lshlrev_b32_e32 v144, 4, v144
	v_and_b32_e32 v144, 0x70, v144
	v_lshl_add_u32 v132, v143, 10, v144
	v_add_u32_e32 v0, 0x2000, v1
	v_ashrrev_i32_e32 v1, 31, v0
	v_lshrrev_b32_e32 v1, 22, v1
	v_add_u32_e32 v1, v0, v1
	v_ashrrev_i32_e32 v1, 10, v1
	v_mul_i32_i24_e32 v2, 0x400, v1
	v_sub_u32_e32 v0, v0, v2
	v_lshrrev_b32_e32 v2, 4, v0
	v_bitop3_b32 v0, v2, v0, 32 bitop3:0x6c
	v_ashrrev_i32_e32 v3, 31, v0
	v_lshrrev_b32_e32 v3, 26, v3
	v_lshlrev_b32_e32 v2, 3, v1
	v_add_u32_e32 v3, v0, v3
	v_and_b32_e32 v2, -16, v2
	v_ashrrev_i32_e32 v4, 6, v3
	v_and_b32_e32 v3, 0xc0, v3
	v_add_u32_e32 v2, v4, v2
	v_sub_u32_e32 v0, v0, v3
	v_lshlrev_b32_e32 v1, 5, v1
	v_ashrrev_i16_sdwa v0, v239, sext(v0) dst_sel:DWORD dst_unused:UNUSED_PAD src0_sel:DWORD src1_sel:BYTE_0
	v_lshlrev_b32_e32 v3, 1, v2
	v_lshrrev_b32_e32 v5, 2, v2
	v_and_b32_e32 v4, 3, v4
	v_and_b32_e32 v1, 32, v1
	v_bfe_i32 v0, v0, 0, 16
	v_and_b32_e32 v3, 24, v3
	v_and_b32_e32 v5, 4, v5
	v_and_or_b32 v4, v2, s7, v4
	s_add_u32 s30, s4, 0x6a100000
	v_or3_b32 v3, v4, v5, v3
	v_add_lshl_u32 v0, v1, v0, 1
	s_addc_u32 s31, s5, 0
	v_mad_u64_u32 v[134:135], s[2:3], v2, s6, v[0:1]
	v_mbcnt_lo_u32_b32 v142, -1, 0
	v_mbcnt_hi_u32_b32 v142, -1, v142
	v_add_u32_e32 v142, s93, v142
	v_lshrrev_b32_e32 v143, 3, v142
	v_add_u32_e32 v143, 64, v143
	v_lshrrev_b32_e32 v144, 4, v142
	v_xor_b32_e32 v144, v144, v142
	v_lshlrev_b32_e32 v144, 4, v144
	v_and_b32_e32 v144, 0x70, v144
	v_lshl_add_u32 v134, v143, 10, v144
	v_mad_u64_u32 v[136:137], s[2:3], v3, s6, v[0:1]
	v_mbcnt_lo_u32_b32 v142, -1, 0
	v_mbcnt_hi_u32_b32 v142, -1, v142
	v_add_u32_e32 v142, s93, v142
	v_lshrrev_b32_e32 v143, 3, v142
	v_add_u32_e32 v143, 64, v143
	v_and_b32_e32 v144, 12, v143
	v_lshlrev_b32_e32 v144, 1, v144
	v_and_b32_e32 v136, 0xffffffe3, v143
	v_or_b32_e32 v144, v144, v136
	v_lshrrev_b32_e32 v143, 2, v143
	v_and_b32_e32 v143, 4, v143
	v_or_b32_e32 v143, v143, v144
	v_lshrrev_b32_e32 v144, 4, v142
	v_xor_b32_e32 v144, v144, v142
	v_lshlrev_b32_e32 v144, 4, v144
	v_and_b32_e32 v144, 0x70, v144
	v_lshl_add_u32 v136, v143, 10, v144
	s_ashr_i32 s7, s6, 31
	v_readlane_b32 s10, v253, 22
	v_readlane_b32 s20, v253, 17
	s_mul_hi_u32 s2, s10, s6
	s_mul_i32 s3, s10, s7
	s_mul_i32 s17, s10, s6
	s_lshl_b64 s[10:11], s[6:7], 8
	v_readlane_b32 s21, v253, 18
	s_add_i32 s13, s2, s3
	s_mul_i32 s2, s10, s21
	s_mul_hi_u32 s3, s10, s20
	s_add_i32 s18, s3, s2
	s_lshr_b64 s[2:3], s[6:7], 24
	s_ashr_i32 s14, s16, 6
	s_mul_i32 s2, s2, s20
	s_ashr_i32 s15, s16, 8
	s_lshl_b64 s[8:9], s[6:7], 7
	s_lshl_b32 s12, s14, 10
	s_add_i32 s18, s18, s2
	s_mul_i32 s2, s10, s20
	s_add_u32 s20, s28, s2
	s_addc_u32 s21, s29, s18
	s_add_i32 s34, s12, 0
	s_add_i32 s35, s34, 0x10000
	s_mov_b32 m0, s35
	s_nop 0
	global_load_lds_dwordx4 v132, s[20:21]
	s_add_i32 s36, s34, 0x12000
	s_mov_b32 m0, s36
	s_nop 0
	global_load_lds_dwordx4 v136, s[20:21]
	s_add_u32 s2, s20, s8
	s_addc_u32 s3, s21, s9
	s_add_i32 s37, s34, 0x14000
	s_mov_b32 m0, s37
	s_nop 0
	global_load_lds_dwordx4 v132, s[2:3]
	s_add_i32 s38, s34, 0x16000
	s_mov_b32 m0, s38
	s_nop 0
	global_load_lds_dwordx4 v136, s[2:3]
	s_add_u32 s22, s30, s17
	s_addc_u32 s23, s31, s13
	s_mov_b32 m0, s34
	s_nop 0
	global_load_lds_dwordx4 v130, s[22:23]
	s_add_i32 s39, s34, 0x2000
	s_mov_b32 m0, s39
	s_nop 0
	global_load_lds_dwordx4 v134, s[22:23]
	s_add_u32 s12, s22, s8
	s_addc_u32 s13, s23, s9
	s_add_i32 s40, s34, 0x4000
	s_mov_b32 m0, s40
	s_nop 0
	global_load_lds_dwordx4 v130, s[12:13]
	s_add_i32 s41, s34, 0x6000
	s_mov_b32 m0, s41
	s_nop 0
	global_load_lds_dwordx4 v134, s[12:13]
	s_cmp_eq_u32 s15, 1
	s_cselect_b64 s[12:13], -1, 0
	s_cmp_lg_u32 s15, 1
	s_cbranch_scc1 .LBB0_259
	s_barrier
.LBB0_259:
	s_and_b32 s17, s14, 3
	v_and_b32_e32 v131, 15, v156
	s_lshr_b32 s14, s7, 25
	v_bfe_u32 v96, v156, 4, 2
	s_add_i32 s14, s6, s14
	v_lshlrev_b32_e32 v0, 6, v131
	v_lshlrev_b32_e32 v1, 2, v156
	s_ashr_i32 s42, s14, 7
	v_lshl_or_b32 v0, v96, 4, v0
	s_lshl_b32 s14, s15, 13
	v_and_b32_e32 v1, 32, v1
	v_bitop3_b32 v2, v0, s14, v1 bitop3:0xde
	s_lshl_b32 s14, s17, 12
	s_add_u32 s43, s4, 0x3c300000
	s_addc_u32 s44, s5, 0
	s_add_u32 s4, s20, 0x80
	v_bitop3_b32 v0, v0, s14, v1 bitop3:0xde
	s_waitcnt vmcnt(2)
	s_barrier
	s_addc_u32 s5, s21, 0
	s_add_i32 s45, s34, 0x18000
	s_mov_b32 m0, s45
	s_nop 0
	global_load_lds_dwordx4 v132, s[4:5]
	s_add_i32 s46, s34, 0x1a000
	s_mov_b32 m0, s46
	s_nop 0
	global_load_lds_dwordx4 v136, s[4:5]
	s_add_u32 s4, s22, 0x80
	s_addc_u32 s5, s23, 0
	s_add_i32 s47, s34, 0x8000
	s_mov_b32 m0, s47
	s_nop 0
	global_load_lds_dwordx4 v130, s[4:5]
	s_add_i32 s48, s34, 0xa000
	s_mov_b32 m0, s48
	s_nop 0
	global_load_lds_dwordx4 v134, s[4:5]
	s_add_u32 s2, s2, 0x80
	s_addc_u32 s3, s3, 0
	s_add_i32 s49, s34, 0x1c000
	s_mov_b32 m0, s49
	s_nop 0
	global_load_lds_dwordx4 v132, s[2:3]
	s_add_i32 s50, s34, 0x1e000
	s_mov_b32 m0, s50
	s_nop 0
	global_load_lds_dwordx4 v136, s[2:3]
	s_cmpk_gt_i32 s6, 0x7f
	s_cselect_b64 s[4:5], -1, 0
	s_add_i32 s51, s42, -2
	s_add_i32 s52, s34, 0xc000
	s_waitcnt vmcnt(6)
	s_cmpk_lt_u32 s16, 0x100
	s_cselect_b64 s[14:15], -1, 0
	s_and_b32 s2, s16, 0xfffff00
	s_lshl_b32 s3, s17, 6
	s_or_b32 s53, s3, s2
	s_mov_b32 s16, 0
	v_add_u32_e32 v133, 0, v0
	v_mbcnt_lo_u32_b32 v142, -1, 0
	v_mbcnt_hi_u32_b32 v142, -1, v142
	v_add_u32_e32 v142, s93, v142
	v_bfe_u32 v143, v142, 4, 2
	v_bfe_u32 v144, v142, 1, 3
	v_xor_b32_e32 v143, v143, v144
	v_lshlrev_b32_e32 v143, 4, v143
	v_and_b32_e32 v144, 15, v142
	v_lshl_or_b32 v143, v144, 7, v143
	v_bfe_u32 v144, v142, 6, 2
	v_lshl_or_b32 v133, v144, 12, v143
	v_add_u32_e32 v135, 0, v2
	v_mbcnt_lo_u32_b32 v142, -1, 0
	v_mbcnt_hi_u32_b32 v142, -1, v142
	v_add_u32_e32 v142, s93, v142
	v_bfe_u32 v143, v142, 4, 2
	v_bfe_u32 v144, v142, 1, 3
	v_xor_b32_e32 v143, v143, v144
	v_lshlrev_b32_e32 v143, 4, v143
	v_and_b32_e32 v144, 15, v142
	v_lshl_or_b32 v143, v144, 7, v143
	v_lshrrev_b32_e32 v144, 8, v142
	v_lshl_or_b32 v135, v144, 13, v143
	v_readlane_b32 s57, v253, 16
	v_readlane_b32 s58, v253, 21
	s_barrier
	s_branch .LBB0_262

.LBB0_272:
	v_add_u32_e32 v137, 0x10000, v133
	v_xor_b32_e32 v153, 64, v137
	ds_read_b128 v[138:141], v137
	ds_read_b128 v[142:145], v153
	ds_read_b128 v[146:149], v137 offset:2048
	ds_read_b128 v[150:153], v153 offset:2048
	v_add_u32_e32 v137, 0x14000, v133
	v_xor_b32_e32 v169, 64, v137
	ds_read_b128 v[154:157], v137
	ds_read_b128 v[158:161], v169
	ds_read_b128 v[162:165], v137 offset:2048
	ds_read_b128 v[166:169], v169 offset:2048
	s_add_i32 s63, s22, 2
	s_cmp_eq_u32 s51, s22
	s_cselect_b32 s26, s18, s61
	s_cselect_b32 s27, s19, s62
	s_cselect_b32 s24, s16, s59
	s_cselect_b32 s25, s17, s60
	s_add_u32 s22, s26, 0x80
	s_addc_u32 s23, s27, 0
	v_xor_b32_e32 v205, 64, v135
	ds_read_b128 v[170:173], v135
	ds_read_b128 v[174:177], v205
	ds_read_b128 v[178:181], v135 offset:2048
	ds_read_b128 v[182:185], v205 offset:2048
	ds_read_b128 v[186:189], v135 offset:4096
	ds_read_b128 v[190:193], v205 offset:4096
	ds_read_b128 v[198:201], v135 offset:6144
	ds_read_b128 v[202:205], v205 offset:6144
	s_mov_b32 m0, s52
	s_nop 0
	global_load_lds_dwordx4 v130, s[20:21]
	s_add_i32 s64, s34, 0xe000
	s_mov_b32 m0, s64
	s_nop 0
	global_load_lds_dwordx4 v134, s[20:21]
	s_waitcnt vmcnt(8)
	s_waitcnt lgkmcnt(0)
	s_barrier
	s_setprio 1
	s_waitcnt lgkmcnt(6)
	v_mfma_scale_f32_16x16x128_f8f6f4 v[126:129], v[138:145], v[170:177], v[126:129], v243, v243 op_sel_hi:[0,0,0]
	v_mfma_scale_f32_16x16x128_f8f6f4 v[122:125], v[146:153], v[170:177], v[122:125], v243, v243 op_sel_hi:[0,0,0]
	s_waitcnt lgkmcnt(4)
	v_mfma_scale_f32_16x16x128_f8f6f4 v[110:113], v[138:145], v[178:185], v[110:113], v243, v243 op_sel_hi:[0,0,0]
	v_mfma_scale_f32_16x16x128_f8f6f4 v[106:109], v[146:153], v[178:185], v[106:109], v243, v243 op_sel_hi:[0,0,0]
	s_waitcnt lgkmcnt(2)
	v_mfma_scale_f32_16x16x128_f8f6f4 v[206:209], v[138:145], v[186:193], v[92:95], v243, v243 op_sel_hi:[0,0,0]
	v_mfma_scale_f32_16x16x128_f8f6f4 v[210:213], v[146:153], v[186:193], v[88:91], v243, v243 op_sel_hi:[0,0,0]
	s_waitcnt lgkmcnt(0)
	v_mfma_scale_f32_16x16x128_f8f6f4 v[214:217], v[138:145], v[198:205], v[76:79], v243, v243 op_sel_hi:[0,0,0]
	v_mfma_scale_f32_16x16x128_f8f6f4 v[218:221], v[146:153], v[198:205], v[72:75], v243, v243 op_sel_hi:[0,0,0]
	s_setprio 0
	s_setprio 1
	v_mfma_scale_f32_16x16x128_f8f6f4 v[118:121], v[154:161], v[170:177], v[118:121], v243, v243 op_sel_hi:[0,0,0]
	v_mfma_scale_f32_16x16x128_f8f6f4 v[114:117], v[162:169], v[170:177], v[114:117], v243, v243 op_sel_hi:[0,0,0]
	v_mfma_scale_f32_16x16x128_f8f6f4 v[102:105], v[154:161], v[178:185], v[102:105], v243, v243 op_sel_hi:[0,0,0]
	v_mfma_scale_f32_16x16x128_f8f6f4 v[98:101], v[162:169], v[178:185], v[98:101], v243, v243 op_sel_hi:[0,0,0]
	v_mfma_scale_f32_16x16x128_f8f6f4 v[170:173], v[154:161], v[186:193], v[84:87], v243, v243 op_sel_hi:[0,0,0]
	v_mfma_scale_f32_16x16x128_f8f6f4 v[174:177], v[162:169], v[186:193], v[80:83], v243, v243 op_sel_hi:[0,0,0]
	v_mfma_scale_f32_16x16x128_f8f6f4 v[178:181], v[154:161], v[198:205], v[68:71], v243, v243 op_sel_hi:[0,0,0]
	v_mfma_scale_f32_16x16x128_f8f6f4 v[182:185], v[162:169], v[198:205], v[64:67], v243, v243 op_sel_hi:[0,0,0]
	s_setprio 0
	s_barrier
	s_nop 4
	v_xor_b32_e32 v95, 64, v135
	ds_read_b128 v[64:67], v135 offset:16384
	ds_read_b128 v[68:71], v95 offset:16384
	ds_read_b128 v[72:75], v135 offset:18432
	ds_read_b128 v[76:79], v95 offset:18432
	ds_read_b128 v[80:83], v135 offset:20480
	ds_read_b128 v[84:87], v95 offset:20480
	ds_read_b128 v[88:91], v135 offset:22528
	ds_read_b128 v[92:95], v95 offset:22528
	s_mov_b32 m0, s35
	s_nop 0
	global_load_lds_dwordx4 v132, s[24:25]
	s_nop 0
	s_mov_b32 m0, s36
	s_nop 0
	global_load_lds_dwordx4 v136, s[24:25]
	s_add_u32 s64, s24, s8
	s_addc_u32 s65, s25, s9
	s_mov_b32 m0, s37
	s_nop 0
	global_load_lds_dwordx4 v132, s[64:65]
	s_nop 0
	s_mov_b32 m0, s38
	s_nop 0
	global_load_lds_dwordx4 v136, s[64:65]
	s_mov_b32 m0, s34
	s_nop 0
	global_load_lds_dwordx4 v130, s[26:27]
	s_nop 0
	s_mov_b32 m0, s39
	s_nop 0
	global_load_lds_dwordx4 v134, s[26:27]
	s_waitcnt vmcnt(8)
	s_waitcnt lgkmcnt(0)
	s_barrier
	s_setprio 1
	s_waitcnt lgkmcnt(6)
	v_mfma_scale_f32_16x16x128_f8f6f4 v[60:63], v[138:145], v[64:71], v[60:63], v243, v243 op_sel_hi:[0,0,0]
	v_mfma_scale_f32_16x16x128_f8f6f4 v[56:59], v[146:153], v[64:71], v[56:59], v243, v243 op_sel_hi:[0,0,0]
	s_waitcnt lgkmcnt(4)
	v_mfma_scale_f32_16x16x128_f8f6f4 v[186:189], v[138:145], v[72:79], v[44:47], v243, v243 op_sel_hi:[0,0,0]
	v_mfma_scale_f32_16x16x128_f8f6f4 v[190:193], v[146:153], v[72:79], v[40:43], v243, v243 op_sel_hi:[0,0,0]
	s_waitcnt lgkmcnt(2)
	v_mfma_scale_f32_16x16x128_f8f6f4 v[198:201], v[138:145], v[80:87], v[28:31], v243, v243 op_sel_hi:[0,0,0]
	v_mfma_scale_f32_16x16x128_f8f6f4 v[202:205], v[146:153], v[80:87], v[24:27], v243, v243 op_sel_hi:[0,0,0]
	s_waitcnt lgkmcnt(0)
	v_mfma_scale_f32_16x16x128_f8f6f4 v[244:247], v[138:145], v[88:95], v[12:15], v243, v243 op_sel_hi:[0,0,0]
	v_mfma_scale_f32_16x16x128_f8f6f4 v[248:251], v[146:153], v[88:95], v[8:11], v243, v243 op_sel_hi:[0,0,0]
	s_setprio 0
	s_setprio 1
	v_mfma_scale_f32_16x16x128_f8f6f4 v[52:55], v[154:161], v[64:71], v[52:55], v243, v243 op_sel_hi:[0,0,0]
	v_mfma_scale_f32_16x16x128_f8f6f4 v[48:51], v[162:169], v[64:71], v[48:51], v243, v243 op_sel_hi:[0,0,0]
	v_mfma_scale_f32_16x16x128_f8f6f4 v[194:197], v[154:161], v[72:79], v[36:39], v243, v243 op_sel_hi:[0,0,0]
	v_mfma_scale_f32_16x16x128_f8f6f4 v[230:233], v[162:169], v[72:79], v[32:35], v243, v243 op_sel_hi:[0,0,0]
	v_mfma_scale_f32_16x16x128_f8f6f4 v[226:229], v[154:161], v[80:87], v[20:23], v243, v243 op_sel_hi:[0,0,0]
	v_mfma_scale_f32_16x16x128_f8f6f4 v[238:241], v[162:169], v[80:87], v[16:19], v243, v243 op_sel_hi:[0,0,0]
	v_mfma_scale_f32_16x16x128_f8f6f4 v[234:237], v[154:161], v[88:95], v[4:7], v243, v243 op_sel_hi:[0,0,0]
	v_mfma_scale_f32_16x16x128_f8f6f4 v[222:225], v[162:169], v[88:95], v[0:3], v243, v243 op_sel_hi:[0,0,0]
	s_setprio 0
	s_barrier
	v_add_u32_e32 v8, 0x18000, v133
	s_nop 3
	v_xor_b32_e32 v23, 64, v8
	ds_read_b128 v[0:3], v8
	ds_read_b128 v[4:7], v23
	ds_read_b128 v[16:19], v8 offset:2048
	ds_read_b128 v[20:23], v23 offset:2048
	v_add_u32_e32 v8, 0x1c000, v133
	v_xor_b32_e32 v153, 64, v8
	ds_read_b128 v[138:141], v8
	ds_read_b128 v[142:145], v153
	ds_read_b128 v[146:149], v8 offset:2048
	ds_read_b128 v[150:153], v153 offset:2048
	v_xor_b32_e32 v47, 64, v135
	ds_read_b128 v[8:11], v135 offset:32768
	ds_read_b128 v[12:15], v47 offset:32768
	ds_read_b128 v[24:27], v135 offset:34816
	ds_read_b128 v[28:31], v47 offset:34816
	ds_read_b128 v[32:35], v135 offset:36864
	ds_read_b128 v[36:39], v47 offset:36864
	ds_read_b128 v[40:43], v135 offset:38912
	ds_read_b128 v[44:47], v47 offset:38912
	s_add_u32 s26, s26, s8
	s_addc_u32 s27, s27, s9
	s_mov_b32 m0, s40
	s_nop 0
	global_load_lds_dwordx4 v130, s[26:27]
	s_nop 0
	s_mov_b32 m0, s41
	s_nop 0
	global_load_lds_dwordx4 v134, s[26:27]
	s_waitcnt vmcnt(8)
	s_waitcnt lgkmcnt(0)
	s_barrier
	s_setprio 1
	s_waitcnt lgkmcnt(6)
	v_mfma_scale_f32_16x16x128_f8f6f4 v[126:129], v[0:7], v[8:15], v[126:129], v243, v243 op_sel_hi:[0,0,0]
	v_mfma_scale_f32_16x16x128_f8f6f4 v[122:125], v[16:23], v[8:15], v[122:125], v243, v243 op_sel_hi:[0,0,0]
	s_waitcnt lgkmcnt(4)
	v_mfma_scale_f32_16x16x128_f8f6f4 v[110:113], v[0:7], v[24:31], v[110:113], v243, v243 op_sel_hi:[0,0,0]
	v_mfma_scale_f32_16x16x128_f8f6f4 v[106:109], v[16:23], v[24:31], v[106:109], v243, v243 op_sel_hi:[0,0,0]
	s_waitcnt lgkmcnt(2)
	v_mfma_scale_f32_16x16x128_f8f6f4 v[92:95], v[0:7], v[32:39], v[206:209], v243, v243 op_sel_hi:[0,0,0]
	v_mfma_scale_f32_16x16x128_f8f6f4 v[88:91], v[16:23], v[32:39], v[210:213], v243, v243 op_sel_hi:[0,0,0]
	s_waitcnt lgkmcnt(0)
	v_mfma_scale_f32_16x16x128_f8f6f4 v[76:79], v[0:7], v[40:47], v[214:217], v243, v243 op_sel_hi:[0,0,0]
	v_mfma_scale_f32_16x16x128_f8f6f4 v[72:75], v[16:23], v[40:47], v[218:221], v243, v243 op_sel_hi:[0,0,0]
	s_setprio 0
	s_setprio 1
	v_mfma_scale_f32_16x16x128_f8f6f4 v[118:121], v[138:145], v[8:15], v[118:121], v243, v243 op_sel_hi:[0,0,0]
	v_mfma_scale_f32_16x16x128_f8f6f4 v[114:117], v[146:153], v[8:15], v[114:117], v243, v243 op_sel_hi:[0,0,0]
	v_mfma_scale_f32_16x16x128_f8f6f4 v[102:105], v[138:145], v[24:31], v[102:105], v243, v243 op_sel_hi:[0,0,0]
	v_mfma_scale_f32_16x16x128_f8f6f4 v[98:101], v[146:153], v[24:31], v[98:101], v243, v243 op_sel_hi:[0,0,0]
	v_mfma_scale_f32_16x16x128_f8f6f4 v[84:87], v[138:145], v[32:39], v[170:173], v243, v243 op_sel_hi:[0,0,0]
	v_mfma_scale_f32_16x16x128_f8f6f4 v[80:83], v[146:153], v[32:39], v[174:177], v243, v243 op_sel_hi:[0,0,0]
	v_mfma_scale_f32_16x16x128_f8f6f4 v[68:71], v[138:145], v[40:47], v[178:181], v243, v243 op_sel_hi:[0,0,0]
	v_mfma_scale_f32_16x16x128_f8f6f4 v[64:67], v[146:153], v[40:47], v[182:185], v243, v243 op_sel_hi:[0,0,0]
	s_setprio 0
	s_barrier
	v_xor_b32_e32 v177, 64, v135
	ds_read_b128 v[32:35], v135 offset:49152
	ds_read_b128 v[36:39], v177 offset:49152
	ds_read_b128 v[154:157], v135 offset:51200
	ds_read_b128 v[158:161], v177 offset:51200
	ds_read_b128 v[162:165], v135 offset:53248
	ds_read_b128 v[166:169], v177 offset:53248
	ds_read_b128 v[170:173], v135 offset:55296
	ds_read_b128 v[174:177], v177 offset:55296
	s_add_u32 s24, s24, 0x80
	s_addc_u32 s25, s25, 0
	s_mov_b32 m0, s45
	s_nop 0
	global_load_lds_dwordx4 v132, s[24:25]
	s_nop 0
	s_mov_b32 m0, s46
	s_nop 0
	global_load_lds_dwordx4 v136, s[24:25]
	s_add_u32 s24, s24, s8
	s_addc_u32 s25, s25, s9
	s_mov_b32 m0, s49
	s_nop 0
	global_load_lds_dwordx4 v132, s[24:25]
	s_nop 0
	s_mov_b32 m0, s50
	s_nop 0
	global_load_lds_dwordx4 v136, s[24:25]
	s_mov_b32 m0, s47
	s_nop 0
	global_load_lds_dwordx4 v130, s[22:23]
	s_nop 0
	s_mov_b32 m0, s48
	s_nop 0
	global_load_lds_dwordx4 v134, s[22:23]
	s_waitcnt vmcnt(8)
	s_waitcnt lgkmcnt(0)
	s_barrier
	s_setprio 1
	s_waitcnt lgkmcnt(6)
	v_mfma_scale_f32_16x16x128_f8f6f4 v[60:63], v[0:7], v[32:39], v[60:63], v243, v243 op_sel_hi:[0,0,0]
	v_mfma_scale_f32_16x16x128_f8f6f4 v[56:59], v[16:23], v[32:39], v[56:59], v243, v243 op_sel_hi:[0,0,0]
	s_waitcnt lgkmcnt(4)
	v_mfma_scale_f32_16x16x128_f8f6f4 v[44:47], v[0:7], v[154:161], v[186:189], v243, v243 op_sel_hi:[0,0,0]
	v_mfma_scale_f32_16x16x128_f8f6f4 v[40:43], v[16:23], v[154:161], v[190:193], v243, v243 op_sel_hi:[0,0,0]
	s_waitcnt lgkmcnt(2)
	v_mfma_scale_f32_16x16x128_f8f6f4 v[28:31], v[0:7], v[162:169], v[198:201], v243, v243 op_sel_hi:[0,0,0]
	v_mfma_scale_f32_16x16x128_f8f6f4 v[24:27], v[16:23], v[162:169], v[202:205], v243, v243 op_sel_hi:[0,0,0]
	s_waitcnt lgkmcnt(0)
	v_mfma_scale_f32_16x16x128_f8f6f4 v[12:15], v[0:7], v[170:177], v[244:247], v243, v243 op_sel_hi:[0,0,0]
	v_mfma_scale_f32_16x16x128_f8f6f4 v[8:11], v[16:23], v[170:177], v[248:251], v243, v243 op_sel_hi:[0,0,0]
	s_setprio 0
	s_setprio 1
	v_mfma_scale_f32_16x16x128_f8f6f4 v[52:55], v[138:145], v[32:39], v[52:55], v243, v243 op_sel_hi:[0,0,0]
	v_mfma_scale_f32_16x16x128_f8f6f4 v[48:51], v[146:153], v[32:39], v[48:51], v243, v243 op_sel_hi:[0,0,0]
	v_mfma_scale_f32_16x16x128_f8f6f4 v[36:39], v[138:145], v[154:161], v[194:197], v243, v243 op_sel_hi:[0,0,0]
	v_mfma_scale_f32_16x16x128_f8f6f4 v[32:35], v[146:153], v[154:161], v[230:233], v243, v243 op_sel_hi:[0,0,0]
	v_mfma_scale_f32_16x16x128_f8f6f4 v[20:23], v[138:145], v[162:169], v[226:229], v243, v243 op_sel_hi:[0,0,0]
	v_mfma_scale_f32_16x16x128_f8f6f4 v[16:19], v[146:153], v[162:169], v[238:241], v243, v243 op_sel_hi:[0,0,0]
	v_mfma_scale_f32_16x16x128_f8f6f4 v[4:7], v[138:145], v[170:177], v[234:237], v243, v243 op_sel_hi:[0,0,0]
	v_mfma_scale_f32_16x16x128_f8f6f4 v[0:3], v[146:153], v[170:177], v[222:225], v243, v243 op_sel_hi:[0,0,0]
	s_setprio 0
	s_barrier
	s_add_u32 s59, s59, 0x100
	s_addc_u32 s60, s60, 0
	s_add_u32 s61, s61, 0x100
	s_addc_u32 s62, s62, 0
	s_add_u32 s20, s20, 0x100
	s_addc_u32 s21, s21, 0
	s_cmp_ge_i32 s63, s42
	s_mov_b32 s22, s63
	s_cbranch_scc0 .LBB0_272
	v_mov_b32_e32 v239, 1
	v_mov_b32_e32 v240, 0x260
	v_mov_b32_e32 v241, 0x358637bd
	v_mov_b32_e32 v224, 0x3727c5ac
	v_bfrev_b32_e32 v226, -2
	v_mov_b32_e32 v227, 0x600
	v_mov_b64_e32 v[230:231], 0x100
	v_mov_b64_e32 v[232:233], 0xff
	v_mov_b32_e32 v229, 0x3d800000

.LBB0_1137:
	s_andn2_b64 vcc, exec, s[2:3]
	v_readlane_b32 s2, v252, 58
	v_readlane_b32 s3, v252, 59
	s_nop 1
	v_cndmask_b32_e64 v0, 0, 1, s[2:3]
	v_cmp_ne_u32_e64 s[36:37], 1, v0
	s_cbranch_vccnz .LBB0_1219
	v_readlane_b32 s4, v252, 0
	v_readlane_b32 s5, v252, 1
	s_waitcnt vmcnt(0) expcnt(0) lgkmcnt(0)
	v_mbcnt_lo_u32_b32 v0, -1, 0
	v_mbcnt_hi_u32_b32 v0, -1, v0
	s_movk_i32 s2, 0x300
	v_add_u32_e32 v0, s93, v0
	s_and_b64 vcc, exec, s[36:37]
	s_nop 0
	v_readfirstlane_b32 s18, v0
	s_cbranch_vccnz .LBB0_1167
	v_bfe_i32 v3, v0, 27, 1
	v_lshlrev_b32_e32 v1, 4, v0
	v_lshrrev_b32_e32 v3, 22, v3
	v_add_u32_e32 v3, v1, v3
	v_and_b32_e32 v3, 0xfffffc00, v3
	v_sub_u32_e32 v3, v1, v3
	v_lshrrev_b32_e32 v4, 4, v3
	s_load_dwordx2 s[4:5], s[4:5], 0x98
	v_ashrrev_i32_e32 v2, 31, v0
	v_bitop3_b32 v3, v4, v3, 32 bitop3:0x6c
	v_lshrrev_b32_e32 v2, 26, v2
	v_ashrrev_i32_e32 v5, 31, v3
	v_add_u32_e32 v2, v0, v2
	v_lshrrev_b32_e32 v5, 26, v5
	s_mul_i32 s86, s44, 0xc0000
	v_ashrrev_i32_e32 v2, 6, v2
	v_add_u32_e32 v5, v3, v5
	s_lshl_b64 s[6:7], s[86:87], 1
	v_lshlrev_b32_e32 v4, 3, v2
	v_ashrrev_i32_e32 v6, 6, v5
	v_and_b32_e32 v5, 0xc0, v5
	s_waitcnt lgkmcnt(0)
	s_add_u32 s3, s4, s6
	v_and_b32_e32 v4, -16, v4
	v_lshlrev_b32_e32 v2, 5, v2
	v_sub_u32_e32 v3, v3, v5
	s_addc_u32 s6, s5, s7
	v_add_u32_e32 v4, v6, v4
	v_and_b32_e32 v2, 32, v2
	v_ashrrev_i16_sdwa v3, v239, sext(v3) dst_sel:DWORD dst_unused:UNUSED_PAD src0_sel:DWORD src1_sel:BYTE_0
	s_add_u32 s30, s3, 0x2d00000
	v_add_u32_sdwa v2, v2, sext(v3) dst_sel:DWORD dst_unused:UNUSED_PAD src0_sel:DWORD src1_sel:WORD_0
	v_lshlrev_b32_e32 v3, 1, v4
	v_lshrrev_b32_e32 v5, 2, v4
	v_and_b32_e32 v6, 3, v6
	s_mov_b32 s3, 0x7fffffe0
	v_and_b32_e32 v3, 24, v3
	v_and_b32_e32 v5, 4, v5
	v_and_or_b32 v6, v4, s3, v6
	v_or3_b32 v3, v6, v5, v3
	v_mul_lo_u32 v4, v4, s2
	v_mul_lo_u32 v3, v3, s2
	v_add_u32_e32 v1, 0x2000, v1
	v_add_lshl_u32 v164, v2, v4, 1
	v_mbcnt_lo_u32_b32 v180, -1, 0
	v_mbcnt_hi_u32_b32 v180, -1, v180
	v_add_u32_e32 v180, s93, v180
	v_lshrrev_b32_e32 v181, 3, v180
	v_lshrrev_b32_e32 v182, 4, v180
	v_xor_b32_e32 v182, v182, v180
	v_lshlrev_b32_e32 v182, 4, v182
	v_and_b32_e32 v182, 0x70, v182
	v_mul_u32_u24_e32 v181, 0x600, v181
	v_add_u32_e32 v164, v181, v182
	v_add_lshl_u32 v165, v3, v2, 1
	v_mbcnt_lo_u32_b32 v180, -1, 0
	v_mbcnt_hi_u32_b32 v180, -1, v180
	v_add_u32_e32 v180, s93, v180
	v_lshrrev_b32_e32 v181, 3, v180
	v_and_b32_e32 v182, 12, v181
	v_lshlrev_b32_e32 v182, 1, v182
	v_and_b32_e32 v165, 0xffffffe3, v181
	v_or_b32_e32 v182, v182, v165
	v_lshrrev_b32_e32 v181, 2, v181
	v_and_b32_e32 v181, 4, v181
	v_or_b32_e32 v181, v181, v182
	v_lshrrev_b32_e32 v182, 4, v180
	v_xor_b32_e32 v182, v182, v180
	v_lshlrev_b32_e32 v182, 4, v182
	v_and_b32_e32 v182, 0x70, v182
	v_mul_u32_u24_e32 v181, 0x600, v181
	v_add_u32_e32 v165, v181, v182
	v_ashrrev_i32_e32 v2, 31, v1
	v_lshrrev_b32_e32 v2, 22, v2
	v_add_u32_e32 v2, v1, v2
	v_ashrrev_i32_e32 v2, 10, v2
	v_mul_i32_i24_e32 v3, 0x400, v2
	v_sub_u32_e32 v1, v1, v3
	v_lshrrev_b32_e32 v3, 4, v1
	v_bitop3_b32 v1, v3, v1, 32 bitop3:0x6c
	v_ashrrev_i32_e32 v4, 31, v1
	v_lshrrev_b32_e32 v4, 26, v4
	v_lshlrev_b32_e32 v3, 3, v2
	v_add_u32_e32 v4, v1, v4
	s_addc_u32 s31, s6, 0
	v_and_b32_e32 v3, -16, v3
	v_ashrrev_i32_e32 v5, 6, v4
	s_add_u32 s34, s4, 0x42d00000
	v_add_u32_e32 v3, v5, v3
	v_and_b32_e32 v5, 3, v5
	s_addc_u32 s35, s5, 0
	v_and_or_b32 v5, v3, s3, v5
	s_ashr_i32 s3, s2, 31
	s_lshl_b32 s12, s2, 1
	s_lshl_b64 s[8:9], s[2:3], 1
	s_lshr_b64 s[10:11], s[2:3], 31
	v_readlane_b32 s16, v253, 31
	s_mul_i32 s10, s10, s16
	s_mul_hi_u32 s11, s8, s16
	s_ashr_i32 s13, s12, 31
	v_readlane_b32 s22, v253, 35
	v_and_b32_e32 v4, 0xc0, v4
	v_readlane_b32 s17, v253, 32
	s_add_i32 s15, s11, s10
	s_lshl_b64 s[10:11], s[12:13], 8
	v_readlane_b32 s23, v253, 36
	v_lshlrev_b32_e32 v2, 5, v2
	v_sub_u32_e32 v1, v1, v4
	s_mul_i32 s21, s8, s16
	s_mul_i32 s16, s10, s23
	s_mul_hi_u32 s17, s10, s22
	s_lshr_b64 s[12:13], s[12:13], 24
	s_ashr_i32 s19, s18, 6
	v_and_b32_e32 v2, 32, v2
	v_ashrrev_i16_sdwa v1, v239, sext(v1) dst_sel:DWORD dst_unused:UNUSED_PAD src0_sel:DWORD src1_sel:BYTE_0
	s_add_i32 s16, s17, s16
	s_mul_i32 s12, s12, s22
	v_add_u32_sdwa v1, v2, sext(v1) dst_sel:DWORD dst_unused:UNUSED_PAD src0_sel:DWORD src1_sel:WORD_0
	v_lshlrev_b32_e32 v2, 1, v3
	v_lshrrev_b32_e32 v4, 2, v3
	s_ashr_i32 s20, s18, 8
	s_lshl_b64 s[6:7], s[2:3], 8
	s_lshl_b32 s14, s19, 10
	s_add_i32 s16, s16, s12
	s_mul_i32 s12, s10, s22
	v_and_b32_e32 v2, 24, v2
	v_and_b32_e32 v4, 4, v4
	s_add_u32 s22, s30, s12
	v_or3_b32 v2, v5, v4, v2
	s_addc_u32 s23, s31, s16
	s_add_i32 s38, s14, 0
	v_mul_lo_u32 v2, v2, s2
	s_add_i32 s39, s38, 0x10000
	s_mov_b32 m0, s39
	s_nop 0
	global_load_lds_dwordx4 v165, s[22:23]
	s_add_i32 s40, s38, 0x12000
	v_add_lshl_u32 v167, v2, v1, 1
	v_mbcnt_lo_u32_b32 v180, -1, 0
	v_mbcnt_hi_u32_b32 v180, -1, v180
	v_add_u32_e32 v180, s93, v180
	v_lshrrev_b32_e32 v181, 3, v180
	v_add_u32_e32 v181, 64, v181
	v_and_b32_e32 v182, 12, v181
	v_lshlrev_b32_e32 v182, 1, v182
	v_and_b32_e32 v167, 0xffffffe3, v181
	v_or_b32_e32 v182, v182, v167
	v_lshrrev_b32_e32 v181, 2, v181
	v_and_b32_e32 v181, 4, v181
	v_or_b32_e32 v181, v181, v182
	v_lshrrev_b32_e32 v182, 4, v180
	v_xor_b32_e32 v182, v182, v180
	v_lshlrev_b32_e32 v182, 4, v182
	v_and_b32_e32 v182, 0x70, v182
	v_mul_u32_u24_e32 v181, 0x600, v181
	v_add_u32_e32 v167, v181, v182
	s_mov_b32 m0, s40
	s_nop 0
	global_load_lds_dwordx4 v167, s[22:23]
	s_add_u32 s16, s22, s6
	s_addc_u32 s17, s23, s7
	s_add_i32 s41, s38, 0x14000
	s_mov_b32 m0, s41
	s_nop 0
	global_load_lds_dwordx4 v165, s[16:17]
	s_add_i32 s42, s38, 0x16000
	s_mov_b32 m0, s42
	s_nop 0
	global_load_lds_dwordx4 v167, s[16:17]
	s_add_u32 s24, s34, s21
	v_mul_lo_u32 v3, v3, s2
	s_addc_u32 s25, s35, s15
	s_mov_b32 m0, s38
	s_nop 0
	global_load_lds_dwordx4 v164, s[24:25]
	v_add_lshl_u32 v166, v1, v3, 1
	v_mbcnt_lo_u32_b32 v180, -1, 0
	v_mbcnt_hi_u32_b32 v180, -1, v180
	v_add_u32_e32 v180, s93, v180
	v_lshrrev_b32_e32 v181, 3, v180
	v_add_u32_e32 v181, 64, v181
	v_lshrrev_b32_e32 v182, 4, v180
	v_xor_b32_e32 v182, v182, v180
	v_lshlrev_b32_e32 v182, 4, v182
	v_and_b32_e32 v182, 0x70, v182
	v_mul_u32_u24_e32 v181, 0x600, v181
	v_add_u32_e32 v166, v181, v182
	s_add_i32 s43, s38, 0x2000
	s_mov_b32 m0, s43
	s_nop 0
	global_load_lds_dwordx4 v166, s[24:25]
	s_add_u32 s12, s24, s6
	s_addc_u32 s13, s25, s7
	s_add_i32 s44, s38, 0x4000
	s_mov_b32 m0, s44
	s_nop 0
	global_load_lds_dwordx4 v164, s[12:13]
	s_add_i32 s45, s38, 0x6000
	s_mov_b32 m0, s45
	s_nop 0
	global_load_lds_dwordx4 v166, s[12:13]
	s_cmp_eq_u32 s20, 1
	s_cselect_b64 s[12:13], -1, 0
	s_cmp_lg_u32 s20, 1
	s_cbranch_scc1 .LBB0_1141
	s_barrier
.LBB0_1141:
	s_add_u32 s46, s4, 0x3c300000
	s_addc_u32 s47, s5, 0
	s_add_u32 s14, s4, 0x48500000
	s_addc_u32 s15, s5, 0
	v_bfe_u32 v168, v0, 4, 2
	s_lshr_b32 s3, s3, 26
	v_and_b32_e32 v169, 15, v0
	s_add_i32 s3, s2, s3
	v_lshlrev_b32_e32 v1, 4, v168
	v_lshlrev_b32_e32 v0, 2, v0
	s_and_b32 s19, s19, 3
	s_ashr_i32 s48, s3, 6
	v_lshl_or_b32 v1, v169, 6, v1
	s_lshl_b32 s3, s20, 13
	v_and_b32_e32 v0, 32, v0
	s_lshl_b32 s49, s20, 6
	v_bitop3_b32 v2, v1, s3, v0 bitop3:0xde
	s_lshl_b32 s50, s19, 5
	s_lshl_b32 s3, s19, 12
	s_add_u32 s4, s22, 0x80
	v_bitop3_b32 v0, v1, s3, v0 bitop3:0xde
	s_waitcnt vmcnt(2)
	s_barrier
	s_addc_u32 s5, s23, 0
	s_add_i32 s51, s38, 0x18000
	s_mov_b32 m0, s51
	s_nop 0
	global_load_lds_dwordx4 v165, s[4:5]
	s_add_i32 s52, s38, 0x1a000
	s_mov_b32 m0, s52
	s_nop 0
	global_load_lds_dwordx4 v167, s[4:5]
	s_add_u32 s4, s24, 0x80
	s_addc_u32 s5, s25, 0
	s_add_i32 s53, s38, 0x8000
	s_mov_b32 m0, s53
	s_nop 0
	global_load_lds_dwordx4 v164, s[4:5]
	s_add_i32 s54, s38, 0xa000
	s_mov_b32 m0, s54
	s_nop 0
	global_load_lds_dwordx4 v166, s[4:5]
	s_add_u32 s4, s16, 0x80
	s_addc_u32 s5, s17, 0
	s_add_i32 s55, s38, 0x1c000
	s_mov_b32 m0, s55
	s_nop 0
	global_load_lds_dwordx4 v165, s[4:5]
	s_add_i32 s56, s38, 0x1e000
	s_mov_b32 m0, s56
	s_nop 0
	global_load_lds_dwordx4 v167, s[4:5]
	s_cmp_gt_i32 s2, 63
	s_cselect_b64 s[16:17], -1, 0
	s_and_b32 s2, s18, 0xfffff00
	s_lshl_b32 s3, s19, 6
	s_waitcnt vmcnt(6)
	s_or_b32 s57, s3, s2
	s_add_i32 s58, s48, -2
	s_add_i32 s59, s38, 0xc000
	s_cmpk_lt_u32 s18, 0x100
	s_mov_b32 s60, 0
	s_cselect_b64 s[18:19], -1, 0
	v_add_u32_e32 v170, 0, v0
	v_mbcnt_lo_u32_b32 v180, -1, 0
	v_mbcnt_hi_u32_b32 v180, -1, v180
	v_add_u32_e32 v180, s93, v180
	v_bfe_u32 v181, v180, 4, 2
	v_bfe_u32 v182, v180, 1, 3
	v_xor_b32_e32 v181, v181, v182
	v_lshlrev_b32_e32 v181, 4, v181
	v_and_b32_e32 v182, 15, v180
	v_lshl_or_b32 v181, v182, 7, v181
	v_bfe_u32 v182, v180, 6, 2
	v_lshl_or_b32 v170, v182, 12, v181
	v_add_u32_e32 v171, 0, v2
	v_mbcnt_lo_u32_b32 v180, -1, 0
	v_mbcnt_hi_u32_b32 v180, -1, v180
	v_add_u32_e32 v180, s93, v180
	v_bfe_u32 v181, v180, 4, 2
	v_bfe_u32 v182, v180, 1, 3
	v_xor_b32_e32 v181, v181, v182
	v_lshlrev_b32_e32 v181, 4, v181
	v_and_b32_e32 v182, 15, v180
	v_lshl_or_b32 v181, v182, 7, v181
	v_lshrrev_b32_e32 v182, 8, v180
	v_lshl_or_b32 v171, v182, 13, v181
	v_readlane_b32 s63, v253, 20
	v_readlane_b32 s64, v253, 19
	s_barrier
	s_branch .LBB0_1144

.LBB0_1158:
	v_add_u32_e32 v96, 0x10000, v170
	v_xor_b32_e32 v147, 64, v96
	ds_read_b128 v[132:135], v96
	ds_read_b128 v[136:139], v147
	ds_read_b128 v[140:143], v96 offset:2048
	ds_read_b128 v[144:147], v147 offset:2048
	v_add_u32_e32 v96, 0x14000, v170
	v_xor_b32_e32 v163, 64, v96
	ds_read_b128 v[148:151], v96
	ds_read_b128 v[152:155], v163
	ds_read_b128 v[156:159], v96 offset:2048
	ds_read_b128 v[160:163], v163 offset:2048
	s_add_i32 s71, s28, 2
	s_cmp_eq_u32 s58, s28
	s_cselect_b32 s28, s20, s69
	s_cselect_b32 s29, s21, s70
	s_cselect_b32 s26, s4, s67
	s_cselect_b32 s27, s5, s68
	s_add_u32 s24, s28, 0x80
	s_addc_u32 s25, s29, 0
	v_xor_b32_e32 v203, 64, v171
	ds_read_b128 v[172:175], v171
	ds_read_b128 v[176:179], v203
	ds_read_b128 v[180:183], v171 offset:2048
	ds_read_b128 v[184:187], v203 offset:2048
	ds_read_b128 v[188:191], v171 offset:4096
	ds_read_b128 v[192:195], v203 offset:4096
	ds_read_b128 v[196:199], v171 offset:6144
	ds_read_b128 v[200:203], v203 offset:6144
	s_mov_b32 m0, s59
	s_nop 0
	global_load_lds_dwordx4 v164, s[22:23]
	s_add_i32 s72, s38, 0xe000
	s_mov_b32 m0, s72
	s_nop 0
	global_load_lds_dwordx4 v166, s[22:23]
	s_waitcnt vmcnt(8)
	s_waitcnt lgkmcnt(0)
	s_barrier
	s_setprio 1
	s_waitcnt lgkmcnt(7)
	v_mfma_f32_16x16x32_bf16 v[124:127], v[132:135], v[172:175], v[124:127]
	v_mfma_f32_16x16x32_bf16 v[128:131], v[140:143], v[172:175], v[128:131]
	s_waitcnt lgkmcnt(5)
	v_mfma_f32_16x16x32_bf16 v[112:115], v[132:135], v[180:183], v[112:115]
	v_mfma_f32_16x16x32_bf16 v[108:111], v[140:143], v[180:183], v[108:111]
	s_waitcnt lgkmcnt(3)
	v_mfma_f32_16x16x32_bf16 v[92:95], v[132:135], v[188:191], v[92:95]
	v_mfma_f32_16x16x32_bf16 v[88:91], v[140:143], v[188:191], v[88:91]
	s_waitcnt lgkmcnt(1)
	v_mfma_f32_16x16x32_bf16 v[76:79], v[132:135], v[196:199], v[76:79]
	v_mfma_f32_16x16x32_bf16 v[72:75], v[140:143], v[196:199], v[72:75]
	v_mfma_f32_16x16x32_bf16 v[124:127], v[136:139], v[176:179], v[124:127]
	v_mfma_f32_16x16x32_bf16 v[128:131], v[144:147], v[176:179], v[128:131]
	v_mfma_f32_16x16x32_bf16 v[112:115], v[136:139], v[184:187], v[112:115]
	v_mfma_f32_16x16x32_bf16 v[108:111], v[144:147], v[184:187], v[108:111]
	v_mfma_f32_16x16x32_bf16 v[92:95], v[136:139], v[192:195], v[92:95]
	v_mfma_f32_16x16x32_bf16 v[88:91], v[144:147], v[192:195], v[88:91]
	s_waitcnt lgkmcnt(0)
	v_mfma_f32_16x16x32_bf16 v[76:79], v[136:139], v[200:203], v[76:79]
	v_mfma_f32_16x16x32_bf16 v[72:75], v[144:147], v[200:203], v[72:75]
	s_setprio 0
	s_setprio 1
	v_mfma_f32_16x16x32_bf16 v[120:123], v[148:151], v[172:175], v[120:123]
	v_mfma_f32_16x16x32_bf16 v[116:119], v[156:159], v[172:175], v[116:119]
	v_mfma_f32_16x16x32_bf16 v[104:107], v[148:151], v[180:183], v[104:107]
	v_mfma_f32_16x16x32_bf16 v[98:101], v[156:159], v[180:183], v[100:103]
	v_mfma_f32_16x16x32_bf16 v[84:87], v[148:151], v[188:191], v[84:87]
	v_mfma_f32_16x16x32_bf16 v[80:83], v[156:159], v[188:191], v[80:83]
	v_mfma_f32_16x16x32_bf16 v[68:71], v[148:151], v[196:199], v[68:71]
	v_mfma_f32_16x16x32_bf16 v[64:67], v[156:159], v[196:199], v[64:67]
	v_mfma_f32_16x16x32_bf16 v[120:123], v[152:155], v[176:179], v[120:123]
	v_mfma_f32_16x16x32_bf16 v[116:119], v[160:163], v[176:179], v[116:119]
	v_mfma_f32_16x16x32_bf16 v[104:107], v[152:155], v[184:187], v[104:107]
	v_mfma_f32_16x16x32_bf16 v[98:101], v[160:163], v[184:187], v[98:101]
	v_mfma_f32_16x16x32_bf16 v[84:87], v[152:155], v[192:195], v[84:87]
	v_mfma_f32_16x16x32_bf16 v[80:83], v[160:163], v[192:195], v[80:83]
	v_mfma_f32_16x16x32_bf16 v[68:71], v[152:155], v[200:203], v[68:71]
	v_mfma_f32_16x16x32_bf16 v[64:67], v[160:163], v[200:203], v[64:67]
	s_setprio 0
	s_barrier
	v_xor_b32_e32 v203, 64, v171
	ds_read_b128 v[172:175], v171 offset:16384
	ds_read_b128 v[176:179], v203 offset:16384
	ds_read_b128 v[180:183], v171 offset:18432
	ds_read_b128 v[184:187], v203 offset:18432
	ds_read_b128 v[188:191], v171 offset:20480
	ds_read_b128 v[192:195], v203 offset:20480
	ds_read_b128 v[196:199], v171 offset:22528
	ds_read_b128 v[200:203], v203 offset:22528
	s_mov_b32 m0, s39
	s_nop 0
	global_load_lds_dwordx4 v165, s[26:27]
	s_nop 0
	s_mov_b32 m0, s40
	s_nop 0
	global_load_lds_dwordx4 v167, s[26:27]
	s_add_u32 s72, s26, s6
	s_addc_u32 s73, s27, s7
	s_mov_b32 m0, s41
	s_nop 0
	global_load_lds_dwordx4 v165, s[72:73]
	s_nop 0
	s_mov_b32 m0, s42
	s_nop 0
	global_load_lds_dwordx4 v167, s[72:73]
	s_mov_b32 m0, s38
	s_nop 0
	global_load_lds_dwordx4 v164, s[28:29]
	s_nop 0
	s_mov_b32 m0, s43
	s_nop 0
	global_load_lds_dwordx4 v166, s[28:29]
	s_waitcnt vmcnt(8)
	s_waitcnt lgkmcnt(0)
	s_barrier
	s_setprio 1
	s_waitcnt lgkmcnt(7)
	v_mfma_f32_16x16x32_bf16 v[60:63], v[132:135], v[172:175], v[60:63]
	v_mfma_f32_16x16x32_bf16 v[56:59], v[140:143], v[172:175], v[56:59]
	s_waitcnt lgkmcnt(5)
	v_mfma_f32_16x16x32_bf16 v[44:47], v[132:135], v[180:183], v[44:47]
	v_mfma_f32_16x16x32_bf16 v[40:43], v[140:143], v[180:183], v[40:43]
	s_waitcnt lgkmcnt(3)
	v_mfma_f32_16x16x32_bf16 v[28:31], v[132:135], v[188:191], v[28:31]
	v_mfma_f32_16x16x32_bf16 v[24:27], v[140:143], v[188:191], v[24:27]
	s_waitcnt lgkmcnt(1)
	v_mfma_f32_16x16x32_bf16 v[12:15], v[132:135], v[196:199], v[12:15]
	v_mfma_f32_16x16x32_bf16 v[8:11], v[140:143], v[196:199], v[8:11]
	v_mfma_f32_16x16x32_bf16 v[60:63], v[136:139], v[176:179], v[60:63]
	v_mfma_f32_16x16x32_bf16 v[56:59], v[144:147], v[176:179], v[56:59]
	v_mfma_f32_16x16x32_bf16 v[44:47], v[136:139], v[184:187], v[44:47]
	v_mfma_f32_16x16x32_bf16 v[40:43], v[144:147], v[184:187], v[40:43]
	v_mfma_f32_16x16x32_bf16 v[28:31], v[136:139], v[192:195], v[28:31]
	v_mfma_f32_16x16x32_bf16 v[24:27], v[144:147], v[192:195], v[24:27]
	s_waitcnt lgkmcnt(0)
	v_mfma_f32_16x16x32_bf16 v[12:15], v[136:139], v[200:203], v[12:15]
	v_mfma_f32_16x16x32_bf16 v[8:11], v[144:147], v[200:203], v[8:11]
	s_setprio 0
	s_setprio 1
	v_mfma_f32_16x16x32_bf16 v[52:55], v[148:151], v[172:175], v[52:55]
	v_mfma_f32_16x16x32_bf16 v[48:51], v[156:159], v[172:175], v[48:51]
	v_mfma_f32_16x16x32_bf16 v[36:39], v[148:151], v[180:183], v[36:39]
	v_mfma_f32_16x16x32_bf16 v[32:35], v[156:159], v[180:183], v[32:35]
	v_mfma_f32_16x16x32_bf16 v[20:23], v[148:151], v[188:191], v[20:23]
	v_mfma_f32_16x16x32_bf16 v[16:19], v[156:159], v[188:191], v[16:19]
	v_mfma_f32_16x16x32_bf16 v[4:7], v[148:151], v[196:199], v[4:7]
	v_mfma_f32_16x16x32_bf16 v[0:3], v[156:159], v[196:199], v[0:3]
	v_mfma_f32_16x16x32_bf16 v[52:55], v[152:155], v[176:179], v[52:55]
	v_mfma_f32_16x16x32_bf16 v[48:51], v[160:163], v[176:179], v[48:51]
	v_mfma_f32_16x16x32_bf16 v[36:39], v[152:155], v[184:187], v[36:39]
	v_mfma_f32_16x16x32_bf16 v[32:35], v[160:163], v[184:187], v[32:35]
	v_mfma_f32_16x16x32_bf16 v[20:23], v[152:155], v[192:195], v[20:23]
	v_mfma_f32_16x16x32_bf16 v[16:19], v[160:163], v[192:195], v[16:19]
	v_mfma_f32_16x16x32_bf16 v[4:7], v[152:155], v[200:203], v[4:7]
	v_mfma_f32_16x16x32_bf16 v[0:3], v[160:163], v[200:203], v[0:3]
	s_setprio 0
	s_barrier
	v_add_u32_e32 v96, 0x18000, v170
	v_xor_b32_e32 v147, 64, v96
	ds_read_b128 v[132:135], v96
	ds_read_b128 v[136:139], v147
	ds_read_b128 v[140:143], v96 offset:2048
	ds_read_b128 v[144:147], v147 offset:2048
	v_add_u32_e32 v96, 0x1c000, v170
	v_xor_b32_e32 v163, 64, v96
	ds_read_b128 v[148:151], v96
	ds_read_b128 v[152:155], v163
	ds_read_b128 v[156:159], v96 offset:2048
	ds_read_b128 v[160:163], v163 offset:2048
	v_xor_b32_e32 v203, 64, v171
	ds_read_b128 v[172:175], v171 offset:32768
	ds_read_b128 v[176:179], v203 offset:32768
	ds_read_b128 v[180:183], v171 offset:34816
	ds_read_b128 v[184:187], v203 offset:34816
	ds_read_b128 v[188:191], v171 offset:36864
	ds_read_b128 v[192:195], v203 offset:36864
	ds_read_b128 v[196:199], v171 offset:38912
	ds_read_b128 v[200:203], v203 offset:38912
	s_add_u32 s28, s28, s6
	s_addc_u32 s29, s29, s7
	s_mov_b32 m0, s44
	s_nop 0
	global_load_lds_dwordx4 v164, s[28:29]
	s_nop 0
	s_mov_b32 m0, s45
	s_nop 0
	global_load_lds_dwordx4 v166, s[28:29]
	s_waitcnt vmcnt(8)
	s_waitcnt lgkmcnt(0)
	s_barrier
	s_setprio 1
	s_waitcnt lgkmcnt(7)
	v_mfma_f32_16x16x32_bf16 v[124:127], v[132:135], v[172:175], v[124:127]
	v_mfma_f32_16x16x32_bf16 v[128:131], v[140:143], v[172:175], v[128:131]
	s_waitcnt lgkmcnt(5)
	v_mfma_f32_16x16x32_bf16 v[112:115], v[132:135], v[180:183], v[112:115]
	v_mfma_f32_16x16x32_bf16 v[108:111], v[140:143], v[180:183], v[108:111]
	s_waitcnt lgkmcnt(3)
	v_mfma_f32_16x16x32_bf16 v[92:95], v[132:135], v[188:191], v[92:95]
	v_mfma_f32_16x16x32_bf16 v[88:91], v[140:143], v[188:191], v[88:91]
	s_waitcnt lgkmcnt(1)
	v_mfma_f32_16x16x32_bf16 v[76:79], v[132:135], v[196:199], v[76:79]
	v_mfma_f32_16x16x32_bf16 v[72:75], v[140:143], v[196:199], v[72:75]
	v_mfma_f32_16x16x32_bf16 v[124:127], v[136:139], v[176:179], v[124:127]
	v_mfma_f32_16x16x32_bf16 v[128:131], v[144:147], v[176:179], v[128:131]
	v_mfma_f32_16x16x32_bf16 v[112:115], v[136:139], v[184:187], v[112:115]
	v_mfma_f32_16x16x32_bf16 v[108:111], v[144:147], v[184:187], v[108:111]
	v_mfma_f32_16x16x32_bf16 v[92:95], v[136:139], v[192:195], v[92:95]
	v_mfma_f32_16x16x32_bf16 v[88:91], v[144:147], v[192:195], v[88:91]
	s_waitcnt lgkmcnt(0)
	v_mfma_f32_16x16x32_bf16 v[76:79], v[136:139], v[200:203], v[76:79]
	v_mfma_f32_16x16x32_bf16 v[72:75], v[144:147], v[200:203], v[72:75]
	s_setprio 0
	s_setprio 1
	v_mfma_f32_16x16x32_bf16 v[120:123], v[148:151], v[172:175], v[120:123]
	v_mfma_f32_16x16x32_bf16 v[116:119], v[156:159], v[172:175], v[116:119]
	v_mfma_f32_16x16x32_bf16 v[102:105], v[148:151], v[180:183], v[104:107]
	v_mfma_f32_16x16x32_bf16 v[98:101], v[156:159], v[180:183], v[98:101]
	v_mfma_f32_16x16x32_bf16 v[84:87], v[148:151], v[188:191], v[84:87]
	v_mfma_f32_16x16x32_bf16 v[80:83], v[156:159], v[188:191], v[80:83]
	v_mfma_f32_16x16x32_bf16 v[68:71], v[148:151], v[196:199], v[68:71]
	v_mfma_f32_16x16x32_bf16 v[64:67], v[156:159], v[196:199], v[64:67]
	v_mfma_f32_16x16x32_bf16 v[120:123], v[152:155], v[176:179], v[120:123]
	v_mfma_f32_16x16x32_bf16 v[116:119], v[160:163], v[176:179], v[116:119]
	v_mfma_f32_16x16x32_bf16 v[104:107], v[152:155], v[184:187], v[102:105]
	v_mfma_f32_16x16x32_bf16 v[100:103], v[160:163], v[184:187], v[98:101]
	v_mfma_f32_16x16x32_bf16 v[84:87], v[152:155], v[192:195], v[84:87]
	v_mfma_f32_16x16x32_bf16 v[80:83], v[160:163], v[192:195], v[80:83]
	v_mfma_f32_16x16x32_bf16 v[68:71], v[152:155], v[200:203], v[68:71]
	v_mfma_f32_16x16x32_bf16 v[64:67], v[160:163], v[200:203], v[64:67]
	s_setprio 0
	s_barrier
	v_xor_b32_e32 v203, 64, v171
	ds_read_b128 v[172:175], v171 offset:49152
	ds_read_b128 v[176:179], v203 offset:49152
	ds_read_b128 v[180:183], v171 offset:51200
	ds_read_b128 v[184:187], v203 offset:51200
	ds_read_b128 v[188:191], v171 offset:53248
	ds_read_b128 v[192:195], v203 offset:53248
	ds_read_b128 v[196:199], v171 offset:55296
	ds_read_b128 v[200:203], v203 offset:55296
	s_add_u32 s26, s26, 0x80
	s_addc_u32 s27, s27, 0
	s_mov_b32 m0, s51
	s_nop 0
	global_load_lds_dwordx4 v165, s[26:27]
	s_nop 0
	s_mov_b32 m0, s52
	s_nop 0
	global_load_lds_dwordx4 v167, s[26:27]
	s_add_u32 s26, s26, s6
	s_addc_u32 s27, s27, s7
	s_mov_b32 m0, s55
	s_nop 0
	global_load_lds_dwordx4 v165, s[26:27]
	s_nop 0
	s_mov_b32 m0, s56
	s_nop 0
	global_load_lds_dwordx4 v167, s[26:27]
	s_mov_b32 m0, s53
	s_nop 0
	global_load_lds_dwordx4 v164, s[24:25]
	s_nop 0
	s_mov_b32 m0, s54
	s_nop 0
	global_load_lds_dwordx4 v166, s[24:25]
	s_waitcnt vmcnt(8)
	s_waitcnt lgkmcnt(0)
	s_barrier
	s_setprio 1
	s_waitcnt lgkmcnt(7)
	v_mfma_f32_16x16x32_bf16 v[60:63], v[132:135], v[172:175], v[60:63]
	v_mfma_f32_16x16x32_bf16 v[56:59], v[140:143], v[172:175], v[56:59]
	s_waitcnt lgkmcnt(5)
	v_mfma_f32_16x16x32_bf16 v[44:47], v[132:135], v[180:183], v[44:47]
	v_mfma_f32_16x16x32_bf16 v[40:43], v[140:143], v[180:183], v[40:43]
	s_waitcnt lgkmcnt(3)
	v_mfma_f32_16x16x32_bf16 v[28:31], v[132:135], v[188:191], v[28:31]
	v_mfma_f32_16x16x32_bf16 v[24:27], v[140:143], v[188:191], v[24:27]
	s_waitcnt lgkmcnt(1)
	v_mfma_f32_16x16x32_bf16 v[12:15], v[132:135], v[196:199], v[12:15]
	v_mfma_f32_16x16x32_bf16 v[8:11], v[140:143], v[196:199], v[8:11]
	v_mfma_f32_16x16x32_bf16 v[60:63], v[136:139], v[176:179], v[60:63]
	v_mfma_f32_16x16x32_bf16 v[56:59], v[144:147], v[176:179], v[56:59]
	v_mfma_f32_16x16x32_bf16 v[44:47], v[136:139], v[184:187], v[44:47]
	v_mfma_f32_16x16x32_bf16 v[40:43], v[144:147], v[184:187], v[40:43]
	v_mfma_f32_16x16x32_bf16 v[28:31], v[136:139], v[192:195], v[28:31]
	v_mfma_f32_16x16x32_bf16 v[24:27], v[144:147], v[192:195], v[24:27]
	s_waitcnt lgkmcnt(0)
	v_mfma_f32_16x16x32_bf16 v[12:15], v[136:139], v[200:203], v[12:15]
	v_mfma_f32_16x16x32_bf16 v[8:11], v[144:147], v[200:203], v[8:11]
	s_setprio 0
	s_setprio 1
	v_mfma_f32_16x16x32_bf16 v[52:55], v[148:151], v[172:175], v[52:55]
	v_mfma_f32_16x16x32_bf16 v[48:51], v[156:159], v[172:175], v[48:51]
	v_mfma_f32_16x16x32_bf16 v[36:39], v[148:151], v[180:183], v[36:39]
	v_mfma_f32_16x16x32_bf16 v[32:35], v[156:159], v[180:183], v[32:35]
	v_mfma_f32_16x16x32_bf16 v[20:23], v[148:151], v[188:191], v[20:23]
	v_mfma_f32_16x16x32_bf16 v[16:19], v[156:159], v[188:191], v[16:19]
	v_mfma_f32_16x16x32_bf16 v[4:7], v[148:151], v[196:199], v[4:7]
	v_mfma_f32_16x16x32_bf16 v[0:3], v[156:159], v[196:199], v[0:3]
	v_mfma_f32_16x16x32_bf16 v[52:55], v[152:155], v[176:179], v[52:55]
	v_mfma_f32_16x16x32_bf16 v[48:51], v[160:163], v[176:179], v[48:51]
	v_mfma_f32_16x16x32_bf16 v[36:39], v[152:155], v[184:187], v[36:39]
	v_mfma_f32_16x16x32_bf16 v[32:35], v[160:163], v[184:187], v[32:35]
	v_mfma_f32_16x16x32_bf16 v[20:23], v[152:155], v[192:195], v[20:23]
	v_mfma_f32_16x16x32_bf16 v[16:19], v[160:163], v[192:195], v[16:19]
	v_mfma_f32_16x16x32_bf16 v[4:7], v[152:155], v[200:203], v[4:7]
	v_mfma_f32_16x16x32_bf16 v[0:3], v[160:163], v[200:203], v[0:3]
	s_setprio 0
	s_barrier
	s_add_u32 s67, s67, 0x100
	s_addc_u32 s68, s68, 0
	s_add_u32 s69, s69, 0x100
	s_addc_u32 s70, s70, 0
	s_add_u32 s22, s22, 0x100
	s_addc_u32 s23, s23, 0
	s_cmp_ge_i32 s71, s48
	s_cbranch_scc1 .LBB0_1161
	s_mov_b32 s28, s71
	s_cmp_lt_i32 s28, 8
	s_cbranch_scc1 .LBB0_1154

.LBB0_1221:
	s_andn2_b64 vcc, exec, s[2:3]
	s_cbranch_vccnz .LBB0_1337
	v_readlane_b32 s8, v252, 0
	v_readlane_b32 s9, v252, 1
	s_waitcnt vmcnt(0) expcnt(0) lgkmcnt(0)
	v_mbcnt_lo_u32_b32 v0, -1, 0
	v_mbcnt_hi_u32_b32 v0, -1, v0
	s_and_b64 vcc, exec, s[36:37]
	v_add_u32_e32 v0, s93, v0
	s_nop 0
	s_nop 0
	v_readfirstlane_b32 s24, v0
	s_cbranch_vccnz .LBB0_1284
	v_bfe_i32 v3, v0, 27, 1
	v_lshlrev_b32_e32 v1, 4, v0
	v_lshrrev_b32_e32 v3, 22, v3
	v_add_u32_e32 v3, v1, v3
	v_and_b32_e32 v3, 0xfffffc00, v3
	v_sub_u32_e32 v3, v1, v3
	v_ashrrev_i32_e32 v2, 31, v0
	v_lshrrev_b32_e32 v4, 4, v3
	v_lshrrev_b32_e32 v2, 26, v2
	v_bitop3_b32 v3, v4, v3, 32 bitop3:0x6c
	v_add_u32_e32 v2, v0, v2
	v_ashrrev_i32_e32 v5, 31, v3
	v_ashrrev_i32_e32 v2, 6, v2
	v_lshrrev_b32_e32 v5, 26, v5
	v_lshlrev_b32_e32 v4, 3, v2
	v_add_u32_e32 v5, v3, v5
	v_and_b32_e32 v4, -16, v4
	v_ashrrev_i32_e32 v6, 6, v5
	v_and_b32_e32 v5, 0xc0, v5
	v_add_u32_e32 v4, v6, v4
	v_sub_u32_e32 v3, v3, v5
	v_lshlrev_b32_e32 v2, 5, v2
	v_ashrrev_i16_sdwa v3, v239, sext(v3) dst_sel:DWORD dst_unused:UNUSED_PAD src0_sel:DWORD src1_sel:BYTE_0
	v_lshlrev_b32_e32 v5, 1, v4
	v_lshlrev_b32_e32 v7, 2, v4
	v_lshrrev_b32_e32 v8, 2, v4
	v_and_b32_e32 v6, 3, v6
	v_and_b32_e32 v2, 32, v2
	v_bfe_i32 v3, v3, 0, 16
	v_and_b32_e32 v5, 0x1fffc0, v5
	v_and_b32_e32 v8, 4, v8
	v_and_or_b32 v6, v7, 48, v6
	v_or3_b32 v5, v6, v5, v8
	v_add_lshl_u32 v2, v2, v3, 1
	v_add_u32_e32 v1, 0x2000, v1
	v_lshl_add_u32 v96, v4, 11, v2
	v_mbcnt_lo_u32_b32 v134, -1, 0
	v_mbcnt_hi_u32_b32 v134, -1, v134
	v_add_u32_e32 v134, s93, v134
	v_lshrrev_b32_e32 v135, 3, v134
	v_lshrrev_b32_e32 v136, 4, v134
	v_xor_b32_e32 v136, v136, v134
	v_lshlrev_b32_e32 v136, 4, v136
	v_and_b32_e32 v136, 0x70, v136
	v_lshl_add_u32 v96, v135, 11, v136
	v_lshl_add_u32 v244, v5, 11, v2
	v_mbcnt_lo_u32_b32 v134, -1, 0
	v_mbcnt_hi_u32_b32 v134, -1, v134
	v_add_u32_e32 v134, s93, v134
	v_lshrrev_b32_e32 v135, 3, v134
	v_and_b32_e32 v136, 0x60, v135
	v_lshlrev_b32_e32 v136, 1, v136
	v_and_or_b32 v136, v135, 3, v136
	v_and_b32_e32 v244, 12, v135
	v_lshl_or_b32 v136, v244, 2, v136
	v_lshrrev_b32_e32 v135, 2, v135
	v_and_b32_e32 v135, 4, v135
	v_or_b32_e32 v135, v135, v136
	v_lshrrev_b32_e32 v136, 4, v134
	v_xor_b32_e32 v136, v136, v134
	v_lshlrev_b32_e32 v136, 4, v136
	v_and_b32_e32 v136, 0x70, v136
	v_lshl_add_u32 v244, v135, 11, v136
	v_ashrrev_i32_e32 v2, 31, v1
	s_load_dwordx2 s[2:3], s[8:9], 0x98
	v_lshrrev_b32_e32 v2, 22, v2
	v_add_u32_e32 v2, v1, v2
	v_ashrrev_i32_e32 v2, 10, v2
	v_mul_i32_i24_e32 v3, 0x400, v2
	s_lshl_b32 s4, s44, 21
	v_sub_u32_e32 v1, v1, v3
	s_waitcnt lgkmcnt(0)
	s_add_u32 s4, s2, s4
	v_lshrrev_b32_e32 v3, 4, v1
	s_addc_u32 s5, s3, 0
	v_bitop3_b32 v1, v3, v1, 32 bitop3:0x6c
	s_add_u32 s46, s4, 0x3300000
	v_ashrrev_i32_e32 v4, 31, v1
	s_addc_u32 s47, s5, 0
	v_lshrrev_b32_e32 v4, 26, v4
	s_add_u32 s48, s2, 0x48500000
	v_lshlrev_b32_e32 v3, 3, v2
	v_add_u32_e32 v4, v1, v4
	s_addc_u32 s49, s3, 0
	s_ashr_i32 s25, s24, 6
	v_and_b32_e32 v3, -16, v3
	v_ashrrev_i32_e32 v5, 6, v4
	v_and_b32_e32 v4, 0xc0, v4
	s_load_dwordx4 s[4:7], s[8:9], 0x40
	v_add_u32_e32 v3, v5, v3
	v_sub_u32_e32 v1, v1, v4
	s_ashr_i32 s26, s24, 8
	s_lshl_b32 s50, s25, 10
	v_readlane_b32 s8, v253, 37
	v_lshlrev_b32_e32 v2, 5, v2
	v_ashrrev_i16_sdwa v1, v239, sext(v1) dst_sel:DWORD dst_unused:UNUSED_PAD src0_sel:DWORD src1_sel:BYTE_0
	v_lshlrev_b32_e32 v4, 1, v3
	v_lshlrev_b32_e32 v6, 2, v3
	v_lshrrev_b32_e32 v7, 2, v3
	v_and_b32_e32 v5, 3, v5
	v_readlane_b32 s9, v253, 38
	s_add_u32 s40, s46, s8
	v_and_b32_e32 v2, 32, v2
	v_bfe_i32 v1, v1, 0, 16
	v_and_b32_e32 v4, 0x1fffc0, v4
	v_and_b32_e32 v7, 4, v7
	v_and_or_b32 v5, v6, 48, v5
	s_addc_u32 s41, s47, s9
	s_add_i32 s50, s50, 0
	v_or3_b32 v4, v5, v4, v7
	v_add_lshl_u32 v1, v2, v1, 1
	s_add_i32 s51, s50, 0x10000
	s_mov_b32 m0, s51
	s_nop 0
	global_load_lds_dwordx4 v244, s[40:41]
	v_lshl_add_u32 v246, v4, 11, v1
	v_mbcnt_lo_u32_b32 v134, -1, 0
	v_mbcnt_hi_u32_b32 v134, -1, v134
	v_add_u32_e32 v134, s93, v134
	v_lshrrev_b32_e32 v135, 3, v134
	v_add_u32_e32 v135, 64, v135
	v_and_b32_e32 v136, 0x60, v135
	v_lshlrev_b32_e32 v136, 1, v136
	v_and_or_b32 v136, v135, 3, v136
	v_and_b32_e32 v246, 12, v135
	v_lshl_or_b32 v136, v246, 2, v136
	v_lshrrev_b32_e32 v135, 2, v135
	v_and_b32_e32 v135, 4, v135
	v_or_b32_e32 v135, v135, v136
	v_lshrrev_b32_e32 v136, 4, v134
	v_xor_b32_e32 v136, v136, v134
	v_lshlrev_b32_e32 v136, 4, v136
	v_and_b32_e32 v136, 0x70, v136
	v_lshl_add_u32 v246, v135, 11, v136
	s_add_i32 s52, s50, 0x12000
	s_mov_b32 m0, s52
	s_nop 0
	global_load_lds_dwordx4 v246, s[40:41]
	s_add_u32 s8, s40, 0x4000
	s_addc_u32 s9, s41, 0
	s_add_i32 s53, s50, 0x14000
	s_mov_b32 m0, s53
	s_nop 0
	global_load_lds_dwordx4 v244, s[8:9]
	s_add_i32 s54, s50, 0x16000
	s_mov_b32 m0, s54
	s_nop 0
	global_load_lds_dwordx4 v246, s[8:9]
	v_readlane_b32 s8, v253, 33
	v_readlane_b32 s9, v253, 34
	s_add_u32 s38, s48, s8
	s_addc_u32 s39, s49, s9
	s_mov_b32 m0, s50
	s_nop 0
	global_load_lds_dwordx4 v96, s[38:39]
	v_lshl_add_u32 v245, v3, 11, v1
	v_mbcnt_lo_u32_b32 v134, -1, 0
	v_mbcnt_hi_u32_b32 v134, -1, v134
	v_add_u32_e32 v134, s93, v134
	v_lshrrev_b32_e32 v135, 3, v134
	v_add_u32_e32 v135, 64, v135
	v_lshrrev_b32_e32 v136, 4, v134
	v_xor_b32_e32 v136, v136, v134
	v_lshlrev_b32_e32 v136, 4, v136
	v_and_b32_e32 v136, 0x70, v136
	v_lshl_add_u32 v245, v135, 11, v136
	s_add_i32 s55, s50, 0x2000
	s_mov_b32 m0, s55
	s_nop 0
	global_load_lds_dwordx4 v245, s[38:39]
	s_add_u32 s8, s38, 0x40000
	s_addc_u32 s9, s39, 0
	s_add_i32 s56, s50, 0x4000
	s_mov_b32 m0, s56
	s_nop 0
	global_load_lds_dwordx4 v96, s[8:9]
	s_add_i32 s57, s50, 0x6000
	s_mov_b32 m0, s57
	s_nop 0
	global_load_lds_dwordx4 v245, s[8:9]
	s_cmp_eq_u32 s26, 1
	s_cselect_b64 s[8:9], -1, 0
	s_cmp_lg_u32 s26, 1
	s_cbranch_scc1 .LBB0_1225
	s_barrier
.LBB0_1225:
	s_add_u32 s10, s2, 0x33b00000
	s_addc_u32 s11, s3, 0
	s_add_u32 s12, s2, 0x35b00000
	s_addc_u32 s13, s3, 0
	s_add_u32 s14, s2, 0x69100000
	s_addc_u32 s15, s3, 0
	s_lshl_b32 s86, s44, 10
	s_lshl_b64 s[18:19], s[86:87], 2
	s_waitcnt lgkmcnt(0)
	s_add_u32 s16, s4, s18
	s_addc_u32 s17, s5, s19
	s_add_u32 s18, s6, s18
	s_addc_u32 s19, s7, s19
	s_add_u32 s20, s2, 0x4a500000
	s_addc_u32 s21, s3, 0
	s_lshl_b32 s86, s44, 12
	s_lshl_b64 s[4:5], s[86:87], 2
	s_add_u32 s4, s2, s4
	s_addc_u32 s5, s3, s5
	s_add_u32 s58, s4, 0x40000
	s_addc_u32 s59, s5, 0
	v_bfe_u32 v248, v0, 4, 2
	s_add_u32 s22, s2, 0x3ff00
	v_and_b32_e32 v247, 15, v0
	v_lshlrev_b32_e32 v1, 4, v248
	v_lshlrev_b32_e32 v0, 2, v0
	s_addc_u32 s23, s3, 0
	s_and_b32 s4, s25, 3
	v_lshl_or_b32 v1, v247, 6, v1
	s_lshl_b32 s2, s26, 13
	v_and_b32_e32 v0, 32, v0
	s_lshl_b32 s60, s26, 6
	v_bitop3_b32 v2, v1, s2, v0 bitop3:0xde
	s_lshl_b32 s2, s4, 12
	v_bitop3_b32 v0, v1, s2, v0 bitop3:0xde
	s_add_u32 s2, s40, 0x80
	s_waitcnt vmcnt(2)
	s_barrier
	s_addc_u32 s3, s41, 0
	s_add_i32 s61, s50, 0x18000
	s_mov_b32 m0, s61
	s_nop 0
	global_load_lds_dwordx4 v244, s[2:3]
	s_add_i32 s62, s50, 0x1a000
	s_mov_b32 m0, s62
	s_nop 0
	global_load_lds_dwordx4 v246, s[2:3]
	s_add_u32 s2, s38, 0x80
	s_addc_u32 s3, s39, 0
	s_add_i32 s63, s50, 0x8000
	s_mov_b32 m0, s63
	s_nop 0
	global_load_lds_dwordx4 v96, s[2:3]
	s_add_i32 s64, s50, 0xa000
	s_mov_b32 m0, s64
	s_nop 0
	global_load_lds_dwordx4 v245, s[2:3]
	s_add_u32 s2, s40, 0x4080
	s_addc_u32 s3, s41, 0
	s_add_i32 s65, s50, 0x1c000
	s_add_i32 s66, s50, 0x1e000
	s_add_i32 s67, s50, 0xc000
	s_mov_b32 m0, s65
	s_nop 0
	global_load_lds_dwordx4 v244, s[2:3]
	s_cmpk_lt_u32 s24, 0x100
	s_mov_b32 m0, s66
	s_nop 0
	global_load_lds_dwordx4 v246, s[2:3]
	s_cselect_b64 s[24:25], -1, 0
	s_lshl_b32 s2, s26, 2
	s_or_b32 s2, s2, s4
	s_lshl_b32 s68, s4, 6
	s_lshl_b32 s69, s2, 5
	s_cmp_eq_u32 s2, 0
	s_waitcnt vmcnt(6)
	s_cselect_b64 s[26:27], -1, 0
	s_lshl_b32 s2, s4, 3
	s_add_i32 s71, s2, 0
	v_readlane_b32 s2, v253, 20
	s_mov_b32 s70, 0
	s_add_i32 s71, s71, 0x22000
	v_add_u32_e32 v249, 0, v0
	v_mbcnt_lo_u32_b32 v134, -1, 0
	v_mbcnt_hi_u32_b32 v134, -1, v134
	v_add_u32_e32 v134, s93, v134
	v_bfe_u32 v135, v134, 4, 2
	v_bfe_u32 v136, v134, 1, 3
	v_xor_b32_e32 v135, v135, v136
	v_lshlrev_b32_e32 v135, 4, v135
	v_and_b32_e32 v136, 15, v134
	v_lshl_or_b32 v135, v136, 7, v135
	v_bfe_u32 v136, v134, 6, 2
	v_lshl_or_b32 v249, v136, 12, v135
	v_add_u32_e32 v250, 0, v2
	v_mbcnt_lo_u32_b32 v134, -1, 0
	v_mbcnt_hi_u32_b32 v134, -1, v134
	v_add_u32_e32 v134, s93, v134
	v_bfe_u32 v135, v134, 4, 2
	v_bfe_u32 v136, v134, 1, 3
	v_xor_b32_e32 v135, v135, v136
	v_lshlrev_b32_e32 v135, 4, v135
	v_and_b32_e32 v136, 15, v134
	v_lshl_or_b32 v135, v136, 7, v135
	v_lshrrev_b32_e32 v136, 8, v134
	v_lshl_or_b32 v250, v136, 13, v135
	s_mov_b32 s4, s2
	v_readlane_b32 s44, v253, 19
	s_barrier
	s_branch .LBB0_1228

.LBB0_1237:
	v_add_u32_e32 v142, 0x10000, v249
	v_add_u32_e32 v158, 0x14000, v249
	v_xor_b32_e32 v145, 64, v142
	ds_read_b128 v[130:133], v142
	ds_read_b128 v[134:137], v145
	ds_read_b128 v[138:141], v142 offset:2048
	ds_read_b128 v[142:145], v145 offset:2048
	v_xor_b32_e32 v161, 64, v158
	ds_read_b128 v[146:149], v158
	ds_read_b128 v[150:153], v161
	ds_read_b128 v[154:157], v158 offset:2048
	ds_read_b128 v[158:161], v161 offset:2048
	s_add_u32 s2, s38, 0x100
	s_addc_u32 s3, s39, 0
	s_cmp_eq_u32 s45, 12
	s_cselect_b32 s42, s34, s2
	s_cselect_b32 s43, s35, s3
	s_cselect_b32 s40, s30, s5
	s_cselect_b32 s41, s31, s29
	s_add_u32 s6, s42, 0x80
	s_addc_u32 s7, s43, 0
	v_xor_b32_e32 v193, 64, v250
	ds_read_b128 v[162:165], v250
	ds_read_b128 v[166:169], v193
	ds_read_b128 v[170:173], v250 offset:2048
	ds_read_b128 v[174:177], v193 offset:2048
	ds_read_b128 v[178:181], v250 offset:4096
	ds_read_b128 v[182:185], v193 offset:4096
	ds_read_b128 v[186:189], v250 offset:6144
	ds_read_b128 v[190:193], v193 offset:6144
	s_add_u32 s38, s38, 0x40080
	s_addc_u32 s39, s39, 0
	s_mov_b32 m0, s67
	s_nop 0
	global_load_lds_dwordx4 v96, s[38:39]
	s_add_i32 s73, s50, 0xe000
	s_mov_b32 m0, s73
	s_nop 0
	global_load_lds_dwordx4 v245, s[38:39]
	s_waitcnt vmcnt(8)
	s_waitcnt lgkmcnt(0)
	s_barrier
	s_setprio 1
	s_waitcnt lgkmcnt(7)
	v_mfma_f32_16x16x32_bf16 v[126:129], v[130:133], v[162:165], v[126:129]
	v_mfma_f32_16x16x32_bf16 v[122:125], v[138:141], v[162:165], v[122:125]
	s_waitcnt lgkmcnt(5)
	v_mfma_f32_16x16x32_bf16 v[110:113], v[130:133], v[170:173], v[110:113]
	v_mfma_f32_16x16x32_bf16 v[106:109], v[138:141], v[170:173], v[106:109]
	s_waitcnt lgkmcnt(3)
	v_mfma_f32_16x16x32_bf16 v[92:95], v[130:133], v[178:181], v[92:95]
	v_mfma_f32_16x16x32_bf16 v[88:91], v[138:141], v[178:181], v[88:91]
	s_waitcnt lgkmcnt(1)
	v_mfma_f32_16x16x32_bf16 v[76:79], v[130:133], v[186:189], v[76:79]
	v_mfma_f32_16x16x32_bf16 v[72:75], v[138:141], v[186:189], v[72:75]
	v_mfma_f32_16x16x32_bf16 v[126:129], v[134:137], v[166:169], v[126:129]
	v_mfma_f32_16x16x32_bf16 v[122:125], v[142:145], v[166:169], v[122:125]
	v_mfma_f32_16x16x32_bf16 v[110:113], v[134:137], v[174:177], v[110:113]
	v_mfma_f32_16x16x32_bf16 v[106:109], v[142:145], v[174:177], v[106:109]
	v_mfma_f32_16x16x32_bf16 v[92:95], v[134:137], v[182:185], v[92:95]
	v_mfma_f32_16x16x32_bf16 v[88:91], v[142:145], v[182:185], v[88:91]
	s_waitcnt lgkmcnt(0)
	v_mfma_f32_16x16x32_bf16 v[76:79], v[134:137], v[190:193], v[76:79]
	v_mfma_f32_16x16x32_bf16 v[72:75], v[142:145], v[190:193], v[72:75]
	s_setprio 0
	s_setprio 1
	v_mfma_f32_16x16x32_bf16 v[118:121], v[146:149], v[162:165], v[118:121]
	v_mfma_f32_16x16x32_bf16 v[114:117], v[154:157], v[162:165], v[114:117]
	v_mfma_f32_16x16x32_bf16 v[102:105], v[146:149], v[170:173], v[102:105]
	v_mfma_f32_16x16x32_bf16 v[98:101], v[154:157], v[170:173], v[98:101]
	v_mfma_f32_16x16x32_bf16 v[84:87], v[146:149], v[178:181], v[84:87]
	v_mfma_f32_16x16x32_bf16 v[80:83], v[154:157], v[178:181], v[80:83]
	v_mfma_f32_16x16x32_bf16 v[68:71], v[146:149], v[186:189], v[68:71]
	v_mfma_f32_16x16x32_bf16 v[64:67], v[154:157], v[186:189], v[64:67]
	v_mfma_f32_16x16x32_bf16 v[118:121], v[150:153], v[166:169], v[118:121]
	v_mfma_f32_16x16x32_bf16 v[114:117], v[158:161], v[166:169], v[114:117]
	v_mfma_f32_16x16x32_bf16 v[102:105], v[150:153], v[174:177], v[102:105]
	v_mfma_f32_16x16x32_bf16 v[98:101], v[158:161], v[174:177], v[98:101]
	v_mfma_f32_16x16x32_bf16 v[84:87], v[150:153], v[182:185], v[84:87]
	v_mfma_f32_16x16x32_bf16 v[80:83], v[158:161], v[182:185], v[80:83]
	v_mfma_f32_16x16x32_bf16 v[68:71], v[150:153], v[190:193], v[68:71]
	v_mfma_f32_16x16x32_bf16 v[64:67], v[158:161], v[190:193], v[64:67]
	s_setprio 0
	s_barrier
	v_xor_b32_e32 v193, 64, v250
	ds_read_b128 v[162:165], v250 offset:16384
	ds_read_b128 v[166:169], v193 offset:16384
	ds_read_b128 v[170:173], v250 offset:18432
	ds_read_b128 v[174:177], v193 offset:18432
	ds_read_b128 v[178:181], v250 offset:20480
	ds_read_b128 v[182:185], v193 offset:20480
	ds_read_b128 v[186:189], v250 offset:22528
	ds_read_b128 v[190:193], v193 offset:22528
	s_mov_b32 m0, s51
	s_nop 0
	global_load_lds_dwordx4 v244, s[40:41]
	s_nop 0
	s_mov_b32 m0, s52
	s_nop 0
	global_load_lds_dwordx4 v246, s[40:41]
	s_add_u32 s38, s40, 0x4000
	s_addc_u32 s39, s41, 0
	s_mov_b32 m0, s53
	s_nop 0
	global_load_lds_dwordx4 v244, s[38:39]
	s_nop 0
	s_mov_b32 m0, s54
	s_nop 0
	global_load_lds_dwordx4 v246, s[38:39]
	s_mov_b32 m0, s50
	s_nop 0
	global_load_lds_dwordx4 v96, s[42:43]
	s_nop 0
	s_mov_b32 m0, s55
	s_nop 0
	global_load_lds_dwordx4 v245, s[42:43]
	s_waitcnt vmcnt(8)
	s_waitcnt lgkmcnt(0)
	s_barrier
	s_setprio 1
	s_waitcnt lgkmcnt(7)
	v_mfma_f32_16x16x32_bf16 v[60:63], v[130:133], v[162:165], v[60:63]
	v_mfma_f32_16x16x32_bf16 v[56:59], v[138:141], v[162:165], v[56:59]
	s_waitcnt lgkmcnt(5)
	v_mfma_f32_16x16x32_bf16 v[44:47], v[130:133], v[170:173], v[44:47]
	v_mfma_f32_16x16x32_bf16 v[40:43], v[138:141], v[170:173], v[40:43]
	s_waitcnt lgkmcnt(3)
	v_mfma_f32_16x16x32_bf16 v[28:31], v[130:133], v[178:181], v[28:31]
	v_mfma_f32_16x16x32_bf16 v[24:27], v[138:141], v[178:181], v[24:27]
	s_waitcnt lgkmcnt(1)
	v_mfma_f32_16x16x32_bf16 v[12:15], v[130:133], v[186:189], v[12:15]
	v_mfma_f32_16x16x32_bf16 v[8:11], v[138:141], v[186:189], v[8:11]
	v_mfma_f32_16x16x32_bf16 v[60:63], v[134:137], v[166:169], v[60:63]
	v_mfma_f32_16x16x32_bf16 v[56:59], v[142:145], v[166:169], v[56:59]
	v_mfma_f32_16x16x32_bf16 v[44:47], v[134:137], v[174:177], v[44:47]
	v_mfma_f32_16x16x32_bf16 v[40:43], v[142:145], v[174:177], v[40:43]
	v_mfma_f32_16x16x32_bf16 v[28:31], v[134:137], v[182:185], v[28:31]
	v_mfma_f32_16x16x32_bf16 v[24:27], v[142:145], v[182:185], v[24:27]
	s_waitcnt lgkmcnt(0)
	v_mfma_f32_16x16x32_bf16 v[12:15], v[134:137], v[190:193], v[12:15]
	v_mfma_f32_16x16x32_bf16 v[8:11], v[142:145], v[190:193], v[8:11]
	s_setprio 0
	s_setprio 1
	v_mfma_f32_16x16x32_bf16 v[52:55], v[146:149], v[162:165], v[52:55]
	v_mfma_f32_16x16x32_bf16 v[48:51], v[154:157], v[162:165], v[48:51]
	v_mfma_f32_16x16x32_bf16 v[36:39], v[146:149], v[170:173], v[36:39]
	v_mfma_f32_16x16x32_bf16 v[32:35], v[154:157], v[170:173], v[32:35]
	v_mfma_f32_16x16x32_bf16 v[20:23], v[146:149], v[178:181], v[20:23]
	v_mfma_f32_16x16x32_bf16 v[16:19], v[154:157], v[178:181], v[16:19]
	v_mfma_f32_16x16x32_bf16 v[4:7], v[146:149], v[186:189], v[4:7]
	v_mfma_f32_16x16x32_bf16 v[0:3], v[154:157], v[186:189], v[0:3]
	v_mfma_f32_16x16x32_bf16 v[52:55], v[150:153], v[166:169], v[52:55]
	v_mfma_f32_16x16x32_bf16 v[48:51], v[158:161], v[166:169], v[48:51]
	v_mfma_f32_16x16x32_bf16 v[36:39], v[150:153], v[174:177], v[36:39]
	v_mfma_f32_16x16x32_bf16 v[32:35], v[158:161], v[174:177], v[32:35]
	v_mfma_f32_16x16x32_bf16 v[20:23], v[150:153], v[182:185], v[20:23]
	v_mfma_f32_16x16x32_bf16 v[16:19], v[158:161], v[182:185], v[16:19]
	v_mfma_f32_16x16x32_bf16 v[4:7], v[150:153], v[190:193], v[4:7]
	v_mfma_f32_16x16x32_bf16 v[0:3], v[158:161], v[190:193], v[0:3]
	s_setprio 0
	s_barrier
	v_add_u32_e32 v142, 0x18000, v249
	v_add_u32_e32 v158, 0x1c000, v249
	v_xor_b32_e32 v145, 64, v142
	ds_read_b128 v[130:133], v142
	ds_read_b128 v[134:137], v145
	ds_read_b128 v[138:141], v142 offset:2048
	ds_read_b128 v[142:145], v145 offset:2048
	v_xor_b32_e32 v161, 64, v158
	ds_read_b128 v[146:149], v158
	ds_read_b128 v[150:153], v161
	ds_read_b128 v[154:157], v158 offset:2048
	ds_read_b128 v[158:161], v161 offset:2048
	v_xor_b32_e32 v193, 64, v250
	ds_read_b128 v[162:165], v250 offset:32768
	ds_read_b128 v[166:169], v193 offset:32768
	ds_read_b128 v[170:173], v250 offset:34816
	ds_read_b128 v[174:177], v193 offset:34816
	ds_read_b128 v[178:181], v250 offset:36864
	ds_read_b128 v[182:185], v193 offset:36864
	ds_read_b128 v[186:189], v250 offset:38912
	ds_read_b128 v[190:193], v193 offset:38912
	s_add_u32 s38, s42, 0x40000
	s_addc_u32 s39, s43, 0
	s_mov_b32 m0, s56
	s_nop 0
	global_load_lds_dwordx4 v96, s[38:39]
	s_nop 0
	s_mov_b32 m0, s57
	s_nop 0
	global_load_lds_dwordx4 v245, s[38:39]
	s_waitcnt vmcnt(8)
	s_waitcnt lgkmcnt(0)
	s_barrier
	s_setprio 1
	s_waitcnt lgkmcnt(7)
	v_mfma_f32_16x16x32_bf16 v[126:129], v[130:133], v[162:165], v[126:129]
	v_mfma_f32_16x16x32_bf16 v[122:125], v[138:141], v[162:165], v[122:125]
	s_waitcnt lgkmcnt(5)
	v_mfma_f32_16x16x32_bf16 v[110:113], v[130:133], v[170:173], v[110:113]
	v_mfma_f32_16x16x32_bf16 v[106:109], v[138:141], v[170:173], v[106:109]
	s_waitcnt lgkmcnt(3)
	v_mfma_f32_16x16x32_bf16 v[92:95], v[130:133], v[178:181], v[92:95]
	v_mfma_f32_16x16x32_bf16 v[88:91], v[138:141], v[178:181], v[88:91]
	s_waitcnt lgkmcnt(1)
	v_mfma_f32_16x16x32_bf16 v[76:79], v[130:133], v[186:189], v[76:79]
	v_mfma_f32_16x16x32_bf16 v[72:75], v[138:141], v[186:189], v[72:75]
	v_mfma_f32_16x16x32_bf16 v[126:129], v[134:137], v[166:169], v[126:129]
	v_mfma_f32_16x16x32_bf16 v[122:125], v[142:145], v[166:169], v[122:125]
	v_mfma_f32_16x16x32_bf16 v[110:113], v[134:137], v[174:177], v[110:113]
	v_mfma_f32_16x16x32_bf16 v[106:109], v[142:145], v[174:177], v[106:109]
	v_mfma_f32_16x16x32_bf16 v[92:95], v[134:137], v[182:185], v[92:95]
	v_mfma_f32_16x16x32_bf16 v[88:91], v[142:145], v[182:185], v[88:91]
	s_waitcnt lgkmcnt(0)
	v_mfma_f32_16x16x32_bf16 v[76:79], v[134:137], v[190:193], v[76:79]
	v_mfma_f32_16x16x32_bf16 v[72:75], v[142:145], v[190:193], v[72:75]
	s_setprio 0
	s_setprio 1
	v_mfma_f32_16x16x32_bf16 v[118:121], v[146:149], v[162:165], v[118:121]
	v_mfma_f32_16x16x32_bf16 v[114:117], v[154:157], v[162:165], v[114:117]
	v_mfma_f32_16x16x32_bf16 v[102:105], v[146:149], v[170:173], v[102:105]
	v_mfma_f32_16x16x32_bf16 v[98:101], v[154:157], v[170:173], v[98:101]
	v_mfma_f32_16x16x32_bf16 v[84:87], v[146:149], v[178:181], v[84:87]
	v_mfma_f32_16x16x32_bf16 v[80:83], v[154:157], v[178:181], v[80:83]
	v_mfma_f32_16x16x32_bf16 v[68:71], v[146:149], v[186:189], v[68:71]
	v_mfma_f32_16x16x32_bf16 v[64:67], v[154:157], v[186:189], v[64:67]
	v_mfma_f32_16x16x32_bf16 v[118:121], v[150:153], v[166:169], v[118:121]
	v_mfma_f32_16x16x32_bf16 v[114:117], v[158:161], v[166:169], v[114:117]
	v_mfma_f32_16x16x32_bf16 v[102:105], v[150:153], v[174:177], v[102:105]
	v_mfma_f32_16x16x32_bf16 v[98:101], v[158:161], v[174:177], v[98:101]
	v_mfma_f32_16x16x32_bf16 v[84:87], v[150:153], v[182:185], v[84:87]
	v_mfma_f32_16x16x32_bf16 v[80:83], v[158:161], v[182:185], v[80:83]
	v_mfma_f32_16x16x32_bf16 v[68:71], v[150:153], v[190:193], v[68:71]
	v_mfma_f32_16x16x32_bf16 v[64:67], v[158:161], v[190:193], v[64:67]
	s_setprio 0
	s_barrier
	v_xor_b32_e32 v193, 64, v250
	ds_read_b128 v[162:165], v250 offset:49152
	ds_read_b128 v[166:169], v193 offset:49152
	ds_read_b128 v[170:173], v250 offset:51200
	ds_read_b128 v[174:177], v193 offset:51200
	ds_read_b128 v[178:181], v250 offset:53248
	ds_read_b128 v[182:185], v193 offset:53248
	ds_read_b128 v[186:189], v250 offset:55296
	ds_read_b128 v[190:193], v193 offset:55296
	s_add_u32 s38, s40, 0x80
	s_addc_u32 s39, s41, 0
	s_mov_b32 m0, s61
	s_nop 0
	global_load_lds_dwordx4 v244, s[38:39]
	s_nop 0
	s_mov_b32 m0, s62
	s_nop 0
	global_load_lds_dwordx4 v246, s[38:39]
	s_add_u32 s38, s40, 0x4080
	s_addc_u32 s39, s41, 0
	s_mov_b32 m0, s65
	s_nop 0
	global_load_lds_dwordx4 v244, s[38:39]
	s_nop 0
	s_mov_b32 m0, s66
	s_nop 0
	global_load_lds_dwordx4 v246, s[38:39]
	s_mov_b32 m0, s63
	s_nop 0
	global_load_lds_dwordx4 v96, s[6:7]
	s_nop 0
	s_mov_b32 m0, s64
	s_nop 0
	global_load_lds_dwordx4 v245, s[6:7]
	s_waitcnt vmcnt(8)
	s_waitcnt lgkmcnt(0)
	s_barrier
	s_setprio 1
	s_waitcnt lgkmcnt(7)
	v_mfma_f32_16x16x32_bf16 v[60:63], v[130:133], v[162:165], v[60:63]
	v_mfma_f32_16x16x32_bf16 v[56:59], v[138:141], v[162:165], v[56:59]
	s_waitcnt lgkmcnt(5)
	v_mfma_f32_16x16x32_bf16 v[44:47], v[130:133], v[170:173], v[44:47]
	v_mfma_f32_16x16x32_bf16 v[40:43], v[138:141], v[170:173], v[40:43]
	s_waitcnt lgkmcnt(3)
	v_mfma_f32_16x16x32_bf16 v[28:31], v[130:133], v[178:181], v[28:31]
	v_mfma_f32_16x16x32_bf16 v[24:27], v[138:141], v[178:181], v[24:27]
	s_waitcnt lgkmcnt(1)
	v_mfma_f32_16x16x32_bf16 v[12:15], v[130:133], v[186:189], v[12:15]
	v_mfma_f32_16x16x32_bf16 v[8:11], v[138:141], v[186:189], v[8:11]
	v_mfma_f32_16x16x32_bf16 v[60:63], v[134:137], v[166:169], v[60:63]
	v_mfma_f32_16x16x32_bf16 v[56:59], v[142:145], v[166:169], v[56:59]
	v_mfma_f32_16x16x32_bf16 v[44:47], v[134:137], v[174:177], v[44:47]
	v_mfma_f32_16x16x32_bf16 v[40:43], v[142:145], v[174:177], v[40:43]
	v_mfma_f32_16x16x32_bf16 v[28:31], v[134:137], v[182:185], v[28:31]
	v_mfma_f32_16x16x32_bf16 v[24:27], v[142:145], v[182:185], v[24:27]
	s_waitcnt lgkmcnt(0)
	v_mfma_f32_16x16x32_bf16 v[12:15], v[134:137], v[190:193], v[12:15]
	v_mfma_f32_16x16x32_bf16 v[8:11], v[142:145], v[190:193], v[8:11]
	s_setprio 0
	s_setprio 1
	v_mfma_f32_16x16x32_bf16 v[52:55], v[146:149], v[162:165], v[52:55]
	v_mfma_f32_16x16x32_bf16 v[48:51], v[154:157], v[162:165], v[48:51]
	v_mfma_f32_16x16x32_bf16 v[36:39], v[146:149], v[170:173], v[36:39]
	v_mfma_f32_16x16x32_bf16 v[32:35], v[154:157], v[170:173], v[32:35]
	v_mfma_f32_16x16x32_bf16 v[20:23], v[146:149], v[178:181], v[20:23]
	v_mfma_f32_16x16x32_bf16 v[16:19], v[154:157], v[178:181], v[16:19]
	v_mfma_f32_16x16x32_bf16 v[4:7], v[146:149], v[186:189], v[4:7]
	v_mfma_f32_16x16x32_bf16 v[0:3], v[154:157], v[186:189], v[0:3]
	v_mfma_f32_16x16x32_bf16 v[52:55], v[150:153], v[166:169], v[52:55]
	v_mfma_f32_16x16x32_bf16 v[48:51], v[158:161], v[166:169], v[48:51]
	v_mfma_f32_16x16x32_bf16 v[36:39], v[150:153], v[174:177], v[36:39]
	v_mfma_f32_16x16x32_bf16 v[32:35], v[158:161], v[174:177], v[32:35]
	v_mfma_f32_16x16x32_bf16 v[20:23], v[150:153], v[182:185], v[20:23]
	v_mfma_f32_16x16x32_bf16 v[16:19], v[158:161], v[182:185], v[16:19]
	v_mfma_f32_16x16x32_bf16 v[4:7], v[150:153], v[190:193], v[4:7]
	v_mfma_f32_16x16x32_bf16 v[0:3], v[158:161], v[190:193], v[0:3]
	s_setprio 0
	s_barrier
	s_add_i32 s45, s45, 2
	s_add_u32 s5, s5, 0x100
	s_addc_u32 s29, s29, 0
	s_cmp_gt_u32 s45, 13
	s_mov_b64 s[38:39], s[2:3]
	s_cbranch_scc0 .LBB0_1237
	s_and_b64 vcc, exec, s[24:25]
	s_cbranch_vccz .LBB0_1240
	s_barrier

.LBB0_1429:
	v_ashrrev_i32_e32 v0, 31, v3
	v_lshrrev_b32_e32 v0, 26, v0
	v_add_u32_e32 v0, v3, v0
	v_ashrrev_i32_e32 v5, 6, v0
	v_bfe_i32 v0, v3, 27, 1
	v_lshlrev_b32_e32 v9, 4, v3
	v_lshrrev_b32_e32 v0, 22, v0
	v_add_u32_e32 v0, v9, v0
	v_and_b32_e32 v0, 0xfffffc00, v0
	s_add_u32 s16, s10, 0x62800000
	v_sub_u32_e32 v0, v9, v0
	s_addc_u32 s17, s11, 0
	v_lshrrev_b32_e32 v1, 4, v0
	s_lshl_b32 s4, s14, 2
	v_bitop3_b32 v6, v1, v0, 32 bitop3:0x6c
	v_lshlrev_b32_e32 v0, 3, v5
	s_add_i32 s4, s4, 0
	v_and_b32_e32 v7, -16, v0
	v_ashrrev_i32_e32 v0, 31, v6
	s_add_i32 s4, s4, 0x20400
	v_lshrrev_b32_e32 v4, 26, v0
	v_mov_b32_e32 v0, s4
	ds_read2_b32 v[0:1], v0 offset1:32
	v_add_u32_e32 v4, v6, v4
	v_ashrrev_i32_e32 v4, 6, v4
	v_add_u32_e32 v199, v4, v7
	v_mbcnt_lo_u32_b32 v186, -1, 0
	v_mbcnt_hi_u32_b32 v186, -1, v186
	v_add_u32_e32 v186, s93, v186
	v_lshrrev_b32_e32 v199, 3, v186
	s_lshl_b32 s7, s14, 14
	s_waitcnt lgkmcnt(0)
	v_sub_u32_e32 v1, v249, v1
	v_lshlrev_b32_e32 v12, 8, v1
	v_add_u32_e32 v1, v12, v199
	v_cmp_lt_i32_e32 vcc, v1, v0
	v_mov_b32_e32 v8, 0
	v_mov_b32_e32 v7, 0
	s_and_saveexec_b64 s[4:5], vcc
	s_cbranch_execz .LBB0_1431
	v_add_u32_e32 v10, s7, v1
	v_ashrrev_i32_e32 v11, 31, v10
	v_lshl_add_u64 v[10:11], v[10:11], 2, s[16:17]
	global_load_dword v7, v[10:11], off
.LBB0_1431:
	s_or_b64 exec, exec, s[4:5]
	v_add_u32_e32 v1, 0x2000, v9
	v_ashrrev_i32_e32 v9, 31, v1
	v_lshrrev_b32_e32 v9, 22, v9
	v_add_u32_e32 v9, v1, v9
	v_ashrrev_i32_e32 v10, 10, v9
	v_mul_i32_i24_e32 v9, 0x400, v10
	v_sub_u32_e32 v1, v1, v9
	v_lshrrev_b32_e32 v9, 4, v1
	v_bitop3_b32 v11, v9, v1, 32 bitop3:0x6c
	v_lshlrev_b32_e32 v1, 3, v10
	v_and_b32_e32 v9, -16, v1
	v_ashrrev_i32_e32 v1, 31, v11
	v_lshrrev_b32_e32 v1, 26, v1
	v_add_u32_e32 v1, v11, v1
	v_ashrrev_i32_e32 v1, 6, v1
	v_add_u32_e32 v201, v1, v9
	v_mbcnt_lo_u32_b32 v186, -1, 0
	v_mbcnt_hi_u32_b32 v186, -1, v186
	v_add_u32_e32 v186, s93, v186
	v_lshrrev_b32_e32 v201, 3, v186
	v_add_u32_e32 v201, 64, v201
	v_add_u32_e32 v9, v12, v201
	v_cmp_lt_i32_e32 vcc, v9, v0
	s_and_saveexec_b64 s[4:5], vcc
	s_cbranch_execz .LBB0_1433
	v_add_u32_e32 v8, s7, v9
	v_ashrrev_i32_e32 v9, 31, v8
	v_lshl_add_u64 v[8:9], v[8:9], 2, s[16:17]
	global_load_dword v8, v[8:9], off

.LBB0_1437:
	s_or_b64 exec, exec, s[4:5]
	v_lshlrev_b32_e32 v0, 5, v5
	v_lshlrev_b32_e32 v5, 6, v4
	v_sub_u32_e32 v5, v6, v5
	v_ashrrev_i16_sdwa v5, v239, sext(v5) dst_sel:DWORD dst_unused:UNUSED_PAD src0_sel:DWORD src1_sel:BYTE_0
	v_and_b32_e32 v0, 32, v0
	v_bfe_i32 v5, v5, 0, 16
	v_add_lshl_u32 v96, v0, v5, 1
	v_mbcnt_lo_u32_b32 v186, -1, 0
	v_mbcnt_hi_u32_b32 v186, -1, v186
	v_add_u32_e32 v186, s93, v186
	v_lshrrev_b32_e32 v96, 4, v186
	v_xor_b32_e32 v96, v96, v186
	v_lshlrev_b32_e32 v96, 4, v96
	v_and_b32_e32 v96, 0x70, v96
	v_lshlrev_b32_e32 v5, 6, v1
	v_sub_u32_e32 v5, v11, v5
	v_lshlrev_b32_e32 v0, 5, v10
	v_ashrrev_i16_sdwa v5, v239, sext(v5) dst_sel:DWORD dst_unused:UNUSED_PAD src0_sel:DWORD src1_sel:BYTE_0
	v_and_b32_e32 v0, 32, v0
	v_bfe_i32 v5, v5, 0, 16
	v_add_lshl_u32 v200, v0, v5, 1
	v_mbcnt_lo_u32_b32 v186, -1, 0
	v_mbcnt_hi_u32_b32 v186, -1, v186
	v_add_u32_e32 v186, s93, v186
	v_lshrrev_b32_e32 v200, 4, v186
	v_xor_b32_e32 v200, v200, v186
	v_lshlrev_b32_e32 v200, 4, v200
	v_and_b32_e32 v200, 0x70, v200
	s_waitcnt vmcnt(0)
	v_mad_u64_u32 v[214:215], s[4:5], v13, s12, v[96:97]
	v_mad_u64_u32 v[216:217], s[4:5], v8, s12, v[200:201]
	v_mad_u64_u32 v[218:219], s[4:5], v7, s12, v[96:97]
	s_lshl_b32 s86, s44, 16
	v_lshlrev_b32_e32 v0, 1, v199
	v_lshrrev_b32_e32 v5, 2, v199
	v_and_b32_e32 v4, 3, v4
	s_movk_i32 s13, 0xffe0
	s_lshl_b64 s[4:5], s[86:87], 10
	v_and_b32_e32 v0, 24, v0
	v_and_b32_e32 v5, 4, v5
	v_and_or_b32 v4, v199, s13, v4
	s_add_u32 s54, s50, s4
	v_or3_b32 v0, v4, v5, v0
	s_addc_u32 s55, s51, s5
	v_mad_u64_u32 v[202:203], s[4:5], v0, s12, v[96:97]
	v_mbcnt_lo_u32_b32 v186, -1, 0
	v_mbcnt_hi_u32_b32 v186, -1, v186
	v_add_u32_e32 v186, s93, v186
	v_lshrrev_b32_e32 v187, 3, v186
	v_and_b32_e32 v188, 12, v187
	v_lshlrev_b32_e32 v188, 1, v188
	v_and_b32_e32 v202, 0xffffffe3, v187
	v_or_b32_e32 v188, v188, v202
	v_lshrrev_b32_e32 v187, 2, v187
	v_and_b32_e32 v187, 4, v187
	v_or_b32_e32 v187, v187, v188
	v_lshrrev_b32_e32 v188, 4, v186
	v_xor_b32_e32 v188, v188, v186
	v_lshlrev_b32_e32 v188, 4, v188
	v_and_b32_e32 v188, 0x70, v188
	v_lshl_add_u32 v202, v187, 10, v188
	v_lshlrev_b32_e32 v0, 1, v201
	v_lshrrev_b32_e32 v4, 2, v201
	v_and_b32_e32 v1, 3, v1
	v_and_b32_e32 v0, 24, v0
	v_and_b32_e32 v4, 4, v4
	v_and_or_b32 v1, v201, s13, v1
	s_add_u32 s18, s10, 0x69100000
	v_or3_b32 v0, v1, v4, v0
	s_addc_u32 s19, s11, 0
	v_mad_u64_u32 v[204:205], s[4:5], v0, s12, v[200:201]
	v_mbcnt_lo_u32_b32 v186, -1, 0
	v_mbcnt_hi_u32_b32 v186, -1, v186
	v_add_u32_e32 v186, s93, v186
	v_lshrrev_b32_e32 v187, 3, v186
	v_add_u32_e32 v187, 64, v187
	v_and_b32_e32 v188, 12, v187
	v_lshlrev_b32_e32 v188, 1, v188
	v_and_b32_e32 v204, 0xffffffe3, v187
	v_or_b32_e32 v188, v188, v204
	v_lshrrev_b32_e32 v187, 2, v187
	v_and_b32_e32 v187, 4, v187
	v_or_b32_e32 v187, v187, v188
	v_lshrrev_b32_e32 v188, 4, v186
	v_xor_b32_e32 v188, v188, v186
	v_lshlrev_b32_e32 v188, 4, v188
	v_and_b32_e32 v188, 0x70, v188
	v_lshl_add_u32 v204, v187, 10, v188
	s_ashr_i32 s26, s6, 6
	s_ashr_i32 s13, s12, 31
	v_mad_u64_u32 v[220:221], s[4:5], v9, s12, v[200:201]
	s_ashr_i32 s15, s14, 31
	s_ashr_i32 s7, s6, 8
	s_lshl_b64 s[20:21], s[12:13], 7
	s_lshl_b32 s22, s26, 10
	s_lshl_b64 s[4:5], s[14:15], 21
	s_add_u32 s4, s54, s4
	s_addc_u32 s5, s55, s5
	v_readlane_b32 s24, v253, 29
	v_readlane_b32 s25, v253, 30
	s_add_u32 s38, s4, s24
	s_addc_u32 s39, s5, s25
	s_add_i32 s56, s22, 0
	s_add_i32 s57, s56, 0x10000
	s_mov_b32 m0, s57
	s_nop 0
	global_load_lds_dwordx4 v202, s[38:39]
	s_add_i32 s58, s56, 0x12000
	s_mov_b32 m0, s58
	s_nop 0
	global_load_lds_dwordx4 v204, s[38:39]
	s_add_u32 s4, s38, s20
	s_addc_u32 s5, s39, s21
	s_add_i32 s59, s56, 0x14000
	s_mov_b32 m0, s59
	s_nop 0
	global_load_lds_dwordx4 v202, s[4:5]
	s_add_i32 s60, s56, 0x16000
	s_mov_b32 m0, s60
	s_nop 0
	global_load_lds_dwordx4 v204, s[4:5]
	s_add_i32 s61, s56, 0x2000
	s_mov_b32 m0, s56
	s_nop 0
	global_load_lds_dwordx4 v218, s[18:19]
	s_add_i32 s62, s56, 0x4000
	s_mov_b32 m0, s61
	s_nop 0
	global_load_lds_dwordx4 v216, s[18:19]
	s_add_i32 s63, s56, 0x6000
	s_mov_b32 m0, s62
	s_nop 0
	global_load_lds_dwordx4 v214, s[18:19]
	s_cmp_eq_u32 s7, 1
	s_mov_b32 m0, s63
	s_nop 0
	global_load_lds_dwordx4 v220, s[18:19]
	s_cselect_b64 s[22:23], -1, 0
	s_cmp_lg_u32 s7, 1
	s_cbranch_scc1 .LBB0_1439
	s_barrier
.LBB0_1439:
	s_add_u32 s24, s10, 0x4e500000
	s_addc_u32 s25, s11, 0
	s_lshl_b64 s[28:29], s[86:87], 2
	s_add_u32 s64, s2, s28
	s_addc_u32 s65, s3, s29
	s_lshr_b32 s2, s13, 25
	v_and_b32_e32 v0, 63, v3
	v_bfe_u32 v203, v3, 4, 2
	v_and_b32_e32 v205, 15, v3
	s_add_i32 s2, s12, s2
	v_and_b32_e32 v1, 48, v3
	v_lshlrev_b32_e32 v3, 2, v3
	s_ashr_i32 s13, s2, 7
	s_lshl_b32 s2, s7, 13
	v_lshl_or_b32 v1, v205, 6, v1
	v_and_b32_e32 v3, 32, v3
	v_bitop3_b32 v244, v1, s2, v3 bitop3:0xde
	v_mbcnt_lo_u32_b32 v186, -1, 0
	v_mbcnt_hi_u32_b32 v186, -1, v186
	v_add_u32_e32 v186, s93, v186
	v_bfe_u32 v187, v186, 4, 2
	v_bfe_u32 v188, v186, 1, 3
	v_xor_b32_e32 v187, v187, v188
	v_lshlrev_b32_e32 v187, 4, v187
	v_and_b32_e32 v188, 15, v186
	v_lshl_or_b32 v187, v188, 7, v187
	v_lshrrev_b32_e32 v188, 8, v186
	v_lshl_or_b32 v244, v188, 13, v187
	s_lshl_b32 s2, s26, 5
	s_and_b32 s67, s2, 0x60
	s_lshl_b32 s66, s7, 6
	s_lshl_b32 s2, s67, 7
	v_bitop3_b32 v245, s2, v1, v3 bitop3:0xf6
	v_mbcnt_lo_u32_b32 v186, -1, 0
	v_mbcnt_hi_u32_b32 v186, -1, v186
	v_add_u32_e32 v186, s93, v186
	v_bfe_u32 v187, v186, 4, 2
	v_bfe_u32 v188, v186, 1, 3
	v_xor_b32_e32 v187, v187, v188
	v_lshlrev_b32_e32 v187, 4, v187
	v_and_b32_e32 v188, 15, v186
	v_lshl_or_b32 v187, v188, 7, v187
	v_bfe_u32 v188, v186, 6, 2
	v_lshl_or_b32 v245, v188, 12, v187
	s_add_u32 s2, s38, 0x80
	s_waitcnt vmcnt(2)
	s_barrier
	s_addc_u32 s3, s39, 0
	s_add_i32 s68, s56, 0x18000
	s_mov_b32 m0, s68
	s_nop 0
	global_load_lds_dwordx4 v202, s[2:3]
	s_add_i32 s69, s56, 0x1a000
	s_mov_b32 m0, s69
	s_nop 0
	global_load_lds_dwordx4 v204, s[2:3]
	s_add_u32 s2, s18, 0x80
	s_addc_u32 s3, s19, 0
	s_add_i32 s70, s56, 0x8000
	s_mov_b32 m0, s70
	s_nop 0
	global_load_lds_dwordx4 v218, s[2:3]
	s_add_i32 s71, s56, 0xa000
	s_mov_b32 m0, s71
	s_nop 0
	global_load_lds_dwordx4 v216, s[2:3]
	s_add_u32 s2, s4, 0x80
	s_addc_u32 s3, s5, 0
	s_add_i32 s72, s56, 0x1c000
	s_add_i32 s73, s56, 0x1e000
	s_mov_b32 m0, s72
	s_nop 0
	global_load_lds_dwordx4 v202, s[2:3]
	s_cmp_lt_u32 s6, 64
	s_mov_b32 m0, s73
	s_nop 0
	global_load_lds_dwordx4 v204, s[2:3]
	s_cselect_b64 s[26:27], -1, 0
	s_cmpk_gt_i32 s12, 0x7f
	s_waitcnt vmcnt(6)
	s_cselect_b64 s[28:29], -1, 0
	s_add_i32 s74, s13, -2
	s_add_i32 s75, s56, 0xc000
	s_cmpk_lt_u32 s6, 0x100
	v_readlane_b32 s2, v253, 27
	v_lshlrev_b32_e32 v246, 4, v0
	s_mov_b32 s76, 0
	s_cselect_b64 s[30:31], -1, 0
	s_mov_b32 s77, s2
	s_barrier
	v_readlane_b32 s3, v253, 28
	s_branch .LBB0_1442

.LBB0_1452:
	s_add_i32 s79, s79, 2
	s_and_b64 s[44:45], s[48:49], exec
	s_cselect_b32 s45, 0, s42
	s_cselect_b32 s44, 0, s43
	s_add_u32 s46, s18, s45
	s_addc_u32 s47, s19, s44
	s_add_u32 s80, s38, s42
	s_addc_u32 s81, s39, s43
	s_add_u32 s44, s46, 0x80
	s_addc_u32 s45, s47, 0
	s_waitcnt vmcnt(8)
	s_and_b64 s[48:49], s[48:49], exec
	s_waitcnt lgkmcnt(0)
	s_cselect_b32 s80, s36, s80
	s_cselect_b32 s81, s37, s81
	s_add_u32 s48, s80, 0x80
	s_addc_u32 s49, s81, 0
	s_barrier
	s_setprio 1
	s_waitcnt lgkmcnt(0)
	v_mfma_scale_f32_16x16x128_f8f6f4 v[98:101], v[24:31], v[32:39], v[98:101], v243, v243 op_sel_hi:[0,0,0]
	v_mfma_scale_f32_16x16x128_f8f6f4 v[66:69], v[16:23], v[56:63], v[170:173], v243, v243 op_sel_hi:[0,0,0]
	v_mfma_scale_f32_16x16x128_f8f6f4 v[70:73], v[24:31], v[56:63], v[162:165], v243, v243 op_sel_hi:[0,0,0]
	v_mfma_scale_f32_16x16x128_f8f6f4 v[74:77], v[16:23], v[48:55], v[146:149], v243, v243 op_sel_hi:[0,0,0]
	v_mfma_scale_f32_16x16x128_f8f6f4 v[78:81], v[24:31], v[48:55], v[138:141], v243, v243 op_sel_hi:[0,0,0]
	v_mfma_scale_f32_16x16x128_f8f6f4 v[82:85], v[16:23], v[40:47], v[130:133], v243, v243 op_sel_hi:[0,0,0]
	v_mfma_scale_f32_16x16x128_f8f6f4 v[86:89], v[24:31], v[40:47], v[114:117], v243, v243 op_sel_hi:[0,0,0]
	v_mfma_scale_f32_16x16x128_f8f6f4 v[90:93], v[16:23], v[32:39], v[106:109], v243, v243 op_sel_hi:[0,0,0]
	s_setprio 0
	s_setprio 1
	v_mfma_scale_f32_16x16x128_f8f6f4 v[142:145], v[8:15], v[48:55], v[142:145], v243, v243 op_sel_hi:[0,0,0]
	v_mfma_scale_f32_16x16x128_f8f6f4 v[134:137], v[0:7], v[40:47], v[134:137], v243, v243 op_sel_hi:[0,0,0]
	v_mfma_scale_f32_16x16x128_f8f6f4 v[122:125], v[8:15], v[40:47], v[122:125], v243, v243 op_sel_hi:[0,0,0]
	v_mfma_scale_f32_16x16x128_f8f6f4 v[110:113], v[0:7], v[32:39], v[110:113], v243, v243 op_sel_hi:[0,0,0]
	v_mfma_scale_f32_16x16x128_f8f6f4 v[102:105], v[8:15], v[32:39], v[102:105], v243, v243 op_sel_hi:[0,0,0]
	v_mfma_scale_f32_16x16x128_f8f6f4 v[118:121], v[0:7], v[56:63], v[174:177], v243, v243 op_sel_hi:[0,0,0]
	v_mfma_scale_f32_16x16x128_f8f6f4 v[126:129], v[8:15], v[56:63], v[166:169], v243, v243 op_sel_hi:[0,0,0]
	v_mfma_scale_f32_16x16x128_f8f6f4 v[150:153], v[0:7], v[48:55], v[154:157], v243, v243 op_sel_hi:[0,0,0]
	s_setprio 0
	s_barrier
	s_mov_b32 m0, s57
	s_nop 0
	global_load_lds_dwordx4 v202, s[80:81]
	s_nop 0
	s_mov_b32 m0, s58
	s_nop 0
	global_load_lds_dwordx4 v204, s[80:81]
	s_add_u32 s80, s80, s20
	s_addc_u32 s81, s81, s21
	s_mov_b32 m0, s59
	s_nop 0
	global_load_lds_dwordx4 v202, s[80:81]
	s_nop 0
	s_mov_b32 m0, s60
	s_nop 0
	global_load_lds_dwordx4 v204, s[80:81]
	s_mov_b32 m0, s56
	s_nop 0
	global_load_lds_dwordx4 v206, s[46:47]
	s_nop 0
	s_mov_b32 m0, s61
	s_nop 0
	global_load_lds_dwordx4 v208, s[46:47]
	s_waitcnt vmcnt(8)
	s_waitcnt lgkmcnt(0)
	s_barrier
	s_barrier
	v_add_u32_e32 v12, 0x18000, v65
	v_add_u32_e32 v28, 0x1c000, v65
	v_xor_b32_e32 v15, 64, v12
	ds_read_b128 v[0:3], v12
	ds_read_b128 v[4:7], v15
	ds_read_b128 v[8:11], v12 offset:2048
	ds_read_b128 v[12:15], v15 offset:2048
	v_xor_b32_e32 v31, 64, v28
	ds_read_b128 v[16:19], v28
	ds_read_b128 v[20:23], v31
	ds_read_b128 v[24:27], v28 offset:2048
	ds_read_b128 v[28:31], v31 offset:2048
	v_xor_b32_e32 v63, 64, v64
	ds_read_b128 v[32:35], v64 offset:32768
	ds_read_b128 v[36:39], v63 offset:32768
	ds_read_b128 v[40:43], v64 offset:34816
	ds_read_b128 v[44:47], v63 offset:34816
	ds_read_b128 v[48:51], v64 offset:36864
	ds_read_b128 v[52:55], v63 offset:36864
	ds_read_b128 v[56:59], v64 offset:38912
	ds_read_b128 v[60:63], v63 offset:38912
	s_mov_b32 m0, s62
	s_nop 0
	global_load_lds_dwordx4 v210, s[46:47]
	s_nop 0
	s_mov_b32 m0, s63
	s_nop 0
	global_load_lds_dwordx4 v212, s[46:47]
	s_waitcnt vmcnt(8)
	s_waitcnt lgkmcnt(0)
	s_barrier
	s_setprio 1
	s_waitcnt lgkmcnt(6)
	v_mfma_scale_f32_16x16x128_f8f6f4 v[170:173], v[0:7], v[32:39], v[66:69], v243, v243 op_sel_hi:[0,0,0]
	v_mfma_scale_f32_16x16x128_f8f6f4 v[162:165], v[8:15], v[32:39], v[70:73], v243, v243 op_sel_hi:[0,0,0]
	s_waitcnt lgkmcnt(4)
	v_mfma_scale_f32_16x16x128_f8f6f4 v[146:149], v[0:7], v[40:47], v[74:77], v243, v243 op_sel_hi:[0,0,0]
	v_mfma_scale_f32_16x16x128_f8f6f4 v[138:141], v[8:15], v[40:47], v[78:81], v243, v243 op_sel_hi:[0,0,0]
	s_waitcnt lgkmcnt(2)
	v_mfma_scale_f32_16x16x128_f8f6f4 v[130:133], v[0:7], v[48:55], v[82:85], v243, v243 op_sel_hi:[0,0,0]
	v_mfma_scale_f32_16x16x128_f8f6f4 v[114:117], v[8:15], v[48:55], v[86:89], v243, v243 op_sel_hi:[0,0,0]
	s_waitcnt lgkmcnt(0)
	v_mfma_scale_f32_16x16x128_f8f6f4 v[106:109], v[0:7], v[56:63], v[90:93], v243, v243 op_sel_hi:[0,0,0]
	v_mfma_scale_f32_16x16x128_f8f6f4 v[98:101], v[8:15], v[56:63], v[98:101], v243, v243 op_sel_hi:[0,0,0]
	s_setprio 0
	s_setprio 1
	v_mfma_scale_f32_16x16x128_f8f6f4 v[174:177], v[16:23], v[32:39], v[118:121], v243, v243 op_sel_hi:[0,0,0]
	v_mfma_scale_f32_16x16x128_f8f6f4 v[166:169], v[24:31], v[32:39], v[126:129], v243, v243 op_sel_hi:[0,0,0]
	v_mfma_scale_f32_16x16x128_f8f6f4 v[154:157], v[16:23], v[40:47], v[150:153], v243, v243 op_sel_hi:[0,0,0]
	v_mfma_scale_f32_16x16x128_f8f6f4 v[142:145], v[24:31], v[40:47], v[142:145], v243, v243 op_sel_hi:[0,0,0]
	v_mfma_scale_f32_16x16x128_f8f6f4 v[134:137], v[16:23], v[48:55], v[134:137], v243, v243 op_sel_hi:[0,0,0]
	v_mfma_scale_f32_16x16x128_f8f6f4 v[122:125], v[24:31], v[48:55], v[122:125], v243, v243 op_sel_hi:[0,0,0]
	v_mfma_scale_f32_16x16x128_f8f6f4 v[110:113], v[16:23], v[56:63], v[110:113], v243, v243 op_sel_hi:[0,0,0]
	v_mfma_scale_f32_16x16x128_f8f6f4 v[102:105], v[24:31], v[56:63], v[102:105], v243, v243 op_sel_hi:[0,0,0]
	s_setprio 0
	s_barrier
	s_mov_b32 m0, s68
	s_nop 0
	global_load_lds_dwordx4 v202, s[48:49]
	s_nop 0
	s_mov_b32 m0, s69
	s_nop 0
	global_load_lds_dwordx4 v204, s[48:49]
	s_add_u32 s46, s48, s20
	s_addc_u32 s47, s49, s21
	s_mov_b32 m0, s72
	s_nop 0
	global_load_lds_dwordx4 v202, s[46:47]
	s_nop 0
	s_mov_b32 m0, s73
	s_nop 0
	global_load_lds_dwordx4 v204, s[46:47]
	s_mov_b32 m0, s70
	s_nop 0
	global_load_lds_dwordx4 v206, s[44:45]
	s_nop 0
	s_mov_b32 m0, s71
	s_nop 0
	global_load_lds_dwordx4 v208, s[44:45]
	s_waitcnt vmcnt(8)
	s_waitcnt lgkmcnt(0)
	s_barrier
	s_barrier
	s_add_u32 s42, s42, 0x100
	s_addc_u32 s43, s43, 0
	s_cmp_ge_i32 s79, s13
	s_cbranch_scc1 .LBB0_1455
.LBB0_1453:
	v_add_u32_e32 v65, 0, v245
	v_add_u32_e32 v0, 0x10000, v65
	v_add_u32_e32 v12, 0x14000, v65
	v_xor_b32_e32 v31, 64, v0
	ds_read_b128 v[16:19], v0
	ds_read_b128 v[20:23], v31
	ds_read_b128 v[24:27], v0 offset:2048
	ds_read_b128 v[28:31], v31 offset:2048
	v_xor_b32_e32 v15, 64, v12
	ds_read_b128 v[0:3], v12
	ds_read_b128 v[4:7], v15
	ds_read_b128 v[8:11], v12 offset:2048
	ds_read_b128 v[12:15], v15 offset:2048
	s_cmp_eq_u32 s74, s79
	s_cselect_b64 s[48:49], -1, 0
	s_add_u32 s44, s18, s42
	s_addc_u32 s45, s19, s43
	s_add_u32 s44, s44, 0xffffff80
	s_addc_u32 s45, s45, -1
	v_add_u32_e32 v64, 0, v244
	v_xor_b32_e32 v39, 64, v64
	ds_read_b128 v[56:59], v64
	ds_read_b128 v[60:63], v39
	ds_read_b128 v[48:51], v64 offset:2048
	ds_read_b128 v[52:55], v39 offset:2048
	ds_read_b128 v[40:43], v64 offset:4096
	ds_read_b128 v[44:47], v39 offset:4096
	ds_read_b128 v[32:35], v64 offset:6144
	ds_read_b128 v[36:39], v39 offset:6144
	s_mov_b32 m0, s75
	s_nop 0
	global_load_lds_dwordx4 v210, s[44:45]
	s_add_i32 s46, s56, 0xe000
	s_mov_b32 m0, s46
	s_nop 0
	global_load_lds_dwordx4 v212, s[44:45]
	s_and_b64 s[44:45], s[40:41], s[48:49]
	s_andn2_b64 vcc, exec, s[44:45]
	s_cbranch_vccnz .LBB0_1452
	v_mov_b32_e32 v66, s35
	ds_read2_b32 v[66:67], v66 offset1:32
	s_waitcnt lgkmcnt(0)
	v_sub_u32_e32 v67, v67, v247
	v_lshlrev_b32_e32 v67, 8, v67
	v_add_u32_e32 v66, v67, v66
	v_min_i32_e32 v66, 0x100, v66
	v_add_u32_e32 v66, -1, v66
	v_min_i32_e32 v67, v199, v66
	v_min_i32_e32 v68, v201, v66
	v_min_i32_e32 v69, v222, v66
	v_min_i32_e32 v66, v223, v66
	v_lshl_add_u32 v67, v67, 2, s15
	v_lshl_add_u32 v68, v68, 2, s15
	v_lshl_add_u32 v69, v69, 2, s15
	v_lshl_add_u32 v66, v66, 2, s15
	ds_read_b32 v67, v67
	ds_read_b32 v68, v68
	ds_read_b32 v69, v69
	ds_read_b32 v66, v66
	s_waitcnt lgkmcnt(3)
	v_mad_u64_u32 v[206:207], s[44:45], v67, s12, v[96:97]
	s_waitcnt lgkmcnt(2)
	v_mad_u64_u32 v[208:209], s[44:45], v68, s12, v[200:201]
	s_waitcnt lgkmcnt(1)
	v_mad_u64_u32 v[210:211], s[44:45], v69, s12, v[96:97]
	s_waitcnt lgkmcnt(0)
	v_mad_u64_u32 v[212:213], s[44:45], v66, s12, v[200:201]
	s_branch .LBB0_1452

.LBB0_1460:
	s_add_i32 s79, s79, 2
	s_and_b64 s[42:43], s[46:47], exec
	s_cselect_b32 s43, 0, s6
	s_cselect_b32 s42, 0, s7
	s_add_u32 s44, s18, s43
	s_addc_u32 s45, s19, s42
	s_add_u32 s48, s38, s6
	s_addc_u32 s49, s39, s7
	s_add_u32 s42, s44, 0x80
	s_addc_u32 s43, s45, 0
	s_waitcnt vmcnt(8)
	s_and_b64 s[46:47], s[46:47], exec
	s_waitcnt lgkmcnt(0)
	s_cselect_b32 s48, s36, s48
	s_cselect_b32 s49, s37, s49
	s_add_u32 s46, s48, 0x80
	s_addc_u32 s47, s49, 0
	s_barrier
	s_setprio 1
	s_waitcnt lgkmcnt(6)
	v_mfma_scale_f32_16x16x128_f8f6f4 v[170:173], v[16:23], v[56:63], v[170:173], v243, v243 op_sel_hi:[0,0,0]
	v_mfma_scale_f32_16x16x128_f8f6f4 v[162:165], v[24:31], v[56:63], v[162:165], v243, v243 op_sel_hi:[0,0,0]
	s_waitcnt lgkmcnt(4)
	v_mfma_scale_f32_16x16x128_f8f6f4 v[146:149], v[16:23], v[48:55], v[146:149], v243, v243 op_sel_hi:[0,0,0]
	v_mfma_scale_f32_16x16x128_f8f6f4 v[138:141], v[24:31], v[48:55], v[138:141], v243, v243 op_sel_hi:[0,0,0]
	s_waitcnt lgkmcnt(2)
	v_mfma_scale_f32_16x16x128_f8f6f4 v[130:133], v[16:23], v[40:47], v[130:133], v243, v243 op_sel_hi:[0,0,0]
	v_mfma_scale_f32_16x16x128_f8f6f4 v[114:117], v[24:31], v[40:47], v[114:117], v243, v243 op_sel_hi:[0,0,0]
	s_waitcnt lgkmcnt(0)
	v_mfma_scale_f32_16x16x128_f8f6f4 v[106:109], v[16:23], v[32:39], v[106:109], v243, v243 op_sel_hi:[0,0,0]
	v_mfma_scale_f32_16x16x128_f8f6f4 v[98:101], v[24:31], v[32:39], v[98:101], v243, v243 op_sel_hi:[0,0,0]
	s_setprio 0
	s_setprio 1
	v_mfma_scale_f32_16x16x128_f8f6f4 v[174:177], v[0:7], v[56:63], v[174:177], v243, v243 op_sel_hi:[0,0,0]
	v_mfma_scale_f32_16x16x128_f8f6f4 v[166:169], v[8:15], v[56:63], v[166:169], v243, v243 op_sel_hi:[0,0,0]
	v_mfma_scale_f32_16x16x128_f8f6f4 v[154:157], v[0:7], v[48:55], v[154:157], v243, v243 op_sel_hi:[0,0,0]
	v_mfma_scale_f32_16x16x128_f8f6f4 v[142:145], v[8:15], v[48:55], v[142:145], v243, v243 op_sel_hi:[0,0,0]
	v_mfma_scale_f32_16x16x128_f8f6f4 v[134:137], v[0:7], v[40:47], v[134:137], v243, v243 op_sel_hi:[0,0,0]
	v_mfma_scale_f32_16x16x128_f8f6f4 v[122:125], v[8:15], v[40:47], v[122:125], v243, v243 op_sel_hi:[0,0,0]
	v_mfma_scale_f32_16x16x128_f8f6f4 v[110:113], v[0:7], v[32:39], v[110:113], v243, v243 op_sel_hi:[0,0,0]
	v_mfma_scale_f32_16x16x128_f8f6f4 v[102:105], v[8:15], v[32:39], v[102:105], v243, v243 op_sel_hi:[0,0,0]
	s_setprio 0
	s_barrier
	v_xor_b32_e32 v63, 64, v206
	ds_read_b128 v[32:35], v206 offset:16384
	ds_read_b128 v[36:39], v63 offset:16384
	ds_read_b128 v[40:43], v206 offset:18432
	ds_read_b128 v[44:47], v63 offset:18432
	ds_read_b128 v[48:51], v206 offset:20480
	ds_read_b128 v[52:55], v63 offset:20480
	ds_read_b128 v[56:59], v206 offset:22528
	ds_read_b128 v[60:63], v63 offset:22528
	s_mov_b32 m0, s57
	s_nop 0
	global_load_lds_dwordx4 v202, s[48:49]
	s_nop 0
	s_mov_b32 m0, s58
	s_nop 0
	global_load_lds_dwordx4 v204, s[48:49]
	s_add_u32 s48, s48, s20
	s_addc_u32 s49, s49, s21
	s_mov_b32 m0, s59
	s_nop 0
	global_load_lds_dwordx4 v202, s[48:49]
	s_nop 0
	s_mov_b32 m0, s60
	s_nop 0
	global_load_lds_dwordx4 v204, s[48:49]
	s_mov_b32 m0, s56
	s_nop 0
	global_load_lds_dwordx4 v218, s[44:45]
	s_nop 0
	s_mov_b32 m0, s61
	s_nop 0
	global_load_lds_dwordx4 v216, s[44:45]
	s_waitcnt vmcnt(8)
	s_waitcnt lgkmcnt(0)
	s_barrier
	s_setprio 1
	s_waitcnt lgkmcnt(6)
	v_mfma_scale_f32_16x16x128_f8f6f4 v[190:193], v[16:23], v[32:39], v[190:193], v243, v243 op_sel_hi:[0,0,0]
	v_mfma_scale_f32_16x16x128_f8f6f4 v[182:185], v[24:31], v[32:39], v[182:185], v243, v243 op_sel_hi:[0,0,0]
	s_waitcnt lgkmcnt(4)
	v_mfma_scale_f32_16x16x128_f8f6f4 v[158:161], v[16:23], v[40:47], v[158:161], v243, v243 op_sel_hi:[0,0,0]
	v_mfma_scale_f32_16x16x128_f8f6f4 v[126:129], v[24:31], v[40:47], v[126:129], v243, v243 op_sel_hi:[0,0,0]
	s_waitcnt lgkmcnt(2)
	v_mfma_scale_f32_16x16x128_f8f6f4 v[92:95], v[16:23], v[48:55], v[92:95], v243, v243 op_sel_hi:[0,0,0]
	v_mfma_scale_f32_16x16x128_f8f6f4 v[84:87], v[24:31], v[48:55], v[84:87], v243, v243 op_sel_hi:[0,0,0]
	s_waitcnt lgkmcnt(0)
	v_mfma_scale_f32_16x16x128_f8f6f4 v[76:79], v[16:23], v[56:63], v[76:79], v243, v243 op_sel_hi:[0,0,0]
	v_mfma_scale_f32_16x16x128_f8f6f4 v[68:71], v[24:31], v[56:63], v[68:71], v243, v243 op_sel_hi:[0,0,0]
	s_setprio 0
	s_setprio 1
	v_mfma_scale_f32_16x16x128_f8f6f4 v[186:189], v[0:7], v[32:39], v[186:189], v243, v243 op_sel_hi:[0,0,0]
	v_mfma_scale_f32_16x16x128_f8f6f4 v[178:181], v[8:15], v[32:39], v[178:181], v243, v243 op_sel_hi:[0,0,0]
	v_mfma_scale_f32_16x16x128_f8f6f4 v[150:153], v[0:7], v[40:47], v[150:153], v243, v243 op_sel_hi:[0,0,0]
	v_mfma_scale_f32_16x16x128_f8f6f4 v[118:121], v[8:15], v[40:47], v[118:121], v243, v243 op_sel_hi:[0,0,0]
	v_mfma_scale_f32_16x16x128_f8f6f4 v[88:91], v[0:7], v[48:55], v[88:91], v243, v243 op_sel_hi:[0,0,0]
	v_mfma_scale_f32_16x16x128_f8f6f4 v[80:83], v[8:15], v[48:55], v[80:83], v243, v243 op_sel_hi:[0,0,0]
	v_mfma_scale_f32_16x16x128_f8f6f4 v[72:75], v[0:7], v[56:63], v[72:75], v243, v243 op_sel_hi:[0,0,0]
	v_mfma_scale_f32_16x16x128_f8f6f4 v[64:67], v[8:15], v[56:63], v[64:67], v243, v243 op_sel_hi:[0,0,0]
	s_setprio 0
	s_barrier
	v_add_u32_e32 v12, 0x18000, v207
	v_add_u32_e32 v28, 0x1c000, v207
	v_xor_b32_e32 v15, 64, v12
	ds_read_b128 v[0:3], v12
	ds_read_b128 v[4:7], v15
	ds_read_b128 v[8:11], v12 offset:2048
	ds_read_b128 v[12:15], v15 offset:2048
	v_xor_b32_e32 v31, 64, v28
	ds_read_b128 v[16:19], v28
	ds_read_b128 v[20:23], v31
	ds_read_b128 v[24:27], v28 offset:2048
	ds_read_b128 v[28:31], v31 offset:2048
	v_xor_b32_e32 v63, 64, v206
	ds_read_b128 v[32:35], v206 offset:32768
	ds_read_b128 v[36:39], v63 offset:32768
	ds_read_b128 v[40:43], v206 offset:34816
	ds_read_b128 v[44:47], v63 offset:34816
	ds_read_b128 v[48:51], v206 offset:36864
	ds_read_b128 v[52:55], v63 offset:36864
	ds_read_b128 v[56:59], v206 offset:38912
	ds_read_b128 v[60:63], v63 offset:38912
	s_mov_b32 m0, s62
	s_nop 0
	global_load_lds_dwordx4 v214, s[44:45]
	s_nop 0
	s_mov_b32 m0, s63
	s_nop 0
	global_load_lds_dwordx4 v220, s[44:45]
	s_waitcnt vmcnt(8)
	s_waitcnt lgkmcnt(0)
	s_barrier
	s_setprio 1
	s_waitcnt lgkmcnt(6)
	v_mfma_scale_f32_16x16x128_f8f6f4 v[170:173], v[0:7], v[32:39], v[170:173], v243, v243 op_sel_hi:[0,0,0]
	v_mfma_scale_f32_16x16x128_f8f6f4 v[162:165], v[8:15], v[32:39], v[162:165], v243, v243 op_sel_hi:[0,0,0]
	s_waitcnt lgkmcnt(4)
	v_mfma_scale_f32_16x16x128_f8f6f4 v[146:149], v[0:7], v[40:47], v[146:149], v243, v243 op_sel_hi:[0,0,0]
	v_mfma_scale_f32_16x16x128_f8f6f4 v[138:141], v[8:15], v[40:47], v[138:141], v243, v243 op_sel_hi:[0,0,0]
	s_waitcnt lgkmcnt(2)
	v_mfma_scale_f32_16x16x128_f8f6f4 v[130:133], v[0:7], v[48:55], v[130:133], v243, v243 op_sel_hi:[0,0,0]
	v_mfma_scale_f32_16x16x128_f8f6f4 v[114:117], v[8:15], v[48:55], v[114:117], v243, v243 op_sel_hi:[0,0,0]
	s_waitcnt lgkmcnt(0)
	v_mfma_scale_f32_16x16x128_f8f6f4 v[106:109], v[0:7], v[56:63], v[106:109], v243, v243 op_sel_hi:[0,0,0]
	v_mfma_scale_f32_16x16x128_f8f6f4 v[98:101], v[8:15], v[56:63], v[98:101], v243, v243 op_sel_hi:[0,0,0]
	s_setprio 0
	s_setprio 1
	v_mfma_scale_f32_16x16x128_f8f6f4 v[174:177], v[16:23], v[32:39], v[174:177], v243, v243 op_sel_hi:[0,0,0]
	v_mfma_scale_f32_16x16x128_f8f6f4 v[166:169], v[24:31], v[32:39], v[166:169], v243, v243 op_sel_hi:[0,0,0]
	v_mfma_scale_f32_16x16x128_f8f6f4 v[154:157], v[16:23], v[40:47], v[154:157], v243, v243 op_sel_hi:[0,0,0]
	v_mfma_scale_f32_16x16x128_f8f6f4 v[142:145], v[24:31], v[40:47], v[142:145], v243, v243 op_sel_hi:[0,0,0]
	v_mfma_scale_f32_16x16x128_f8f6f4 v[134:137], v[16:23], v[48:55], v[134:137], v243, v243 op_sel_hi:[0,0,0]
	v_mfma_scale_f32_16x16x128_f8f6f4 v[122:125], v[24:31], v[48:55], v[122:125], v243, v243 op_sel_hi:[0,0,0]
	v_mfma_scale_f32_16x16x128_f8f6f4 v[110:113], v[16:23], v[56:63], v[110:113], v243, v243 op_sel_hi:[0,0,0]
	v_mfma_scale_f32_16x16x128_f8f6f4 v[102:105], v[24:31], v[56:63], v[102:105], v243, v243 op_sel_hi:[0,0,0]
	s_setprio 0
	s_barrier
	v_xor_b32_e32 v63, 64, v206
	ds_read_b128 v[32:35], v206 offset:49152
	ds_read_b128 v[36:39], v63 offset:49152
	ds_read_b128 v[40:43], v206 offset:51200
	ds_read_b128 v[44:47], v63 offset:51200
	ds_read_b128 v[48:51], v206 offset:53248
	ds_read_b128 v[52:55], v63 offset:53248
	ds_read_b128 v[56:59], v206 offset:55296
	ds_read_b128 v[60:63], v63 offset:55296
	s_mov_b32 m0, s68
	s_nop 0
	global_load_lds_dwordx4 v202, s[46:47]
	s_nop 0
	s_mov_b32 m0, s69
	s_nop 0
	global_load_lds_dwordx4 v204, s[46:47]
	s_add_u32 s44, s46, s20
	s_addc_u32 s45, s47, s21
	s_mov_b32 m0, s72
	s_nop 0
	global_load_lds_dwordx4 v202, s[44:45]
	s_nop 0
	s_mov_b32 m0, s73
	s_nop 0
	global_load_lds_dwordx4 v204, s[44:45]
	s_mov_b32 m0, s70
	s_nop 0
	global_load_lds_dwordx4 v218, s[42:43]
	s_nop 0
	s_mov_b32 m0, s71
	s_nop 0
	global_load_lds_dwordx4 v216, s[42:43]
	s_waitcnt vmcnt(8)
	s_waitcnt lgkmcnt(0)
	s_barrier
	s_setprio 1
	s_waitcnt lgkmcnt(6)
	v_mfma_scale_f32_16x16x128_f8f6f4 v[190:193], v[0:7], v[32:39], v[190:193], v243, v243 op_sel_hi:[0,0,0]
	v_mfma_scale_f32_16x16x128_f8f6f4 v[182:185], v[8:15], v[32:39], v[182:185], v243, v243 op_sel_hi:[0,0,0]
	s_waitcnt lgkmcnt(4)
	v_mfma_scale_f32_16x16x128_f8f6f4 v[158:161], v[0:7], v[40:47], v[158:161], v243, v243 op_sel_hi:[0,0,0]
	v_mfma_scale_f32_16x16x128_f8f6f4 v[126:129], v[8:15], v[40:47], v[126:129], v243, v243 op_sel_hi:[0,0,0]
	s_waitcnt lgkmcnt(2)
	v_mfma_scale_f32_16x16x128_f8f6f4 v[92:95], v[0:7], v[48:55], v[92:95], v243, v243 op_sel_hi:[0,0,0]
	v_mfma_scale_f32_16x16x128_f8f6f4 v[84:87], v[8:15], v[48:55], v[84:87], v243, v243 op_sel_hi:[0,0,0]
	s_waitcnt lgkmcnt(0)
	v_mfma_scale_f32_16x16x128_f8f6f4 v[76:79], v[0:7], v[56:63], v[76:79], v243, v243 op_sel_hi:[0,0,0]
	v_mfma_scale_f32_16x16x128_f8f6f4 v[68:71], v[8:15], v[56:63], v[68:71], v243, v243 op_sel_hi:[0,0,0]
	s_setprio 0
	s_setprio 1
	v_mfma_scale_f32_16x16x128_f8f6f4 v[186:189], v[16:23], v[32:39], v[186:189], v243, v243 op_sel_hi:[0,0,0]
	v_mfma_scale_f32_16x16x128_f8f6f4 v[178:181], v[24:31], v[32:39], v[178:181], v243, v243 op_sel_hi:[0,0,0]
	v_mfma_scale_f32_16x16x128_f8f6f4 v[150:153], v[16:23], v[40:47], v[150:153], v243, v243 op_sel_hi:[0,0,0]
	v_mfma_scale_f32_16x16x128_f8f6f4 v[118:121], v[24:31], v[40:47], v[118:121], v243, v243 op_sel_hi:[0,0,0]
	v_mfma_scale_f32_16x16x128_f8f6f4 v[88:91], v[16:23], v[48:55], v[88:91], v243, v243 op_sel_hi:[0,0,0]
	v_mfma_scale_f32_16x16x128_f8f6f4 v[80:83], v[24:31], v[48:55], v[80:83], v243, v243 op_sel_hi:[0,0,0]
	v_mfma_scale_f32_16x16x128_f8f6f4 v[72:75], v[16:23], v[56:63], v[72:75], v243, v243 op_sel_hi:[0,0,0]
	v_mfma_scale_f32_16x16x128_f8f6f4 v[64:67], v[24:31], v[56:63], v[64:67], v243, v243 op_sel_hi:[0,0,0]
	s_setprio 0
	s_barrier
	s_add_u32 s6, s6, 0x100
	s_addc_u32 s7, s7, 0
	s_cmp_ge_i32 s79, s13
	s_cbranch_scc1 .LBB0_1464
.LBB0_1461:
	v_add_u32_e32 v207, 0, v245
	v_add_u32_e32 v0, 0x10000, v207
	v_add_u32_e32 v12, 0x14000, v207
	v_xor_b32_e32 v31, 64, v0
	ds_read_b128 v[16:19], v0
	ds_read_b128 v[20:23], v31
	ds_read_b128 v[24:27], v0 offset:2048
	ds_read_b128 v[28:31], v31 offset:2048
	v_xor_b32_e32 v15, 64, v12
	ds_read_b128 v[0:3], v12
	ds_read_b128 v[4:7], v15
	ds_read_b128 v[8:11], v12 offset:2048
	ds_read_b128 v[12:15], v15 offset:2048
	s_cmp_eq_u32 s74, s79
	s_cselect_b64 s[46:47], -1, 0
	s_add_u32 s42, s18, s6
	s_addc_u32 s43, s19, s7
	s_add_u32 s42, s42, 0xffffff80
	s_addc_u32 s43, s43, -1
	v_add_u32_e32 v206, 0, v244
	v_xor_b32_e32 v39, 64, v206
	ds_read_b128 v[56:59], v206
	ds_read_b128 v[60:63], v39
	ds_read_b128 v[48:51], v206 offset:2048
	ds_read_b128 v[52:55], v39 offset:2048
	ds_read_b128 v[40:43], v206 offset:4096
	ds_read_b128 v[44:47], v39 offset:4096
	ds_read_b128 v[32:35], v206 offset:6144
	ds_read_b128 v[36:39], v39 offset:6144
	s_mov_b32 m0, s75
	s_nop 0
	global_load_lds_dwordx4 v214, s[42:43]
	s_add_i32 s44, s56, 0xe000
	s_mov_b32 m0, s44
	s_nop 0
	global_load_lds_dwordx4 v220, s[42:43]
	s_and_b64 s[42:43], s[40:41], s[46:47]
	s_andn2_b64 vcc, exec, s[42:43]
	s_cbranch_vccnz .LBB0_1460
	v_mov_b32_e32 v194, s35
	ds_read2_b32 v[194:195], v194 offset1:32
	s_waitcnt lgkmcnt(0)
	v_sub_u32_e32 v195, v195, v247
	v_lshlrev_b32_e32 v195, 8, v195
	v_add_u32_e32 v194, v195, v194
	v_min_i32_e32 v194, 0x100, v194
	v_add_u32_e32 v194, -1, v194
	v_min_i32_e32 v195, v199, v194
	v_min_i32_e32 v196, v201, v194
	v_min_i32_e32 v197, v222, v194
	v_min_i32_e32 v194, v223, v194
	v_lshl_add_u32 v195, v195, 2, s15
	v_lshl_add_u32 v196, v196, 2, s15
	v_lshl_add_u32 v197, v197, 2, s15
	v_lshl_add_u32 v194, v194, 2, s15
	ds_read_b32 v195, v195
	ds_read_b32 v196, v196
	ds_read_b32 v197, v197
	ds_read_b32 v194, v194
	s_waitcnt lgkmcnt(3)
	v_mad_u64_u32 v[218:219], s[42:43], v195, s12, v[96:97]
	s_waitcnt lgkmcnt(2)
	v_mad_u64_u32 v[216:217], s[42:43], v196, s12, v[200:201]
	s_waitcnt lgkmcnt(1)
	v_mad_u64_u32 v[214:215], s[42:43], v197, s12, v[96:97]
	s_waitcnt lgkmcnt(0)
	v_mad_u64_u32 v[220:221], s[42:43], v194, s12, v[200:201]
	s_branch .LBB0_1460

.LBB0_1551:
	s_or_b64 exec, exec, s[2:3]
	v_readlane_b32 s2, v253, 62
	s_waitcnt lgkmcnt(0)
	s_barrier
	v_mov_b32_e32 v0, s2
	ds_read_b32 v0, v0
	s_add_u32 s53, s8, 0x23b00000
	s_addc_u32 s54, s9, 0
	s_movk_i32 s12, 0x400
	v_mov_b32_e32 v1, v130
	s_waitcnt lgkmcnt(0)
	v_readfirstlane_b32 s2, v0
	s_lshl_b32 s55, s2, 2
	s_cmp_ge_i32 s90, s55
	v_readfirstlane_b32 s6, v1
	s_cbranch_scc1 .LBB0_1582
	v_bfe_i32 v3, v1, 27, 1
	v_lshlrev_b32_e32 v2, 4, v1
	v_lshrrev_b32_e32 v3, 22, v3
	v_add_u32_e32 v3, v2, v3
	v_and_b32_e32 v3, 0xfffffc00, v3
	v_sub_u32_e32 v3, v2, v3
	v_ashrrev_i32_e32 v0, 31, v1
	v_lshrrev_b32_e32 v4, 4, v3
	v_lshrrev_b32_e32 v0, 26, v0
	v_bitop3_b32 v3, v4, v3, 32 bitop3:0x6c
	v_add_u32_e32 v0, v1, v0
	v_ashrrev_i32_e32 v5, 31, v3
	v_ashrrev_i32_e32 v0, 6, v0
	v_lshrrev_b32_e32 v5, 26, v5
	v_lshlrev_b32_e32 v4, 3, v0
	v_add_u32_e32 v5, v3, v5
	v_and_b32_e32 v4, -16, v4
	v_ashrrev_i32_e32 v6, 6, v5
	v_and_b32_e32 v5, 0xc0, v5
	v_add_u32_e32 v4, v6, v4
	v_sub_u32_e32 v3, v3, v5
	v_lshlrev_b32_e32 v0, 5, v0
	v_ashrrev_i16_sdwa v3, v239, sext(v3) dst_sel:DWORD dst_unused:UNUSED_PAD src0_sel:DWORD src1_sel:BYTE_0
	v_lshlrev_b32_e32 v5, 1, v4
	v_lshlrev_b32_e32 v7, 2, v4
	v_lshrrev_b32_e32 v8, 2, v4
	v_and_b32_e32 v6, 3, v6
	v_and_b32_e32 v0, 32, v0
	v_bfe_i32 v3, v3, 0, 16
	v_and_b32_e32 v5, 0xffffffc0, v5
	v_and_b32_e32 v8, 4, v8
	v_and_or_b32 v6, v7, 48, v6
	v_or3_b32 v5, v6, v5, v8
	v_add_lshl_u32 v0, v0, v3, 1
	v_mad_u64_u32 v[132:133], s[4:5], v4, s12, v[0:1]
	v_mbcnt_lo_u32_b32 v68, -1, 0
	v_mbcnt_hi_u32_b32 v68, -1, v68
	v_add_u32_e32 v68, s93, v68
	v_lshrrev_b32_e32 v69, 3, v68
	v_lshrrev_b32_e32 v70, 4, v68
	v_xor_b32_e32 v70, v70, v68
	v_lshlrev_b32_e32 v70, 4, v70
	v_and_b32_e32 v70, 0x70, v70
	v_lshl_add_u32 v132, v69, 10, v70
	v_mad_u64_u32 v[134:135], s[4:5], v5, s12, v[0:1]
	v_mbcnt_lo_u32_b32 v68, -1, 0
	v_mbcnt_hi_u32_b32 v68, -1, v68
	v_add_u32_e32 v68, s93, v68
	v_lshrrev_b32_e32 v69, 3, v68
	v_and_b32_e32 v70, 0x60, v69
	v_lshlrev_b32_e32 v70, 1, v70
	v_and_or_b32 v70, v69, 3, v70
	v_and_b32_e32 v134, 12, v69
	v_lshl_or_b32 v70, v134, 2, v70
	v_lshrrev_b32_e32 v69, 2, v69
	v_and_b32_e32 v69, 4, v69
	v_or_b32_e32 v69, v69, v70
	v_lshrrev_b32_e32 v70, 4, v68
	v_xor_b32_e32 v70, v70, v68
	v_lshlrev_b32_e32 v70, 4, v70
	v_and_b32_e32 v70, 0x70, v70
	v_lshl_add_u32 v134, v69, 10, v70
	v_add_u32_e32 v0, 0x2000, v2
	v_ashrrev_i32_e32 v2, 31, v0
	v_lshrrev_b32_e32 v2, 22, v2
	v_add_u32_e32 v2, v0, v2
	v_ashrrev_i32_e32 v2, 10, v2
	v_mul_i32_i24_e32 v3, 0x400, v2
	v_sub_u32_e32 v0, v0, v3
	v_lshrrev_b32_e32 v3, 4, v0
	v_bitop3_b32 v0, v3, v0, 32 bitop3:0x6c
	v_ashrrev_i32_e32 v4, 31, v0
	v_lshrrev_b32_e32 v4, 26, v4
	v_lshlrev_b32_e32 v3, 3, v2
	v_add_u32_e32 v4, v0, v4
	v_and_b32_e32 v3, -16, v3
	v_ashrrev_i32_e32 v5, 6, v4
	v_and_b32_e32 v4, 0xc0, v4
	v_add_u32_e32 v3, v5, v3
	v_sub_u32_e32 v0, v0, v4
	v_lshlrev_b32_e32 v2, 5, v2
	v_ashrrev_i16_sdwa v0, v239, sext(v0) dst_sel:DWORD dst_unused:UNUSED_PAD src0_sel:DWORD src1_sel:BYTE_0
	v_lshlrev_b32_e32 v4, 1, v3
	v_lshlrev_b32_e32 v6, 2, v3
	v_lshrrev_b32_e32 v7, 2, v3
	v_and_b32_e32 v5, 3, v5
	v_and_b32_e32 v2, 32, v2
	v_bfe_i32 v0, v0, 0, 16
	v_and_b32_e32 v4, 0xffffffc0, v4
	v_and_b32_e32 v7, 4, v7
	v_and_or_b32 v5, v6, 48, v5
	v_or3_b32 v4, v5, v4, v7
	v_add_lshl_u32 v0, v2, v0, 1
	v_mad_u64_u32 v[136:137], s[4:5], v3, s12, v[0:1]
	v_mbcnt_lo_u32_b32 v68, -1, 0
	v_mbcnt_hi_u32_b32 v68, -1, v68
	v_add_u32_e32 v68, s93, v68
	v_lshrrev_b32_e32 v69, 3, v68
	v_add_u32_e32 v69, 64, v69
	v_lshrrev_b32_e32 v70, 4, v68
	v_xor_b32_e32 v70, v70, v68
	v_lshlrev_b32_e32 v70, 4, v70
	v_and_b32_e32 v70, 0x70, v70
	v_lshl_add_u32 v136, v69, 10, v70
	v_mad_u64_u32 v[138:139], s[4:5], v4, s12, v[0:1]
	v_mbcnt_lo_u32_b32 v68, -1, 0
	v_mbcnt_hi_u32_b32 v68, -1, v68
	v_add_u32_e32 v68, s93, v68
	v_lshrrev_b32_e32 v69, 3, v68
	v_add_u32_e32 v69, 64, v69
	v_and_b32_e32 v70, 0x60, v69
	v_lshlrev_b32_e32 v70, 1, v70
	v_and_or_b32 v70, v69, 3, v70
	v_and_b32_e32 v138, 12, v69
	v_lshl_or_b32 v70, v138, 2, v70
	v_lshrrev_b32_e32 v69, 2, v69
	v_and_b32_e32 v69, 4, v69
	v_or_b32_e32 v69, v69, v70
	v_lshrrev_b32_e32 v70, 4, v68
	v_xor_b32_e32 v70, v70, v68
	v_lshlrev_b32_e32 v70, 4, v70
	v_and_b32_e32 v70, 0x70, v70
	v_lshl_add_u32 v138, v69, 10, v70
	v_readlane_b32 s4, v253, 4
	s_lshl_b32 s86, s44, 15
	s_lshl_b64 s[2:3], s[86:87], 10
	v_mov_b32_e32 v0, s4
	ds_read_b32 v152, v0 offset:1792
	s_add_u32 s56, s53, s2
	s_addc_u32 s57, s54, s3
	v_readlane_b32 s19, v254, 16
	s_add_u32 s58, s8, 0x4e500000
	s_waitcnt lgkmcnt(0)
	v_lshlrev_b32_e32 v0, 2, v152
	v_add_u32_e32 v0, 0, v0
	v_add_u32_e32 v0, 0x20600, v0
	ds_read_b32 v0, v0
	v_mov_b32_e32 v2, s19
	v_readfirstlane_b32 s19, v152
	s_addc_u32 s59, s9, 0
	s_ashr_i32 s13, s12, 31
	ds_read_b32 v2, v2
	s_waitcnt lgkmcnt(1)
	v_readfirstlane_b32 s4, v0
	s_lshl_b32 s19, s19, 8
	s_ashr_i32 s7, s6, 6
	s_ashr_i32 s5, s4, 31
	s_mul_i32 s20, s19, s13
	s_mul_hi_u32 s21, s19, s12
	s_ashr_i32 s24, s6, 8
	s_lshl_b64 s[14:15], s[12:13], 3
	s_lshl_b64 s[16:17], s[12:13], 7
	s_lshl_b32 s18, s7, 10
	s_add_i32 s21, s21, s20
	s_lshl_b64 s[4:5], s[4:5], 20
	s_add_u32 s4, s56, s4
	s_addc_u32 s5, s57, s5
	v_readlane_b32 s22, v253, 7
	v_readlane_b32 s23, v253, 8
	s_add_u32 s40, s4, s22
	s_addc_u32 s41, s5, s23
	s_add_i32 s60, s18, 0
	s_load_dwordx2 s[2:3], s[10:11], 0x78
	s_add_i32 s61, s60, 0x10000
	s_mov_b32 m0, s61
	s_nop 0
	global_load_lds_dwordx4 v134, s[40:41]
	s_add_i32 s62, s60, 0x12000
	s_mov_b32 m0, s62
	s_nop 0
	global_load_lds_dwordx4 v138, s[40:41]
	s_add_u32 s4, s40, s14
	s_mul_i32 s19, s19, s12
	s_addc_u32 s5, s41, s15
	s_add_i32 s63, s60, 0x14000
	s_mov_b32 m0, s63
	s_nop 0
	global_load_lds_dwordx4 v134, s[4:5]
	s_add_i32 s64, s60, 0x16000
	s_mov_b32 m0, s64
	s_nop 0
	global_load_lds_dwordx4 v138, s[4:5]
	s_add_u32 s42, s58, s19
	s_addc_u32 s43, s59, s21
	s_mov_b32 m0, s60
	s_nop 0
	global_load_lds_dwordx4 v132, s[42:43]
	s_add_i32 s65, s60, 0x2000
	s_mov_b32 m0, s65
	s_nop 0
	global_load_lds_dwordx4 v136, s[42:43]
	s_add_u32 s18, s42, s16
	s_addc_u32 s19, s43, s17
	s_add_i32 s66, s60, 0x4000
	s_mov_b32 m0, s66
	s_nop 0
	global_load_lds_dwordx4 v132, s[18:19]
	s_add_i32 s67, s60, 0x6000
	s_mov_b32 m0, s67
	s_nop 0
	global_load_lds_dwordx4 v136, s[18:19]
	s_cmp_eq_u32 s24, 1
	s_cselect_b64 s[18:19], -1, 0
	s_cmp_lg_u32 s24, 1
	s_cbranch_scc1 .LBB0_1554
	s_barrier
.LBB0_1554:
	v_readlane_b32 s20, v253, 3
	v_and_b32_e32 v3, 63, v1
	v_bfe_u32 v96, v1, 4, 2
	s_waitcnt lgkmcnt(0)
	v_cmp_ge_i32_e32 vcc, s20, v2
	s_add_u32 s20, s8, 0x57500000
	s_addc_u32 s21, s9, 0
	s_lshl_b64 s[22:23], s[86:87], 2
	s_add_u32 s22, s2, s22
	s_addc_u32 s23, s3, s23
	s_lshr_b32 s2, s13, 25
	v_and_b32_e32 v131, 15, v1
	s_add_i32 s2, s12, s2
	v_and_b32_e32 v4, 48, v1
	v_lshlrev_b32_e32 v1, 2, v1
	s_and_b32 s7, s7, 3
	s_ashr_i32 s68, s2, 7
	s_lshl_b32 s2, s24, 13
	v_lshl_or_b32 v4, v131, 6, v4
	v_and_b32_e32 v1, 32, v1
	s_lshl_b32 s69, s24, 6
	v_bitop3_b32 v133, v4, s2, v1 bitop3:0xde
	v_mbcnt_lo_u32_b32 v68, -1, 0
	v_mbcnt_hi_u32_b32 v68, -1, v68
	v_add_u32_e32 v68, s93, v68
	v_bfe_u32 v69, v68, 4, 2
	v_bfe_u32 v70, v68, 1, 3
	v_xor_b32_e32 v69, v69, v70
	v_lshlrev_b32_e32 v69, 4, v69
	v_and_b32_e32 v70, 15, v68
	v_lshl_or_b32 v69, v70, 7, v69
	v_lshrrev_b32_e32 v70, 8, v68
	v_lshl_or_b32 v133, v70, 13, v69
	s_lshl_b32 s2, s7, 12
	v_bitop3_b32 v135, v4, s2, v1 bitop3:0xde
	v_mbcnt_lo_u32_b32 v68, -1, 0
	v_mbcnt_hi_u32_b32 v68, -1, v68
	v_add_u32_e32 v68, s93, v68
	v_bfe_u32 v69, v68, 4, 2
	v_bfe_u32 v70, v68, 1, 3
	v_xor_b32_e32 v69, v69, v70
	v_lshlrev_b32_e32 v69, 4, v69
	v_and_b32_e32 v70, 15, v68
	v_lshl_or_b32 v69, v70, 7, v69
	v_bfe_u32 v70, v68, 6, 2
	v_lshl_or_b32 v135, v70, 12, v69
	s_add_u32 s2, s40, 0x80
	s_waitcnt vmcnt(2)
	s_barrier
	s_addc_u32 s3, s41, 0
	s_add_i32 s70, s60, 0x18000
	s_mov_b32 m0, s70
	s_nop 0
	global_load_lds_dwordx4 v134, s[2:3]
	s_add_i32 s71, s60, 0x1a000
	s_mov_b32 m0, s71
	s_nop 0
	global_load_lds_dwordx4 v138, s[2:3]
	s_add_u32 s2, s42, 0x80
	s_addc_u32 s3, s43, 0
	s_add_i32 s72, s60, 0x8000
	s_mov_b32 m0, s72
	s_nop 0
	global_load_lds_dwordx4 v132, s[2:3]
	s_add_i32 s73, s60, 0xa000
	s_mov_b32 m0, s73
	s_nop 0
	global_load_lds_dwordx4 v136, s[2:3]
	s_add_u32 s2, s4, 0x80
	s_addc_u32 s3, s5, 0
	s_add_i32 s74, s60, 0x1c000
	s_add_i32 s75, s60, 0x1e000
	s_cmp_lt_u32 s6, 64
	s_cselect_b64 s[24:25], -1, 0
	s_cmpk_gt_i32 s12, 0x7f
	s_mov_b32 m0, s74
	s_nop 0
	global_load_lds_dwordx4 v134, s[2:3]
	s_cselect_b64 s[26:27], -1, 0
	s_add_i32 s76, s68, -2
	s_add_i32 s77, s60, 0xc000
	s_mov_b32 m0, s75
	s_nop 0
	global_load_lds_dwordx4 v138, s[2:3]
	s_cmpk_lt_u32 s6, 0x100
	s_waitcnt vmcnt(6)
	s_cselect_b64 s[28:29], -1, 0
	s_lshl_b32 s2, s7, 8
	s_add_i32 s79, s2, 0
	v_readlane_b32 s2, v253, 5
	v_cndmask_b32_e64 v2, 0, 1, vcc
	v_lshlrev_b32_e32 v137, 4, v3
	s_lshl_b32 s78, s7, 6
	s_add_i32 s79, s79, 0x21000
	s_mov_b32 s80, 0
	s_mov_b32 s82, s2
	s_barrier
	v_readlane_b32 s3, v253, 6
	s_branch .LBB0_1557

.LBB0_1566:
	v_add_u32_e32 v144, 0, v135
	v_add_u32_e32 v76, 0x10000, v144
	v_add_u32_e32 v92, 0x14000, v144
	v_xor_b32_e32 v79, 64, v76
	ds_read_b128 v[64:67], v76
	ds_read_b128 v[68:71], v79
	ds_read_b128 v[72:75], v76 offset:2048
	ds_read_b128 v[76:79], v79 offset:2048
	v_xor_b32_e32 v95, 64, v92
	ds_read_b128 v[80:83], v92
	ds_read_b128 v[84:87], v95
	ds_read_b128 v[88:91], v92 offset:2048
	ds_read_b128 v[92:95], v95 offset:2048
	s_add_i32 s88, s46, 2
	s_cmp_eq_u32 s76, s46
	s_cselect_b32 s48, s38, s86
	s_cselect_b32 s49, s39, s87
	s_cselect_b32 s50, s36, s84
	s_cselect_b32 s51, s37, s85
	s_add_u32 s46, s48, 0x80
	s_addc_u32 s47, s49, 0
	v_add_u32_e32 v145, 0, v133
	v_xor_b32_e32 v129, 64, v145
	ds_read_b128 v[98:101], v145
	ds_read_b128 v[102:105], v129
	ds_read_b128 v[106:109], v145 offset:2048
	ds_read_b128 v[110:113], v129 offset:2048
	ds_read_b128 v[114:117], v145 offset:4096
	ds_read_b128 v[118:121], v129 offset:4096
	ds_read_b128 v[122:125], v145 offset:6144
	ds_read_b128 v[126:129], v129 offset:6144
	s_mov_b32 m0, s77
	s_nop 0
	global_load_lds_dwordx4 v132, s[44:45]
	s_add_i32 s89, s60, 0xe000
	s_mov_b32 m0, s89
	s_nop 0
	global_load_lds_dwordx4 v136, s[44:45]
	s_waitcnt vmcnt(8)
	s_waitcnt lgkmcnt(0)
	s_barrier
	s_setprio 1
	s_waitcnt lgkmcnt(6)
	v_mfma_scale_f32_16x16x128_f8f6f4 v[60:63], v[64:71], v[98:105], v[60:63], v243, v243 op_sel_hi:[0,0,0]
	v_mfma_scale_f32_16x16x128_f8f6f4 v[56:59], v[72:79], v[98:105], v[56:59], v243, v243 op_sel_hi:[0,0,0]
	s_waitcnt lgkmcnt(4)
	v_mfma_scale_f32_16x16x128_f8f6f4 v[44:47], v[64:71], v[106:113], v[44:47], v243, v243 op_sel_hi:[0,0,0]
	v_mfma_scale_f32_16x16x128_f8f6f4 v[40:43], v[72:79], v[106:113], v[40:43], v243, v243 op_sel_hi:[0,0,0]
	s_waitcnt lgkmcnt(2)
	v_mfma_scale_f32_16x16x128_f8f6f4 v[28:31], v[64:71], v[114:121], v[28:31], v243, v243 op_sel_hi:[0,0,0]
	v_mfma_scale_f32_16x16x128_f8f6f4 v[24:27], v[72:79], v[114:121], v[24:27], v243, v243 op_sel_hi:[0,0,0]
	s_waitcnt lgkmcnt(0)
	v_mfma_scale_f32_16x16x128_f8f6f4 v[12:15], v[64:71], v[122:129], v[12:15], v243, v243 op_sel_hi:[0,0,0]
	v_mfma_scale_f32_16x16x128_f8f6f4 v[8:11], v[72:79], v[122:129], v[8:11], v243, v243 op_sel_hi:[0,0,0]
	s_setprio 0
	s_setprio 1
	v_mfma_scale_f32_16x16x128_f8f6f4 v[52:55], v[80:87], v[98:105], v[52:55], v243, v243 op_sel_hi:[0,0,0]
	v_mfma_scale_f32_16x16x128_f8f6f4 v[48:51], v[88:95], v[98:105], v[48:51], v243, v243 op_sel_hi:[0,0,0]
	v_mfma_scale_f32_16x16x128_f8f6f4 v[140:143], v[80:87], v[106:113], v[36:39], v243, v243 op_sel_hi:[0,0,0]
	v_mfma_scale_f32_16x16x128_f8f6f4 v[106:109], v[88:95], v[106:113], v[32:35], v243, v243 op_sel_hi:[0,0,0]
	v_mfma_scale_f32_16x16x128_f8f6f4 v[110:113], v[80:87], v[114:121], v[20:23], v243, v243 op_sel_hi:[0,0,0]
	v_mfma_scale_f32_16x16x128_f8f6f4 v[114:117], v[88:95], v[114:121], v[16:19], v243, v243 op_sel_hi:[0,0,0]
	v_mfma_scale_f32_16x16x128_f8f6f4 v[118:121], v[80:87], v[122:129], v[4:7], v243, v243 op_sel_hi:[0,0,0]
	v_mfma_scale_f32_16x16x128_f8f6f4 v[122:125], v[88:95], v[122:129], v[0:3], v243, v243 op_sel_hi:[0,0,0]
	s_setprio 0
	s_barrier
	s_mov_b32 m0, s61
	s_nop 0
	global_load_lds_dwordx4 v134, s[50:51]
	s_add_u32 s90, s50, s14
	s_mov_b32 m0, s62
	s_nop 0
	global_load_lds_dwordx4 v138, s[50:51]
	s_addc_u32 s91, s51, s15
	s_mov_b32 m0, s63
	s_nop 0
	global_load_lds_dwordx4 v134, s[90:91]
	s_nop 0
	s_mov_b32 m0, s64
	s_nop 0
	global_load_lds_dwordx4 v138, s[90:91]
	s_nop 0
	s_mov_b32 m0, s60
	s_nop 0
	global_load_lds_dwordx4 v132, s[48:49]
	s_nop 0
	s_mov_b32 m0, s65
	s_nop 0
	global_load_lds_dwordx4 v136, s[48:49]
	s_waitcnt vmcnt(8)
	s_waitcnt lgkmcnt(0)
	s_barrier
	s_barrier
	v_add_u32_e32 v20, 0x18000, v144
	v_add_u32_e32 v32, 0x1c000, v144
	v_xor_b32_e32 v23, 64, v20
	ds_read_b128 v[0:3], v20
	ds_read_b128 v[4:7], v23
	ds_read_b128 v[16:19], v20 offset:2048
	ds_read_b128 v[20:23], v23 offset:2048
	v_xor_b32_e32 v79, 64, v32
	ds_read_b128 v[64:67], v32
	ds_read_b128 v[68:71], v79
	ds_read_b128 v[72:75], v32 offset:2048
	ds_read_b128 v[76:79], v79 offset:2048
	v_xor_b32_e32 v105, 64, v145
	ds_read_b128 v[32:35], v145 offset:32768
	ds_read_b128 v[36:39], v105 offset:32768
	ds_read_b128 v[80:83], v145 offset:34816
	ds_read_b128 v[84:87], v105 offset:34816
	ds_read_b128 v[88:91], v145 offset:36864
	ds_read_b128 v[92:95], v105 offset:36864
	ds_read_b128 v[98:101], v145 offset:38912
	ds_read_b128 v[102:105], v105 offset:38912
	s_add_u32 s48, s48, s16
	s_addc_u32 s49, s49, s17
	s_mov_b32 m0, s66
	s_nop 0
	global_load_lds_dwordx4 v132, s[48:49]
	s_nop 0
	s_mov_b32 m0, s67
	s_nop 0
	global_load_lds_dwordx4 v136, s[48:49]
	s_waitcnt vmcnt(8)
	s_waitcnt lgkmcnt(0)
	s_barrier
	s_setprio 1
	s_waitcnt lgkmcnt(6)
	v_mfma_scale_f32_16x16x128_f8f6f4 v[60:63], v[0:7], v[32:39], v[60:63], v243, v243 op_sel_hi:[0,0,0]
	v_mfma_scale_f32_16x16x128_f8f6f4 v[56:59], v[16:23], v[32:39], v[56:59], v243, v243 op_sel_hi:[0,0,0]
	s_waitcnt lgkmcnt(4)
	v_mfma_scale_f32_16x16x128_f8f6f4 v[44:47], v[0:7], v[80:87], v[44:47], v243, v243 op_sel_hi:[0,0,0]
	v_mfma_scale_f32_16x16x128_f8f6f4 v[40:43], v[16:23], v[80:87], v[40:43], v243, v243 op_sel_hi:[0,0,0]
	s_waitcnt lgkmcnt(2)
	v_mfma_scale_f32_16x16x128_f8f6f4 v[28:31], v[0:7], v[88:95], v[28:31], v243, v243 op_sel_hi:[0,0,0]
	v_mfma_scale_f32_16x16x128_f8f6f4 v[24:27], v[16:23], v[88:95], v[24:27], v243, v243 op_sel_hi:[0,0,0]
	s_waitcnt lgkmcnt(0)
	v_mfma_scale_f32_16x16x128_f8f6f4 v[12:15], v[0:7], v[98:105], v[12:15], v243, v243 op_sel_hi:[0,0,0]
	v_mfma_scale_f32_16x16x128_f8f6f4 v[8:11], v[16:23], v[98:105], v[8:11], v243, v243 op_sel_hi:[0,0,0]
	s_setprio 0
	s_setprio 1
	v_mfma_scale_f32_16x16x128_f8f6f4 v[52:55], v[64:71], v[32:39], v[52:55], v243, v243 op_sel_hi:[0,0,0]
	s_add_u32 s48, s50, 0x80
	s_addc_u32 s49, s51, 0
	v_mfma_scale_f32_16x16x128_f8f6f4 v[48:51], v[72:79], v[32:39], v[48:51], v243, v243 op_sel_hi:[0,0,0]
	v_mfma_scale_f32_16x16x128_f8f6f4 v[36:39], v[64:71], v[80:87], v[140:143], v243, v243 op_sel_hi:[0,0,0]
	v_mfma_scale_f32_16x16x128_f8f6f4 v[32:35], v[72:79], v[80:87], v[106:109], v243, v243 op_sel_hi:[0,0,0]
	v_mfma_scale_f32_16x16x128_f8f6f4 v[20:23], v[64:71], v[88:95], v[110:113], v243, v243 op_sel_hi:[0,0,0]
	v_mfma_scale_f32_16x16x128_f8f6f4 v[16:19], v[72:79], v[88:95], v[114:117], v243, v243 op_sel_hi:[0,0,0]
	v_mfma_scale_f32_16x16x128_f8f6f4 v[4:7], v[64:71], v[98:105], v[118:121], v243, v243 op_sel_hi:[0,0,0]
	v_mfma_scale_f32_16x16x128_f8f6f4 v[0:3], v[72:79], v[98:105], v[122:125], v243, v243 op_sel_hi:[0,0,0]
	s_setprio 0
	s_barrier
	s_mov_b32 m0, s70
	s_nop 0
	global_load_lds_dwordx4 v134, s[48:49]
	s_nop 0
	s_mov_b32 m0, s71
	s_nop 0
	global_load_lds_dwordx4 v138, s[48:49]
	s_add_u32 s48, s48, s14
	s_addc_u32 s49, s49, s15
	s_mov_b32 m0, s74
	s_nop 0
	global_load_lds_dwordx4 v134, s[48:49]
	s_nop 0
	s_mov_b32 m0, s75
	s_nop 0
	global_load_lds_dwordx4 v138, s[48:49]
	s_mov_b32 m0, s72
	s_nop 0
	global_load_lds_dwordx4 v132, s[46:47]
	s_nop 0
	s_mov_b32 m0, s73
	s_nop 0
	global_load_lds_dwordx4 v136, s[46:47]
	s_waitcnt vmcnt(8)
	s_waitcnt lgkmcnt(0)
	s_barrier
	s_barrier
	s_add_u32 s84, s84, 0x100
	s_addc_u32 s85, s85, 0
	s_add_u32 s86, s86, 0x100
	s_addc_u32 s87, s87, 0
	s_add_u32 s44, s44, 0x100
	s_addc_u32 s45, s45, 0
	s_cmp_ge_i32 s88, s68
	s_mov_b32 s46, s88
	s_cbranch_scc0 .LBB0_1566
	v_readlane_b32 s88, v252, 6
	v_readlane_b32 s46, v254, 34
	v_readlane_b32 s90, v254, 25
	v_readlane_b32 s89, v252, 7
	v_readlane_b32 s84, v254, 31
	s_mov_b32 s87, s95
	v_readlane_b32 s47, v254, 35
	v_readlane_b32 s91, v254, 26
	v_readlane_b32 s85, v254, 32

.LBB0_1572:
	v_add_u32_e32 v153, 0, v135
	v_add_u32_e32 v148, 0x10000, v153
	v_xor_b32_e32 v161, 64, v148
	ds_read_b128 v[140:143], v148
	ds_read_b128 v[144:147], v161
	ds_read_b128 v[154:157], v148 offset:2048
	ds_read_b128 v[158:161], v161 offset:2048
	v_add_u32_e32 v148, 0x14000, v153
	v_xor_b32_e32 v177, 64, v148
	ds_read_b128 v[162:165], v148
	ds_read_b128 v[166:169], v177
	ds_read_b128 v[170:173], v148 offset:2048
	ds_read_b128 v[174:177], v177 offset:2048
	s_add_i32 s31, s35, 2
	s_cmp_eq_u32 s76, s35
	s_cselect_b32 s44, s38, s48
	s_cselect_b32 s45, s39, s49
	s_cselect_b32 s42, s36, s46
	s_cselect_b32 s43, s37, s47
	s_add_u32 s40, s44, 0x80
	s_addc_u32 s41, s45, 0
	v_add_u32_e32 v238, 0, v133
	v_xor_b32_e32 v213, 64, v238
	ds_read_b128 v[178:181], v238
	ds_read_b128 v[182:185], v213
	ds_read_b128 v[186:189], v238 offset:2048
	ds_read_b128 v[190:193], v213 offset:2048
	ds_read_b128 v[198:201], v238 offset:4096
	ds_read_b128 v[202:205], v213 offset:4096
	ds_read_b128 v[206:209], v238 offset:6144
	ds_read_b128 v[210:213], v213 offset:6144
	s_mov_b32 m0, s77
	s_nop 0
	global_load_lds_dwordx4 v132, s[6:7]
	s_add_i32 s35, s60, 0xe000
	s_mov_b32 m0, s35
	s_nop 0
	global_load_lds_dwordx4 v136, s[6:7]
	s_waitcnt vmcnt(8)
	s_waitcnt lgkmcnt(0)
	s_barrier
	s_setprio 1
	s_waitcnt lgkmcnt(6)
	v_mfma_scale_f32_16x16x128_f8f6f4 v[60:63], v[140:147], v[178:185], v[60:63], v243, v243 op_sel_hi:[0,0,0]
	v_mfma_scale_f32_16x16x128_f8f6f4 v[56:59], v[154:161], v[178:185], v[56:59], v243, v243 op_sel_hi:[0,0,0]
	s_waitcnt lgkmcnt(4)
	v_mfma_scale_f32_16x16x128_f8f6f4 v[44:47], v[140:147], v[186:193], v[44:47], v243, v243 op_sel_hi:[0,0,0]
	v_mfma_scale_f32_16x16x128_f8f6f4 v[40:43], v[154:161], v[186:193], v[40:43], v243, v243 op_sel_hi:[0,0,0]
	s_waitcnt lgkmcnt(2)
	v_mfma_scale_f32_16x16x128_f8f6f4 v[148:151], v[140:147], v[198:205], v[28:31], v243, v243 op_sel_hi:[0,0,0]
	v_mfma_scale_f32_16x16x128_f8f6f4 v[194:197], v[154:161], v[198:205], v[24:27], v243, v243 op_sel_hi:[0,0,0]
	s_waitcnt lgkmcnt(0)
	v_mfma_scale_f32_16x16x128_f8f6f4 v[214:217], v[140:147], v[206:213], v[12:15], v243, v243 op_sel_hi:[0,0,0]
	v_mfma_scale_f32_16x16x128_f8f6f4 v[218:221], v[154:161], v[206:213], v[8:11], v243, v243 op_sel_hi:[0,0,0]
	s_setprio 0
	s_setprio 1
	v_mfma_scale_f32_16x16x128_f8f6f4 v[52:55], v[162:169], v[178:185], v[52:55], v243, v243 op_sel_hi:[0,0,0]
	v_mfma_scale_f32_16x16x128_f8f6f4 v[48:51], v[170:177], v[178:185], v[48:51], v243, v243 op_sel_hi:[0,0,0]
	v_mfma_scale_f32_16x16x128_f8f6f4 v[36:39], v[162:169], v[186:193], v[36:39], v243, v243 op_sel_hi:[0,0,0]
	v_mfma_scale_f32_16x16x128_f8f6f4 v[32:35], v[170:177], v[186:193], v[32:35], v243, v243 op_sel_hi:[0,0,0]
	v_mfma_scale_f32_16x16x128_f8f6f4 v[178:181], v[162:169], v[198:205], v[20:23], v243, v243 op_sel_hi:[0,0,0]
	v_mfma_scale_f32_16x16x128_f8f6f4 v[182:185], v[170:177], v[198:205], v[16:19], v243, v243 op_sel_hi:[0,0,0]
	v_mfma_scale_f32_16x16x128_f8f6f4 v[186:189], v[162:169], v[206:213], v[4:7], v243, v243 op_sel_hi:[0,0,0]
	v_mfma_scale_f32_16x16x128_f8f6f4 v[190:193], v[170:177], v[206:213], v[0:3], v243, v243 op_sel_hi:[0,0,0]
	s_setprio 0
	s_barrier
	s_nop 4
	v_xor_b32_e32 v31, 64, v238
	ds_read_b128 v[0:3], v238 offset:16384
	ds_read_b128 v[4:7], v31 offset:16384
	ds_read_b128 v[8:11], v238 offset:18432
	ds_read_b128 v[12:15], v31 offset:18432
	ds_read_b128 v[16:19], v238 offset:20480
	ds_read_b128 v[20:23], v31 offset:20480
	ds_read_b128 v[24:27], v238 offset:22528
	ds_read_b128 v[28:31], v31 offset:22528
	s_mov_b32 m0, s61
	s_nop 0
	global_load_lds_dwordx4 v134, s[42:43]
	s_add_u32 s50, s42, s14
	s_mov_b32 m0, s62
	s_nop 0
	global_load_lds_dwordx4 v138, s[42:43]
	s_addc_u32 s51, s43, s15
	s_mov_b32 m0, s63
	s_nop 0
	global_load_lds_dwordx4 v134, s[50:51]
	s_nop 0
	s_mov_b32 m0, s64
	s_nop 0
	global_load_lds_dwordx4 v138, s[50:51]
	s_nop 0
	s_mov_b32 m0, s60
	s_nop 0
	global_load_lds_dwordx4 v132, s[44:45]
	s_nop 0
	s_mov_b32 m0, s65
	s_nop 0
	global_load_lds_dwordx4 v136, s[44:45]
	s_waitcnt vmcnt(8)
	s_waitcnt lgkmcnt(0)
	s_barrier
	s_setprio 1
	s_waitcnt lgkmcnt(6)
	v_mfma_scale_f32_16x16x128_f8f6f4 v[126:129], v[140:147], v[0:7], v[126:129], v243, v243 op_sel_hi:[0,0,0]
	v_mfma_scale_f32_16x16x128_f8f6f4 v[122:125], v[154:161], v[0:7], v[122:125], v243, v243 op_sel_hi:[0,0,0]
	s_waitcnt lgkmcnt(4)
	v_mfma_scale_f32_16x16x128_f8f6f4 v[118:121], v[140:147], v[8:15], v[118:121], v243, v243 op_sel_hi:[0,0,0]
	v_mfma_scale_f32_16x16x128_f8f6f4 v[114:117], v[154:161], v[8:15], v[114:117], v243, v243 op_sel_hi:[0,0,0]
	s_waitcnt lgkmcnt(2)
	v_mfma_scale_f32_16x16x128_f8f6f4 v[106:109], v[140:147], v[16:23], v[106:109], v243, v243 op_sel_hi:[0,0,0]
	v_mfma_scale_f32_16x16x128_f8f6f4 v[98:101], v[154:161], v[16:23], v[98:101], v243, v243 op_sel_hi:[0,0,0]
	s_waitcnt lgkmcnt(0)
	v_mfma_scale_f32_16x16x128_f8f6f4 v[198:201], v[140:147], v[24:31], v[88:91], v243, v243 op_sel_hi:[0,0,0]
	v_mfma_scale_f32_16x16x128_f8f6f4 v[202:205], v[154:161], v[24:31], v[80:83], v243, v243 op_sel_hi:[0,0,0]
	s_setprio 0
	s_setprio 1
	v_mfma_scale_f32_16x16x128_f8f6f4 v[110:113], v[162:169], v[0:7], v[110:113], v243, v243 op_sel_hi:[0,0,0]
	v_mfma_scale_f32_16x16x128_f8f6f4 v[102:105], v[170:177], v[0:7], v[102:105], v243, v243 op_sel_hi:[0,0,0]
	v_mfma_scale_f32_16x16x128_f8f6f4 v[206:209], v[162:169], v[8:15], v[92:95], v243, v243 op_sel_hi:[0,0,0]
	v_mfma_scale_f32_16x16x128_f8f6f4 v[210:213], v[170:177], v[8:15], v[84:87], v243, v243 op_sel_hi:[0,0,0]
	v_mfma_scale_f32_16x16x128_f8f6f4 v[222:225], v[162:169], v[16:23], v[76:79], v243, v243 op_sel_hi:[0,0,0]
	v_mfma_scale_f32_16x16x128_f8f6f4 v[226:229], v[170:177], v[16:23], v[72:75], v243, v243 op_sel_hi:[0,0,0]
	v_mfma_scale_f32_16x16x128_f8f6f4 v[230:233], v[162:169], v[24:31], v[68:71], v243, v243 op_sel_hi:[0,0,0]
	v_mfma_scale_f32_16x16x128_f8f6f4 v[234:237], v[170:177], v[24:31], v[64:67], v243, v243 op_sel_hi:[0,0,0]
	s_setprio 0
	s_barrier
	v_add_u32_e32 v0, 0x18000, v153
	s_nop 3
	v_xor_b32_e32 v79, 64, v0
	ds_read_b128 v[64:67], v0
	ds_read_b128 v[68:71], v79
	ds_read_b128 v[72:75], v0 offset:2048
	ds_read_b128 v[76:79], v79 offset:2048
	v_add_u32_e32 v0, 0x1c000, v153
	v_xor_b32_e32 v161, 64, v0
	ds_read_b128 v[140:143], v0
	ds_read_b128 v[144:147], v161
	ds_read_b128 v[154:157], v0 offset:2048
	ds_read_b128 v[158:161], v161 offset:2048
	v_xor_b32_e32 v95, 64, v238
	ds_read_b128 v[0:3], v238 offset:32768
	ds_read_b128 v[4:7], v95 offset:32768
	ds_read_b128 v[16:19], v238 offset:34816
	ds_read_b128 v[20:23], v95 offset:34816
	ds_read_b128 v[80:83], v238 offset:36864
	ds_read_b128 v[84:87], v95 offset:36864
	ds_read_b128 v[88:91], v238 offset:38912
	ds_read_b128 v[92:95], v95 offset:38912
	s_add_u32 s44, s44, s16
	s_addc_u32 s45, s45, s17
	s_mov_b32 m0, s66
	s_nop 0
	global_load_lds_dwordx4 v132, s[44:45]
	s_nop 0
	s_mov_b32 m0, s67
	s_nop 0
	global_load_lds_dwordx4 v136, s[44:45]
	s_waitcnt vmcnt(8)
	s_waitcnt lgkmcnt(0)
	s_barrier
	s_setprio 1
	s_waitcnt lgkmcnt(6)
	v_mfma_scale_f32_16x16x128_f8f6f4 v[60:63], v[64:71], v[0:7], v[60:63], v243, v243 op_sel_hi:[0,0,0]
	v_mfma_scale_f32_16x16x128_f8f6f4 v[56:59], v[72:79], v[0:7], v[56:59], v243, v243 op_sel_hi:[0,0,0]
	s_waitcnt lgkmcnt(4)
	v_mfma_scale_f32_16x16x128_f8f6f4 v[44:47], v[64:71], v[16:23], v[44:47], v243, v243 op_sel_hi:[0,0,0]
	v_mfma_scale_f32_16x16x128_f8f6f4 v[40:43], v[72:79], v[16:23], v[40:43], v243, v243 op_sel_hi:[0,0,0]
	s_waitcnt lgkmcnt(2)
	v_mfma_scale_f32_16x16x128_f8f6f4 v[28:31], v[64:71], v[80:87], v[148:151], v243, v243 op_sel_hi:[0,0,0]
	v_mfma_scale_f32_16x16x128_f8f6f4 v[24:27], v[72:79], v[80:87], v[194:197], v243, v243 op_sel_hi:[0,0,0]
	s_waitcnt lgkmcnt(0)
	v_mfma_scale_f32_16x16x128_f8f6f4 v[12:15], v[64:71], v[88:95], v[214:217], v243, v243 op_sel_hi:[0,0,0]
	v_mfma_scale_f32_16x16x128_f8f6f4 v[8:11], v[72:79], v[88:95], v[218:221], v243, v243 op_sel_hi:[0,0,0]
	s_setprio 0
	s_setprio 1
	v_mfma_scale_f32_16x16x128_f8f6f4 v[52:55], v[140:147], v[0:7], v[52:55], v243, v243 op_sel_hi:[0,0,0]
	v_mfma_scale_f32_16x16x128_f8f6f4 v[48:51], v[154:161], v[0:7], v[48:51], v243, v243 op_sel_hi:[0,0,0]
	v_mfma_scale_f32_16x16x128_f8f6f4 v[36:39], v[140:147], v[16:23], v[36:39], v243, v243 op_sel_hi:[0,0,0]
	v_mfma_scale_f32_16x16x128_f8f6f4 v[32:35], v[154:161], v[16:23], v[32:35], v243, v243 op_sel_hi:[0,0,0]
	v_mfma_scale_f32_16x16x128_f8f6f4 v[20:23], v[140:147], v[80:87], v[178:181], v243, v243 op_sel_hi:[0,0,0]
	v_mfma_scale_f32_16x16x128_f8f6f4 v[16:19], v[154:161], v[80:87], v[182:185], v243, v243 op_sel_hi:[0,0,0]
	v_mfma_scale_f32_16x16x128_f8f6f4 v[4:7], v[140:147], v[88:95], v[186:189], v243, v243 op_sel_hi:[0,0,0]
	v_mfma_scale_f32_16x16x128_f8f6f4 v[0:3], v[154:161], v[88:95], v[190:193], v243, v243 op_sel_hi:[0,0,0]
	s_setprio 0
	s_barrier
	v_xor_b32_e32 v193, 64, v238
	ds_read_b128 v[162:165], v238 offset:49152
	ds_read_b128 v[166:169], v193 offset:49152
	ds_read_b128 v[170:173], v238 offset:51200
	ds_read_b128 v[174:177], v193 offset:51200
	ds_read_b128 v[178:181], v238 offset:53248
	ds_read_b128 v[182:185], v193 offset:53248
	ds_read_b128 v[186:189], v238 offset:55296
	ds_read_b128 v[190:193], v193 offset:55296
	s_add_u32 s42, s42, 0x80
	s_addc_u32 s43, s43, 0
	s_mov_b32 m0, s70
	s_nop 0
	global_load_lds_dwordx4 v134, s[42:43]
	s_nop 0
	s_mov_b32 m0, s71
	s_nop 0
	global_load_lds_dwordx4 v138, s[42:43]
	s_add_u32 s42, s42, s14
	s_addc_u32 s43, s43, s15
	s_mov_b32 m0, s74
	s_nop 0
	global_load_lds_dwordx4 v134, s[42:43]
	s_nop 0
	s_mov_b32 m0, s75
	s_nop 0
	global_load_lds_dwordx4 v138, s[42:43]
	s_nop 0
	s_mov_b32 m0, s72
	s_nop 0
	global_load_lds_dwordx4 v132, s[40:41]
	s_nop 0
	s_mov_b32 m0, s73
	s_nop 0
	global_load_lds_dwordx4 v136, s[40:41]
	s_waitcnt vmcnt(8)
	s_waitcnt lgkmcnt(0)
	s_barrier
	s_setprio 1
	s_waitcnt lgkmcnt(6)
	v_mfma_scale_f32_16x16x128_f8f6f4 v[126:129], v[64:71], v[162:169], v[126:129], v243, v243 op_sel_hi:[0,0,0]
	v_mfma_scale_f32_16x16x128_f8f6f4 v[122:125], v[72:79], v[162:169], v[122:125], v243, v243 op_sel_hi:[0,0,0]
	s_waitcnt lgkmcnt(4)
	v_mfma_scale_f32_16x16x128_f8f6f4 v[118:121], v[64:71], v[170:177], v[118:121], v243, v243 op_sel_hi:[0,0,0]
	v_mfma_scale_f32_16x16x128_f8f6f4 v[114:117], v[72:79], v[170:177], v[114:117], v243, v243 op_sel_hi:[0,0,0]
	s_waitcnt lgkmcnt(2)
	v_mfma_scale_f32_16x16x128_f8f6f4 v[106:109], v[64:71], v[178:185], v[106:109], v243, v243 op_sel_hi:[0,0,0]
	v_mfma_scale_f32_16x16x128_f8f6f4 v[98:101], v[72:79], v[178:185], v[98:101], v243, v243 op_sel_hi:[0,0,0]
	s_waitcnt lgkmcnt(0)
	v_mfma_scale_f32_16x16x128_f8f6f4 v[88:91], v[64:71], v[186:193], v[198:201], v243, v243 op_sel_hi:[0,0,0]
	v_mfma_scale_f32_16x16x128_f8f6f4 v[80:83], v[72:79], v[186:193], v[202:205], v243, v243 op_sel_hi:[0,0,0]
	s_setprio 0
	s_setprio 1
	v_mfma_scale_f32_16x16x128_f8f6f4 v[110:113], v[140:147], v[162:169], v[110:113], v243, v243 op_sel_hi:[0,0,0]
	v_mfma_scale_f32_16x16x128_f8f6f4 v[102:105], v[154:161], v[162:169], v[102:105], v243, v243 op_sel_hi:[0,0,0]
	v_mfma_scale_f32_16x16x128_f8f6f4 v[92:95], v[140:147], v[170:177], v[206:209], v243, v243 op_sel_hi:[0,0,0]
	v_mfma_scale_f32_16x16x128_f8f6f4 v[84:87], v[154:161], v[170:177], v[210:213], v243, v243 op_sel_hi:[0,0,0]
	v_mfma_scale_f32_16x16x128_f8f6f4 v[76:79], v[140:147], v[178:185], v[222:225], v243, v243 op_sel_hi:[0,0,0]
	v_mfma_scale_f32_16x16x128_f8f6f4 v[72:75], v[154:161], v[178:185], v[226:229], v243, v243 op_sel_hi:[0,0,0]
	v_mfma_scale_f32_16x16x128_f8f6f4 v[68:71], v[140:147], v[186:193], v[230:233], v243, v243 op_sel_hi:[0,0,0]
	v_mfma_scale_f32_16x16x128_f8f6f4 v[64:67], v[154:161], v[186:193], v[234:237], v243, v243 op_sel_hi:[0,0,0]
	s_setprio 0
	s_barrier
	s_add_u32 s46, s46, 0x100
	s_addc_u32 s47, s47, 0
	s_add_u32 s48, s48, 0x100
	s_addc_u32 s49, s49, 0
	s_add_u32 s6, s6, 0x100
	s_addc_u32 s7, s7, 0
	s_cmp_lt_i32 s31, s68
	s_mov_b32 s35, s31
	s_cbranch_scc1 .LBB0_1572
	s_mov_b32 s6, 0x3e800000
	v_readlane_b32 s46, v254, 34
	v_pk_mul_f32 v[150:151], v[128:129], s[6:7] op_sel_hi:[1,0]
	v_pk_mul_f32 v[148:149], v[126:127], s[6:7] op_sel_hi:[1,0]
	v_pk_mul_f32 v[146:147], v[124:125], s[6:7] op_sel_hi:[1,0]
	v_pk_mul_f32 v[144:145], v[122:123], s[6:7] op_sel_hi:[1,0]
	v_pk_mul_f32 v[142:143], v[112:113], s[6:7] op_sel_hi:[1,0]
	v_pk_mul_f32 v[140:141], v[110:111], s[6:7] op_sel_hi:[1,0]
	v_pk_mul_f32 v[128:129], v[104:105], s[6:7] op_sel_hi:[1,0]
	v_pk_mul_f32 v[126:127], v[102:103], s[6:7] op_sel_hi:[1,0]
	v_pk_mul_f32 v[124:125], v[120:121], s[6:7] op_sel_hi:[1,0]
	v_pk_mul_f32 v[122:123], v[118:119], s[6:7] op_sel_hi:[1,0]
	v_pk_mul_f32 v[120:121], v[116:117], s[6:7] op_sel_hi:[1,0]
	v_pk_mul_f32 v[118:119], v[114:115], s[6:7] op_sel_hi:[1,0]
	v_pk_mul_f32 v[116:117], v[94:95], s[6:7] op_sel_hi:[1,0]
	v_pk_mul_f32 v[114:115], v[92:93], s[6:7] op_sel_hi:[1,0]
	v_pk_mul_f32 v[112:113], v[86:87], s[6:7] op_sel_hi:[1,0]
	v_pk_mul_f32 v[110:111], v[84:85], s[6:7] op_sel_hi:[1,0]
	v_pk_mul_f32 v[104:105], v[108:109], s[6:7] op_sel_hi:[1,0]
	v_pk_mul_f32 v[102:103], v[106:107], s[6:7] op_sel_hi:[1,0]
	v_pk_mul_f32 v[100:101], v[100:101], s[6:7] op_sel_hi:[1,0]
	v_pk_mul_f32 v[98:99], v[98:99], s[6:7] op_sel_hi:[1,0]
	v_pk_mul_f32 v[94:95], v[78:79], s[6:7] op_sel_hi:[1,0]
	v_pk_mul_f32 v[92:93], v[76:77], s[6:7] op_sel_hi:[1,0]
	v_pk_mul_f32 v[86:87], v[74:75], s[6:7] op_sel_hi:[1,0]
	v_pk_mul_f32 v[84:85], v[72:73], s[6:7] op_sel_hi:[1,0]
	v_pk_mul_f32 v[78:79], v[90:91], s[6:7] op_sel_hi:[1,0]
	v_pk_mul_f32 v[76:77], v[88:89], s[6:7] op_sel_hi:[1,0]
	v_pk_mul_f32 v[74:75], v[82:83], s[6:7] op_sel_hi:[1,0]
	v_pk_mul_f32 v[72:73], v[80:81], s[6:7] op_sel_hi:[1,0]
	v_pk_mul_f32 v[70:71], v[70:71], s[6:7] op_sel_hi:[1,0]
	v_pk_mul_f32 v[68:69], v[68:69], s[6:7] op_sel_hi:[1,0]
	v_pk_mul_f32 v[66:67], v[66:67], s[6:7] op_sel_hi:[1,0]
	v_pk_mul_f32 v[64:65], v[64:65], s[6:7] op_sel_hi:[1,0]
	v_readlane_b32 s47, v254, 35
	v_readlane_b32 s44, v254, 38
	v_mov_b32_e32 v224, v244
	v_mov_b32_e32 v226, v245
	v_mov_b32_e32 v227, v246
	v_mov_b64_e32 v[230:231], v[248:249]
	v_mov_b64_e32 v[232:233], v[250:251]
	v_mov_b32_e32 v229, v247
